# GEMM K-loops: load segment at s_setprio 2 above the partner MFMA block (was 0)
# baseline (speedup 1.0000x reference)
.LBB0_216:
	v_add_u32_e32 v130, s88, v196
	v_add_u32_e32 v134, s89, v196
	ds_read_b128 v[158:161], v130
	ds_read_b128 v[150:153], v130 offset:1024
	ds_read_b128 v[154:157], v130 offset:2048
	ds_read_b128 v[146:149], v130 offset:3072
	ds_read_b128 v[142:145], v134
	ds_read_b128 v[130:133], v134 offset:1024
	ds_read_b128 v[138:141], v134 offset:2048
	ds_read_b128 v[134:137], v134 offset:3072
	s_add_u32 s25, s50, 0xfff80080
	s_addc_u32 s56, s51, -1
	s_and_b64 s[18:19], s[18:19], exec
	s_cselect_b32 s59, s31, s56
	s_cselect_b32 s58, s4, s25
	s_cselect_b32 s57, s5, s64
	s_cselect_b32 s56, s29, s92
	v_lshl_add_u64 v[224:225], s[50:51], 0, v[170:171]
	s_add_i32 m0, s39, 0xc000
	ds_read_b128 v[186:189], v198
	ds_read_b128 v[190:193], v198 offset:1024
	ds_read_b128 v[200:203], v198 offset:2048
	ds_read_b128 v[204:207], v198 offset:3072
	ds_read_b128 v[208:211], v198 offset:4096
	ds_read_b128 v[212:215], v198 offset:5120
	ds_read_b128 v[216:219], v198 offset:6144
	ds_read_b128 v[220:223], v198 offset:7168
	global_load_lds_dwordx4 v[224:225], off
	v_lshl_add_u64 v[224:225], s[50:51], 0, v[172:173]
	s_add_i32 m0, s39, 0xe000
	s_nop 0
	global_load_lds_dwordx4 v[224:225], off
	s_waitcnt vmcnt(8)
	s_waitcnt lgkmcnt(0)
	s_barrier
	s_setprio 1
	s_waitcnt lgkmcnt(0)
	v_mfma_i32_16x16x64_i8 v[126:129], v[158:161], v[186:189], v[126:129]
	v_mfma_i32_16x16x64_i8 v[122:125], v[154:157], v[186:189], v[122:125]
	v_mfma_i32_16x16x64_i8 v[110:113], v[158:161], v[200:203], v[110:113]
	v_mfma_i32_16x16x64_i8 v[106:109], v[154:157], v[200:203], v[106:109]
	v_mfma_i32_16x16x64_i8 v[94:97], v[158:161], v[208:211], v[94:97]
	v_mfma_i32_16x16x64_i8 v[90:93], v[154:157], v[208:211], v[90:93]
	v_mfma_i32_16x16x64_i8 v[78:81], v[158:161], v[216:219], v[78:81]
	v_mfma_i32_16x16x64_i8 v[74:77], v[154:157], v[216:219], v[74:77]
	s_nop 0
	v_mfma_i32_16x16x64_i8 v[126:129], v[150:153], v[190:193], v[126:129]
	v_mfma_i32_16x16x64_i8 v[122:125], v[146:149], v[190:193], v[122:125]
	v_mfma_i32_16x16x64_i8 v[110:113], v[150:153], v[204:207], v[110:113]
	v_mfma_i32_16x16x64_i8 v[106:109], v[146:149], v[204:207], v[106:109]
	v_mfma_i32_16x16x64_i8 v[94:97], v[150:153], v[212:215], v[94:97]
	v_mfma_i32_16x16x64_i8 v[90:93], v[146:149], v[212:215], v[90:93]
	v_mfma_i32_16x16x64_i8 v[78:81], v[150:153], v[220:223], v[78:81]
	v_mfma_i32_16x16x64_i8 v[74:77], v[146:149], v[220:223], v[74:77]
	s_setprio 0
	s_setprio 1
	v_mfma_i32_16x16x64_i8 v[118:121], v[142:145], v[186:189], v[118:121]
	v_mfma_i32_16x16x64_i8 v[114:117], v[138:141], v[186:189], v[114:117]
	v_mfma_i32_16x16x64_i8 v[102:105], v[142:145], v[200:203], v[102:105]
	v_mfma_i32_16x16x64_i8 v[98:101], v[138:141], v[200:203], v[98:101]
	v_mfma_i32_16x16x64_i8 v[86:89], v[142:145], v[208:211], v[86:89]
	v_mfma_i32_16x16x64_i8 v[82:85], v[138:141], v[208:211], v[82:85]
	v_mfma_i32_16x16x64_i8 v[70:73], v[142:145], v[216:219], v[70:73]
	v_mfma_i32_16x16x64_i8 v[66:69], v[138:141], v[216:219], v[66:69]
	s_nop 0
	v_mfma_i32_16x16x64_i8 v[118:121], v[130:133], v[190:193], v[118:121]
	v_mfma_i32_16x16x64_i8 v[114:117], v[134:137], v[190:193], v[114:117]
	v_mfma_i32_16x16x64_i8 v[102:105], v[130:133], v[204:207], v[102:105]
	v_mfma_i32_16x16x64_i8 v[98:101], v[134:137], v[204:207], v[98:101]
	v_mfma_i32_16x16x64_i8 v[86:89], v[130:133], v[212:215], v[86:89]
	v_mfma_i32_16x16x64_i8 v[82:85], v[134:137], v[212:215], v[82:85]
	v_mfma_i32_16x16x64_i8 v[70:73], v[130:133], v[220:223], v[70:73]
	v_mfma_i32_16x16x64_i8 v[66:69], v[134:137], v[220:223], v[66:69]
	s_setprio 2
	s_barrier
	s_add_i32 s18, s88, s7
	v_lshl_add_u64 v[186:187], s[56:57], 0, v[164:165]
	s_mov_b32 m0, s18
	ds_read_b128 v[200:203], v198 offset:16384
	ds_read_b128 v[204:207], v198 offset:17408
	ds_read_b128 v[208:211], v198 offset:18432
	ds_read_b128 v[212:215], v198 offset:19456
	ds_read_b128 v[216:219], v198 offset:20480
	ds_read_b128 v[220:223], v198 offset:21504
	ds_read_b128 v[224:227], v198 offset:22528
	ds_read_b128 v[228:231], v198 offset:23552
	global_load_lds_dwordx4 v[186:187], off
	s_add_i32 m0, s18, 0x2000
	s_add_u32 s18, s56, 0x80000
	v_lshl_add_u64 v[188:189], s[56:57], 0, v[168:169]
	s_addc_u32 s19, s57, 0
	s_add_i32 s25, s89, s7
	global_load_lds_dwordx4 v[188:189], off
	v_lshl_add_u64 v[190:191], s[18:19], 0, v[164:165]
	s_mov_b32 m0, s25
	v_lshl_add_u64 v[192:193], s[58:59], 0, v[166:167]
	global_load_lds_dwordx4 v[190:191], off
	v_lshl_add_u64 v[190:191], s[18:19], 0, v[168:169]
	s_add_i32 m0, s25, 0x2000
	s_nop 0
	global_load_lds_dwordx4 v[190:191], off
	v_lshl_add_u64 v[190:191], s[58:59], 0, v[162:163]
	s_mov_b32 m0, s39
	s_nop 0
	global_load_lds_dwordx4 v[190:191], off
	s_mov_b32 m0, s43
	s_nop 0
	global_load_lds_dwordx4 v[192:193], off
	s_waitcnt vmcnt(8)
	s_waitcnt lgkmcnt(0)
	s_barrier
	s_setprio 1
	s_waitcnt lgkmcnt(0)
	v_mfma_i32_16x16x64_i8 v[62:65], v[158:161], v[200:203], v[62:65]
	v_mfma_i32_16x16x64_i8 v[58:61], v[154:157], v[200:203], v[58:61]
	v_mfma_i32_16x16x64_i8 v[46:49], v[158:161], v[208:211], v[46:49]
	v_mfma_i32_16x16x64_i8 v[42:45], v[154:157], v[208:211], v[42:45]
	v_mfma_i32_16x16x64_i8 v[30:33], v[158:161], v[216:219], v[30:33]
	v_mfma_i32_16x16x64_i8 v[26:29], v[154:157], v[216:219], v[26:29]
	v_mfma_i32_16x16x64_i8 v[14:17], v[158:161], v[224:227], v[14:17]
	v_mfma_i32_16x16x64_i8 v[10:13], v[154:157], v[224:227], v[10:13]
	s_nop 0
	v_mfma_i32_16x16x64_i8 v[62:65], v[150:153], v[204:207], v[62:65]
	v_mfma_i32_16x16x64_i8 v[58:61], v[146:149], v[204:207], v[58:61]
	v_mfma_i32_16x16x64_i8 v[46:49], v[150:153], v[212:215], v[46:49]
	v_mfma_i32_16x16x64_i8 v[42:45], v[146:149], v[212:215], v[42:45]
	v_mfma_i32_16x16x64_i8 v[30:33], v[150:153], v[220:223], v[30:33]
	v_mfma_i32_16x16x64_i8 v[26:29], v[146:149], v[220:223], v[26:29]
	v_mfma_i32_16x16x64_i8 v[14:17], v[150:153], v[228:231], v[14:17]
	v_mfma_i32_16x16x64_i8 v[10:13], v[146:149], v[228:231], v[10:13]
	s_setprio 0
	s_setprio 1
	v_mfma_i32_16x16x64_i8 v[54:57], v[142:145], v[200:203], v[54:57]
	v_mfma_i32_16x16x64_i8 v[50:53], v[138:141], v[200:203], v[50:53]
	v_mfma_i32_16x16x64_i8 v[38:41], v[142:145], v[208:211], v[38:41]
	v_mfma_i32_16x16x64_i8 v[34:37], v[138:141], v[208:211], v[34:37]
	v_mfma_i32_16x16x64_i8 v[22:25], v[142:145], v[216:219], v[22:25]
	v_mfma_i32_16x16x64_i8 v[18:21], v[138:141], v[216:219], v[18:21]
	v_mfma_i32_16x16x64_i8 v[6:9], v[142:145], v[224:227], v[6:9]
	v_mfma_i32_16x16x64_i8 v[2:5], v[138:141], v[224:227], v[2:5]
	s_nop 0
	v_mfma_i32_16x16x64_i8 v[54:57], v[130:133], v[204:207], v[54:57]
	v_mfma_i32_16x16x64_i8 v[50:53], v[134:137], v[204:207], v[50:53]
	v_mfma_i32_16x16x64_i8 v[38:41], v[130:133], v[212:215], v[38:41]
	v_mfma_i32_16x16x64_i8 v[34:37], v[134:137], v[212:215], v[34:37]
	v_mfma_i32_16x16x64_i8 v[22:25], v[130:133], v[220:223], v[22:25]
	v_mfma_i32_16x16x64_i8 v[18:21], v[134:137], v[220:223], v[18:21]
	v_mfma_i32_16x16x64_i8 v[6:9], v[130:133], v[228:231], v[6:9]
	v_mfma_i32_16x16x64_i8 v[2:5], v[134:137], v[228:231], v[2:5]
	s_setprio 2
	s_barrier
	s_add_i32 s25, 0, 0x18000
	s_add_i32 vcc_lo, 0, 0x1c000
	v_add_u32_e32 v142, s25, v196
	v_add_u32_e32 v158, vcc_lo, v196
	ds_read_b128 v[130:133], v142
	ds_read_b128 v[134:137], v142 offset:1024
	ds_read_b128 v[138:141], v142 offset:2048
	ds_read_b128 v[142:145], v142 offset:3072
	ds_read_b128 v[146:149], v158
	ds_read_b128 v[150:153], v158 offset:1024
	ds_read_b128 v[154:157], v158 offset:2048
	ds_read_b128 v[158:161], v158 offset:3072
	s_add_u32 s18, s58, 0x80000
	s_addc_u32 s19, s59, 0
	s_mov_b32 m0, s61
	v_lshl_add_u64 v[232:233], s[18:19], 0, v[162:163]
	ds_read_b128 v[200:203], v198 offset:32768
	ds_read_b128 v[204:207], v198 offset:33792
	ds_read_b128 v[208:211], v198 offset:34816
	ds_read_b128 v[212:215], v198 offset:35840
	ds_read_b128 v[216:219], v198 offset:36864
	ds_read_b128 v[220:223], v198 offset:37888
	ds_read_b128 v[224:227], v198 offset:38912
	ds_read_b128 v[228:231], v198 offset:39936
	global_load_lds_dwordx4 v[232:233], off
	v_lshl_add_u64 v[232:233], s[18:19], 0, v[166:167]
	s_mov_b32 m0, s62
	s_nop 0
	global_load_lds_dwordx4 v[232:233], off
	s_waitcnt vmcnt(8)
	s_waitcnt lgkmcnt(0)
	s_barrier
	s_setprio 1
	s_waitcnt lgkmcnt(0)
	v_mfma_i32_16x16x64_i8 v[126:129], v[130:133], v[200:203], v[126:129]
	v_mfma_i32_16x16x64_i8 v[122:125], v[138:141], v[200:203], v[122:125]
	v_mfma_i32_16x16x64_i8 v[110:113], v[130:133], v[208:211], v[110:113]
	v_mfma_i32_16x16x64_i8 v[106:109], v[138:141], v[208:211], v[106:109]
	v_mfma_i32_16x16x64_i8 v[94:97], v[130:133], v[216:219], v[94:97]
	v_mfma_i32_16x16x64_i8 v[90:93], v[138:141], v[216:219], v[90:93]
	v_mfma_i32_16x16x64_i8 v[78:81], v[130:133], v[224:227], v[78:81]
	v_mfma_i32_16x16x64_i8 v[74:77], v[138:141], v[224:227], v[74:77]
	s_nop 0
	v_mfma_i32_16x16x64_i8 v[126:129], v[134:137], v[204:207], v[126:129]
	v_mfma_i32_16x16x64_i8 v[122:125], v[142:145], v[204:207], v[122:125]
	v_mfma_i32_16x16x64_i8 v[110:113], v[134:137], v[212:215], v[110:113]
	v_mfma_i32_16x16x64_i8 v[106:109], v[142:145], v[212:215], v[106:109]
	v_mfma_i32_16x16x64_i8 v[94:97], v[134:137], v[220:223], v[94:97]
	v_mfma_i32_16x16x64_i8 v[90:93], v[142:145], v[220:223], v[90:93]
	v_mfma_i32_16x16x64_i8 v[78:81], v[134:137], v[228:231], v[78:81]
	v_mfma_i32_16x16x64_i8 v[74:77], v[142:145], v[228:231], v[74:77]
	s_setprio 0
	s_setprio 1
	v_mfma_i32_16x16x64_i8 v[118:121], v[146:149], v[200:203], v[118:121]
	v_mfma_i32_16x16x64_i8 v[114:117], v[154:157], v[200:203], v[114:117]
	v_mfma_i32_16x16x64_i8 v[102:105], v[146:149], v[208:211], v[102:105]
	v_mfma_i32_16x16x64_i8 v[98:101], v[154:157], v[208:211], v[98:101]
	v_mfma_i32_16x16x64_i8 v[86:89], v[146:149], v[216:219], v[86:89]
	v_mfma_i32_16x16x64_i8 v[82:85], v[154:157], v[216:219], v[82:85]
	v_mfma_i32_16x16x64_i8 v[70:73], v[146:149], v[224:227], v[70:73]
	v_mfma_i32_16x16x64_i8 v[66:69], v[154:157], v[224:227], v[66:69]
	s_nop 0
	v_mfma_i32_16x16x64_i8 v[118:121], v[150:153], v[204:207], v[118:121]
	v_mfma_i32_16x16x64_i8 v[114:117], v[158:161], v[204:207], v[114:117]
	v_mfma_i32_16x16x64_i8 v[102:105], v[150:153], v[212:215], v[102:105]
	v_mfma_i32_16x16x64_i8 v[98:101], v[158:161], v[212:215], v[98:101]
	v_mfma_i32_16x16x64_i8 v[86:89], v[150:153], v[220:223], v[86:89]
	v_mfma_i32_16x16x64_i8 v[82:85], v[158:161], v[220:223], v[82:85]
	v_mfma_i32_16x16x64_i8 v[70:73], v[150:153], v[228:231], v[70:73]
	v_mfma_i32_16x16x64_i8 v[66:69], v[158:161], v[228:231], v[66:69]
	s_setprio 2
	s_barrier
	s_add_i32 s18, s25, s7
	v_lshl_add_u64 v[186:187], v[186:187], 0, s[14:15]
	s_mov_b32 m0, s18
	ds_read_b128 v[200:203], v198 offset:49152
	ds_read_b128 v[204:207], v198 offset:50176
	ds_read_b128 v[208:211], v198 offset:51200
	ds_read_b128 v[212:215], v198 offset:52224
	ds_read_b128 v[216:219], v198 offset:53248
	ds_read_b128 v[220:223], v198 offset:54272
	ds_read_b128 v[224:227], v198 offset:55296
	ds_read_b128 v[228:231], v198 offset:56320
	global_load_lds_dwordx4 v[186:187], off
	s_add_i32 m0, s18, 0x2000
	s_add_u32 s18, s56, 0x80080
	v_lshl_add_u64 v[186:187], v[188:189], 0, s[14:15]
	s_addc_u32 s19, s57, 0
	s_add_i32 s25, vcc_lo, s7
	global_load_lds_dwordx4 v[186:187], off
	v_lshl_add_u64 v[186:187], s[18:19], 0, v[164:165]
	s_mov_b32 m0, s25
	s_nop 0
	global_load_lds_dwordx4 v[186:187], off
	v_lshl_add_u64 v[186:187], s[18:19], 0, v[168:169]
	s_add_i32 m0, s25, 0x2000
	s_nop 0
	global_load_lds_dwordx4 v[186:187], off
	v_lshl_add_u64 v[186:187], v[190:191], 0, s[14:15]
	s_mov_b32 m0, s67
	s_nop 0
	global_load_lds_dwordx4 v[186:187], off
	v_lshl_add_u64 v[186:187], v[192:193], 0, s[14:15]
	s_mov_b32 m0, s68
	s_nop 0
	global_load_lds_dwordx4 v[186:187], off
	s_waitcnt vmcnt(8)
	s_waitcnt lgkmcnt(0)
	s_barrier
	s_setprio 1
	s_waitcnt lgkmcnt(0)
	v_mfma_i32_16x16x64_i8 v[62:65], v[130:133], v[200:203], v[62:65]
	v_mfma_i32_16x16x64_i8 v[58:61], v[138:141], v[200:203], v[58:61]
	v_mfma_i32_16x16x64_i8 v[46:49], v[130:133], v[208:211], v[46:49]
	v_mfma_i32_16x16x64_i8 v[42:45], v[138:141], v[208:211], v[42:45]
	v_mfma_i32_16x16x64_i8 v[30:33], v[130:133], v[216:219], v[30:33]
	v_mfma_i32_16x16x64_i8 v[26:29], v[138:141], v[216:219], v[26:29]
	v_mfma_i32_16x16x64_i8 v[14:17], v[130:133], v[224:227], v[14:17]
	v_mfma_i32_16x16x64_i8 v[10:13], v[138:141], v[224:227], v[10:13]
	s_nop 0
	v_mfma_i32_16x16x64_i8 v[62:65], v[134:137], v[204:207], v[62:65]
	v_mfma_i32_16x16x64_i8 v[58:61], v[142:145], v[204:207], v[58:61]
	v_mfma_i32_16x16x64_i8 v[46:49], v[134:137], v[212:215], v[46:49]
	v_mfma_i32_16x16x64_i8 v[42:45], v[142:145], v[212:215], v[42:45]
	v_mfma_i32_16x16x64_i8 v[30:33], v[134:137], v[220:223], v[30:33]
	v_mfma_i32_16x16x64_i8 v[26:29], v[142:145], v[220:223], v[26:29]
	v_mfma_i32_16x16x64_i8 v[14:17], v[134:137], v[228:231], v[14:17]
	v_mfma_i32_16x16x64_i8 v[10:13], v[142:145], v[228:231], v[10:13]
	s_setprio 0
	s_setprio 1
	v_mfma_i32_16x16x64_i8 v[54:57], v[146:149], v[200:203], v[54:57]
	v_mfma_i32_16x16x64_i8 v[50:53], v[154:157], v[200:203], v[50:53]
	v_mfma_i32_16x16x64_i8 v[38:41], v[146:149], v[208:211], v[38:41]
	v_mfma_i32_16x16x64_i8 v[34:37], v[154:157], v[208:211], v[34:37]
	v_mfma_i32_16x16x64_i8 v[22:25], v[146:149], v[216:219], v[22:25]
	v_mfma_i32_16x16x64_i8 v[18:21], v[154:157], v[216:219], v[18:21]
	v_mfma_i32_16x16x64_i8 v[6:9], v[146:149], v[224:227], v[6:9]
	v_mfma_i32_16x16x64_i8 v[2:5], v[154:157], v[224:227], v[2:5]
	s_nop 0
	v_mfma_i32_16x16x64_i8 v[54:57], v[150:153], v[204:207], v[54:57]
	v_mfma_i32_16x16x64_i8 v[50:53], v[158:161], v[204:207], v[50:53]
	v_mfma_i32_16x16x64_i8 v[38:41], v[150:153], v[212:215], v[38:41]
	v_mfma_i32_16x16x64_i8 v[34:37], v[158:161], v[212:215], v[34:37]
	v_mfma_i32_16x16x64_i8 v[22:25], v[150:153], v[220:223], v[22:25]
	v_mfma_i32_16x16x64_i8 v[18:21], v[158:161], v[220:223], v[18:21]
	v_mfma_i32_16x16x64_i8 v[6:9], v[150:153], v[228:231], v[6:9]
	v_mfma_i32_16x16x64_i8 v[2:5], v[158:161], v[228:231], v[2:5]
	s_setprio 2
	s_barrier
	s_add_i32 s65, s65, 2
	s_add_u32 s50, s50, 0x100
	s_addc_u32 s51, s51, 0
	s_add_u32 s92, s92, 0x100
	s_addc_u32 s64, s64, 0
	s_cmp_gt_u32 s65, 29
	s_cbranch_scc1 .LBB0_219

.LBB0_332:
	s_add_u32 s6, s61, s4
	s_addc_u32 s7, s62, s5
	s_add_u32 s6, s6, 0x32800100
	s_addc_u32 s7, s7, 0
	s_add_u32 s24, s63, s4
	s_addc_u32 s25, s68, s5
	s_add_i32 s64, 0, 0x10000
	s_cmpk_eq_i32 s4, 0x2a00
	s_cselect_b32 s13, s1, s7
	s_cselect_b32 s12, s0, s6
	s_cselect_b32 s7, s29, s25
	s_cselect_b32 s6, s28, s24
	s_add_i32 s65, 0, 0x14000
	v_add_u32_e32 v2, s64, v188
	v_add_u32_e32 v6, s65, v188
	ds_read_b128 v[26:29], v2
	ds_read_b128 v[30:33], v2 offset:1024
	ds_read_b128 v[18:21], v2 offset:2048
	ds_read_b128 v[22:25], v2 offset:3072
	ds_read_b128 v[10:13], v6
	ds_read_b128 v[14:17], v6 offset:1024
	ds_read_b128 v[2:5], v6 offset:2048
	ds_read_b128 v[6:9], v6 offset:3072
	v_lshl_add_u64 v[214:215], v[168:169], 0, s[4:5]
	s_add_i32 m0, s18, 0xc000
	ds_read_b128 v[172:175], v189
	ds_read_b128 v[176:179], v189 offset:1024
	ds_read_b128 v[190:193], v189 offset:2048
	ds_read_b128 v[194:197], v189 offset:3072
	ds_read_b128 v[198:201], v189 offset:4096
	ds_read_b128 v[202:205], v189 offset:5120
	ds_read_b128 v[206:209], v189 offset:6144
	ds_read_b128 v[210:213], v189 offset:7168
	global_load_lds_dwordx4 v[214:215], off
	v_lshl_add_u64 v[214:215], v[170:171], 0, s[4:5]
	s_add_i32 m0, s18, 0xe000
	s_nop 0
	global_load_lds_dwordx4 v[214:215], off
	s_waitcnt vmcnt(8)
	s_waitcnt lgkmcnt(0)
	s_barrier
	s_setprio 1
	s_waitcnt lgkmcnt(0)
	v_mfma_scale_f32_16x16x128_f8f6f4 v[70:73], v[26:33], v[172:179], v[70:73], v187, v187 op_sel_hi:[0,0,0]
	v_mfma_scale_f32_16x16x128_f8f6f4 v[66:69], v[18:25], v[172:179], v[66:69], v187, v187 op_sel_hi:[0,0,0]
	v_mfma_scale_f32_16x16x128_f8f6f4 v[78:81], v[26:33], v[190:197], v[78:81], v187, v187 op_sel_hi:[0,0,0]
	v_mfma_scale_f32_16x16x128_f8f6f4 v[74:77], v[18:25], v[190:197], v[74:77], v187, v187 op_sel_hi:[0,0,0]
	v_mfma_scale_f32_16x16x128_f8f6f4 v[86:89], v[26:33], v[198:205], v[86:89], v187, v187 op_sel_hi:[0,0,0]
	v_mfma_scale_f32_16x16x128_f8f6f4 v[82:85], v[18:25], v[198:205], v[82:85], v187, v187 op_sel_hi:[0,0,0]
	v_mfma_scale_f32_16x16x128_f8f6f4 v[94:97], v[26:33], v[206:213], v[94:97], v187, v187 op_sel_hi:[0,0,0]
	v_mfma_scale_f32_16x16x128_f8f6f4 v[90:93], v[18:25], v[206:213], v[90:93], v187, v187 op_sel_hi:[0,0,0]
	s_setprio 0
	s_setprio 1
	v_mfma_scale_f32_16x16x128_f8f6f4 v[158:161], v[10:17], v[172:179], v[158:161], v187, v187 op_sel_hi:[0,0,0]
	v_mfma_scale_f32_16x16x128_f8f6f4 v[154:157], v[2:9], v[172:179], v[154:157], v187, v187 op_sel_hi:[0,0,0]
	v_mfma_scale_f32_16x16x128_f8f6f4 v[150:153], v[10:17], v[190:197], v[150:153], v187, v187 op_sel_hi:[0,0,0]
	v_mfma_scale_f32_16x16x128_f8f6f4 v[146:149], v[2:9], v[190:197], v[146:149], v187, v187 op_sel_hi:[0,0,0]
	v_mfma_scale_f32_16x16x128_f8f6f4 v[142:145], v[10:17], v[198:205], v[142:145], v187, v187 op_sel_hi:[0,0,0]
	v_mfma_scale_f32_16x16x128_f8f6f4 v[138:141], v[2:9], v[198:205], v[138:141], v187, v187 op_sel_hi:[0,0,0]
	v_mfma_scale_f32_16x16x128_f8f6f4 v[134:137], v[10:17], v[206:213], v[134:137], v187, v187 op_sel_hi:[0,0,0]
	v_mfma_scale_f32_16x16x128_f8f6f4 v[130:133], v[2:9], v[206:213], v[130:133], v187, v187 op_sel_hi:[0,0,0]
	s_setprio 2
	s_barrier
	s_add_i32 s24, s64, s17
	v_lshl_add_u64 v[172:173], s[6:7], 0, v[162:163]
	s_mov_b32 m0, s24
	ds_read_b128 v[190:193], v189 offset:16384
	ds_read_b128 v[194:197], v189 offset:17408
	ds_read_b128 v[198:201], v189 offset:18432
	ds_read_b128 v[202:205], v189 offset:19456
	ds_read_b128 v[206:209], v189 offset:20480
	ds_read_b128 v[210:213], v189 offset:21504
	ds_read_b128 v[214:217], v189 offset:22528
	ds_read_b128 v[218:221], v189 offset:23552
	global_load_lds_dwordx4 v[172:173], off
	s_add_i32 m0, s24, 0x2000
	s_add_u32 s24, s6, 0x158000
	v_lshl_add_u64 v[174:175], s[6:7], 0, v[166:167]
	s_addc_u32 s25, s7, 0
	s_add_i32 s64, s65, s17
	global_load_lds_dwordx4 v[174:175], off
	v_lshl_add_u64 v[176:177], s[24:25], 0, v[162:163]
	s_mov_b32 m0, s64
	v_lshl_add_u64 v[178:179], s[12:13], 0, v[166:167]
	global_load_lds_dwordx4 v[176:177], off
	v_lshl_add_u64 v[176:177], s[24:25], 0, v[166:167]
	s_add_i32 m0, s64, 0x2000
	s_nop 0
	global_load_lds_dwordx4 v[176:177], off
	v_lshl_add_u64 v[176:177], s[12:13], 0, v[162:163]
	s_mov_b32 m0, s18
	s_nop 0
	global_load_lds_dwordx4 v[176:177], off
	s_mov_b32 m0, s19
	s_nop 0
	global_load_lds_dwordx4 v[178:179], off
	s_waitcnt vmcnt(8)
	s_waitcnt lgkmcnt(0)
	s_barrier
	s_setprio 1
	s_waitcnt lgkmcnt(0)
	v_mfma_scale_f32_16x16x128_f8f6f4 v[102:105], v[26:33], v[190:197], v[102:105], v187, v187 op_sel_hi:[0,0,0]
	v_mfma_scale_f32_16x16x128_f8f6f4 v[98:101], v[18:25], v[190:197], v[98:101], v187, v187 op_sel_hi:[0,0,0]
	v_mfma_scale_f32_16x16x128_f8f6f4 v[110:113], v[26:33], v[198:205], v[110:113], v187, v187 op_sel_hi:[0,0,0]
	v_mfma_scale_f32_16x16x128_f8f6f4 v[106:109], v[18:25], v[198:205], v[106:109], v187, v187 op_sel_hi:[0,0,0]
	v_mfma_scale_f32_16x16x128_f8f6f4 v[118:121], v[26:33], v[206:213], v[118:121], v187, v187 op_sel_hi:[0,0,0]
	v_mfma_scale_f32_16x16x128_f8f6f4 v[114:117], v[18:25], v[206:213], v[114:117], v187, v187 op_sel_hi:[0,0,0]
	v_mfma_scale_f32_16x16x128_f8f6f4 v[126:129], v[26:33], v[214:221], v[126:129], v187, v187 op_sel_hi:[0,0,0]
	v_mfma_scale_f32_16x16x128_f8f6f4 v[122:125], v[18:25], v[214:221], v[122:125], v187, v187 op_sel_hi:[0,0,0]
	s_setprio 0
	s_setprio 1
	v_mfma_scale_f32_16x16x128_f8f6f4 v[38:41], v[10:17], v[190:197], v[38:41], v187, v187 op_sel_hi:[0,0,0]
	v_mfma_scale_f32_16x16x128_f8f6f4 v[34:37], v[2:9], v[190:197], v[34:37], v187, v187 op_sel_hi:[0,0,0]
	v_mfma_scale_f32_16x16x128_f8f6f4 v[46:49], v[10:17], v[198:205], v[46:49], v187, v187 op_sel_hi:[0,0,0]
	v_mfma_scale_f32_16x16x128_f8f6f4 v[42:45], v[2:9], v[198:205], v[42:45], v187, v187 op_sel_hi:[0,0,0]
	v_mfma_scale_f32_16x16x128_f8f6f4 v[54:57], v[10:17], v[206:213], v[54:57], v187, v187 op_sel_hi:[0,0,0]
	v_mfma_scale_f32_16x16x128_f8f6f4 v[50:53], v[2:9], v[206:213], v[50:53], v187, v187 op_sel_hi:[0,0,0]
	v_mfma_scale_f32_16x16x128_f8f6f4 v[62:65], v[10:17], v[214:221], v[62:65], v187, v187 op_sel_hi:[0,0,0]
	v_mfma_scale_f32_16x16x128_f8f6f4 v[58:61], v[2:9], v[214:221], v[58:61], v187, v187 op_sel_hi:[0,0,0]
	s_setprio 2
	s_barrier
	s_add_i32 s24, 0, 0x18000
	s_add_i32 s25, 0, 0x1c000
	v_add_u32_e32 v14, s24, v188
	v_add_u32_e32 v30, s25, v188
	ds_read_b128 v[2:5], v14
	ds_read_b128 v[6:9], v14 offset:1024
	ds_read_b128 v[10:13], v14 offset:2048
	ds_read_b128 v[14:17], v14 offset:3072
	ds_read_b128 v[18:21], v30
	ds_read_b128 v[22:25], v30 offset:1024
	ds_read_b128 v[26:29], v30 offset:2048
	ds_read_b128 v[30:33], v30 offset:3072
	s_add_u32 s12, s12, 0x158000
	s_addc_u32 s13, s13, 0
	s_mov_b32 m0, s93
	v_lshl_add_u64 v[222:223], s[12:13], 0, v[162:163]
	ds_read_b128 v[190:193], v189 offset:32768
	ds_read_b128 v[194:197], v189 offset:33792
	ds_read_b128 v[198:201], v189 offset:34816
	ds_read_b128 v[202:205], v189 offset:35840
	ds_read_b128 v[206:209], v189 offset:36864
	ds_read_b128 v[210:213], v189 offset:37888
	ds_read_b128 v[214:217], v189 offset:38912
	ds_read_b128 v[218:221], v189 offset:39936
	global_load_lds_dwordx4 v[222:223], off
	v_lshl_add_u64 v[222:223], s[12:13], 0, v[166:167]
	s_mov_b32 m0, s94
	s_nop 0
	global_load_lds_dwordx4 v[222:223], off
	s_waitcnt vmcnt(8)
	s_waitcnt lgkmcnt(0)
	s_barrier
	s_setprio 1
	s_waitcnt lgkmcnt(0)
	v_mfma_scale_f32_16x16x128_f8f6f4 v[70:73], v[2:9], v[190:197], v[70:73], v187, v187 op_sel_hi:[0,0,0]
	v_mfma_scale_f32_16x16x128_f8f6f4 v[66:69], v[10:17], v[190:197], v[66:69], v187, v187 op_sel_hi:[0,0,0]
	v_mfma_scale_f32_16x16x128_f8f6f4 v[78:81], v[2:9], v[198:205], v[78:81], v187, v187 op_sel_hi:[0,0,0]
	v_mfma_scale_f32_16x16x128_f8f6f4 v[74:77], v[10:17], v[198:205], v[74:77], v187, v187 op_sel_hi:[0,0,0]
	v_mfma_scale_f32_16x16x128_f8f6f4 v[86:89], v[2:9], v[206:213], v[86:89], v187, v187 op_sel_hi:[0,0,0]
	v_mfma_scale_f32_16x16x128_f8f6f4 v[82:85], v[10:17], v[206:213], v[82:85], v187, v187 op_sel_hi:[0,0,0]
	v_mfma_scale_f32_16x16x128_f8f6f4 v[94:97], v[2:9], v[214:221], v[94:97], v187, v187 op_sel_hi:[0,0,0]
	v_mfma_scale_f32_16x16x128_f8f6f4 v[90:93], v[10:17], v[214:221], v[90:93], v187, v187 op_sel_hi:[0,0,0]
	s_setprio 0
	s_setprio 1
	v_mfma_scale_f32_16x16x128_f8f6f4 v[158:161], v[18:25], v[190:197], v[158:161], v187, v187 op_sel_hi:[0,0,0]
	v_mfma_scale_f32_16x16x128_f8f6f4 v[154:157], v[26:33], v[190:197], v[154:157], v187, v187 op_sel_hi:[0,0,0]
	v_mfma_scale_f32_16x16x128_f8f6f4 v[150:153], v[18:25], v[198:205], v[150:153], v187, v187 op_sel_hi:[0,0,0]
	v_mfma_scale_f32_16x16x128_f8f6f4 v[146:149], v[26:33], v[198:205], v[146:149], v187, v187 op_sel_hi:[0,0,0]
	v_mfma_scale_f32_16x16x128_f8f6f4 v[142:145], v[18:25], v[206:213], v[142:145], v187, v187 op_sel_hi:[0,0,0]
	v_mfma_scale_f32_16x16x128_f8f6f4 v[138:141], v[26:33], v[206:213], v[138:141], v187, v187 op_sel_hi:[0,0,0]
	v_mfma_scale_f32_16x16x128_f8f6f4 v[134:137], v[18:25], v[214:221], v[134:137], v187, v187 op_sel_hi:[0,0,0]
	v_mfma_scale_f32_16x16x128_f8f6f4 v[130:133], v[26:33], v[214:221], v[130:133], v187, v187 op_sel_hi:[0,0,0]
	s_setprio 2
	s_barrier
	s_add_i32 s12, s24, s17
	v_lshl_add_u64 v[172:173], v[172:173], 0, s[76:77]
	s_mov_b32 m0, s12
	ds_read_b128 v[190:193], v189 offset:49152
	ds_read_b128 v[194:197], v189 offset:50176
	ds_read_b128 v[198:201], v189 offset:51200
	ds_read_b128 v[202:205], v189 offset:52224
	ds_read_b128 v[206:209], v189 offset:53248
	ds_read_b128 v[210:213], v189 offset:54272
	ds_read_b128 v[214:217], v189 offset:55296
	ds_read_b128 v[218:221], v189 offset:56320
	global_load_lds_dwordx4 v[172:173], off
	s_add_i32 m0, s12, 0x2000
	s_add_u32 s6, s6, 0x158080
	v_lshl_add_u64 v[172:173], v[174:175], 0, s[76:77]
	s_addc_u32 s7, s7, 0
	s_add_i32 s12, s25, s17
	global_load_lds_dwordx4 v[172:173], off
	v_lshl_add_u64 v[172:173], s[6:7], 0, v[162:163]
	s_mov_b32 m0, s12
	s_nop 0
	global_load_lds_dwordx4 v[172:173], off
	v_lshl_add_u64 v[172:173], s[6:7], 0, v[166:167]
	s_add_i32 m0, s12, 0x2000
	s_nop 0
	global_load_lds_dwordx4 v[172:173], off
	v_lshl_add_u64 v[172:173], v[176:177], 0, s[76:77]
	s_mov_b32 m0, s95
	s_nop 0
	global_load_lds_dwordx4 v[172:173], off
	v_lshl_add_u64 v[172:173], v[178:179], 0, s[76:77]
	s_mov_b32 m0, vcc_lo
	s_nop 0
	global_load_lds_dwordx4 v[172:173], off
	s_waitcnt vmcnt(8)
	s_waitcnt lgkmcnt(0)
	s_barrier
	s_setprio 1
	s_waitcnt lgkmcnt(0)
	v_mfma_scale_f32_16x16x128_f8f6f4 v[102:105], v[2:9], v[190:197], v[102:105], v187, v187 op_sel_hi:[0,0,0]
	v_mfma_scale_f32_16x16x128_f8f6f4 v[98:101], v[10:17], v[190:197], v[98:101], v187, v187 op_sel_hi:[0,0,0]
	v_mfma_scale_f32_16x16x128_f8f6f4 v[110:113], v[2:9], v[198:205], v[110:113], v187, v187 op_sel_hi:[0,0,0]
	v_mfma_scale_f32_16x16x128_f8f6f4 v[106:109], v[10:17], v[198:205], v[106:109], v187, v187 op_sel_hi:[0,0,0]
	v_mfma_scale_f32_16x16x128_f8f6f4 v[118:121], v[2:9], v[206:213], v[118:121], v187, v187 op_sel_hi:[0,0,0]
	v_mfma_scale_f32_16x16x128_f8f6f4 v[114:117], v[10:17], v[206:213], v[114:117], v187, v187 op_sel_hi:[0,0,0]
	v_mfma_scale_f32_16x16x128_f8f6f4 v[126:129], v[2:9], v[214:221], v[126:129], v187, v187 op_sel_hi:[0,0,0]
	v_mfma_scale_f32_16x16x128_f8f6f4 v[122:125], v[10:17], v[214:221], v[122:125], v187, v187 op_sel_hi:[0,0,0]
	s_setprio 0
	s_setprio 1
	v_mfma_scale_f32_16x16x128_f8f6f4 v[38:41], v[18:25], v[190:197], v[38:41], v187, v187 op_sel_hi:[0,0,0]
	v_mfma_scale_f32_16x16x128_f8f6f4 v[34:37], v[26:33], v[190:197], v[34:37], v187, v187 op_sel_hi:[0,0,0]
	v_mfma_scale_f32_16x16x128_f8f6f4 v[46:49], v[18:25], v[198:205], v[46:49], v187, v187 op_sel_hi:[0,0,0]
	v_mfma_scale_f32_16x16x128_f8f6f4 v[42:45], v[26:33], v[198:205], v[42:45], v187, v187 op_sel_hi:[0,0,0]
	v_mfma_scale_f32_16x16x128_f8f6f4 v[54:57], v[18:25], v[206:213], v[54:57], v187, v187 op_sel_hi:[0,0,0]
	v_mfma_scale_f32_16x16x128_f8f6f4 v[50:53], v[26:33], v[206:213], v[50:53], v187, v187 op_sel_hi:[0,0,0]
	v_mfma_scale_f32_16x16x128_f8f6f4 v[62:65], v[18:25], v[214:221], v[62:65], v187, v187 op_sel_hi:[0,0,0]
	v_mfma_scale_f32_16x16x128_f8f6f4 v[58:61], v[26:33], v[214:221], v[58:61], v187, v187 op_sel_hi:[0,0,0]
	s_setprio 2
	s_barrier
	s_add_i32 vcc_hi, vcc_hi, 2
	s_add_u32 s4, s4, 0x100
	s_addc_u32 s5, s5, 0
	s_cmpk_lt_u32 vcc_hi, 0x54
	s_cbranch_scc1 .LBB0_332
	s_waitcnt vmcnt(0)
	s_mov_b64 s[12:13], s[54:55]
	s_cmpk_gt_u32 s89, 0xff
	s_cbranch_scc1 .LBB0_335
	s_barrier

.LBB0_788:
	v_add_u32_e32 v130, s15, v190
	v_add_u32_e32 v134, s50, v190
	ds_read_b128 v[158:161], v130
	ds_read_b128 v[150:153], v130 offset:1024
	ds_read_b128 v[154:157], v130 offset:2048
	ds_read_b128 v[146:149], v130 offset:3072
	ds_read_b128 v[142:145], v134
	ds_read_b128 v[130:133], v134 offset:1024
	ds_read_b128 v[138:141], v134 offset:2048
	ds_read_b128 v[134:137], v134 offset:3072
	s_add_u32 s36, s34, 0xfff80080
	s_addc_u32 s37, s35, -1
	s_and_b64 s[0:1], s[0:1], exec
	s_cselect_b32 s39, s21, s37
	s_cselect_b32 s38, s60, s36
	s_cselect_b32 s37, s17, s63
	s_cselect_b32 s36, s61, s62
	v_lshl_add_u64 v[218:219], s[34:35], 0, v[172:173]
	s_add_i32 m0, s29, 0xc000
	ds_read_b128 v[182:185], v193
	ds_read_b128 v[186:189], v193 offset:1024
	ds_read_b128 v[194:197], v193 offset:2048
	ds_read_b128 v[198:201], v193 offset:3072
	ds_read_b128 v[202:205], v193 offset:4096
	ds_read_b128 v[206:209], v193 offset:5120
	ds_read_b128 v[210:213], v193 offset:6144
	ds_read_b128 v[214:217], v193 offset:7168
	global_load_lds_dwordx4 v[218:219], off
	v_lshl_add_u64 v[218:219], s[34:35], 0, v[174:175]
	s_add_i32 m0, s29, 0xe000
	s_nop 0
	global_load_lds_dwordx4 v[218:219], off
	s_waitcnt vmcnt(8)
	s_waitcnt lgkmcnt(0)
	s_barrier
	s_setprio 1
	s_waitcnt lgkmcnt(0)
	v_mfma_i32_16x16x64_i8 v[126:129], v[158:161], v[182:185], v[126:129]
	v_mfma_i32_16x16x64_i8 v[122:125], v[154:157], v[182:185], v[122:125]
	v_mfma_i32_16x16x64_i8 v[114:117], v[158:161], v[194:197], v[114:117]
	v_mfma_i32_16x16x64_i8 v[106:109], v[154:157], v[194:197], v[106:109]
	v_mfma_i32_16x16x64_i8 v[98:101], v[158:161], v[202:205], v[98:101]
	v_mfma_i32_16x16x64_i8 v[90:93], v[154:157], v[202:205], v[90:93]
	v_mfma_i32_16x16x64_i8 v[82:85], v[158:161], v[210:213], v[82:85]
	v_mfma_i32_16x16x64_i8 v[74:77], v[154:157], v[210:213], v[74:77]
	s_nop 0
	v_mfma_i32_16x16x64_i8 v[126:129], v[150:153], v[186:189], v[126:129]
	v_mfma_i32_16x16x64_i8 v[122:125], v[146:149], v[186:189], v[122:125]
	v_mfma_i32_16x16x64_i8 v[114:117], v[150:153], v[198:201], v[114:117]
	v_mfma_i32_16x16x64_i8 v[106:109], v[146:149], v[198:201], v[106:109]
	v_mfma_i32_16x16x64_i8 v[98:101], v[150:153], v[206:209], v[98:101]
	v_mfma_i32_16x16x64_i8 v[90:93], v[146:149], v[206:209], v[90:93]
	v_mfma_i32_16x16x64_i8 v[82:85], v[150:153], v[214:217], v[82:85]
	v_mfma_i32_16x16x64_i8 v[74:77], v[146:149], v[214:217], v[74:77]
	s_setprio 0
	s_setprio 1
	v_mfma_i32_16x16x64_i8 v[118:121], v[142:145], v[182:185], v[118:121]
	v_mfma_i32_16x16x64_i8 v[110:113], v[138:141], v[182:185], v[110:113]
	v_mfma_i32_16x16x64_i8 v[102:105], v[142:145], v[194:197], v[102:105]
	v_mfma_i32_16x16x64_i8 v[94:97], v[138:141], v[194:197], v[94:97]
	v_mfma_i32_16x16x64_i8 v[86:89], v[142:145], v[202:205], v[86:89]
	v_mfma_i32_16x16x64_i8 v[78:81], v[138:141], v[202:205], v[78:81]
	v_mfma_i32_16x16x64_i8 v[70:73], v[142:145], v[210:213], v[70:73]
	v_mfma_i32_16x16x64_i8 v[66:69], v[138:141], v[210:213], v[66:69]
	s_nop 0
	v_mfma_i32_16x16x64_i8 v[118:121], v[130:133], v[186:189], v[118:121]
	v_mfma_i32_16x16x64_i8 v[110:113], v[134:137], v[186:189], v[110:113]
	v_mfma_i32_16x16x64_i8 v[102:105], v[130:133], v[198:201], v[102:105]
	v_mfma_i32_16x16x64_i8 v[94:97], v[134:137], v[198:201], v[94:97]
	v_mfma_i32_16x16x64_i8 v[86:89], v[130:133], v[206:209], v[86:89]
	v_mfma_i32_16x16x64_i8 v[78:81], v[134:137], v[206:209], v[78:81]
	v_mfma_i32_16x16x64_i8 v[70:73], v[130:133], v[214:217], v[70:73]
	v_mfma_i32_16x16x64_i8 v[66:69], v[134:137], v[214:217], v[66:69]
	s_setprio 2
	s_barrier
	s_add_i32 s0, s15, s40
	v_lshl_add_u64 v[182:183], s[36:37], 0, v[164:165]
	s_mov_b32 m0, s0
	ds_read_b128 v[194:197], v193 offset:16384
	ds_read_b128 v[198:201], v193 offset:17408
	ds_read_b128 v[202:205], v193 offset:18432
	ds_read_b128 v[206:209], v193 offset:19456
	ds_read_b128 v[210:213], v193 offset:20480
	ds_read_b128 v[214:217], v193 offset:21504
	ds_read_b128 v[218:221], v193 offset:22528
	ds_read_b128 v[222:225], v193 offset:23552
	global_load_lds_dwordx4 v[182:183], off
	s_add_i32 m0, s0, 0x2000
	s_add_u32 s0, s36, 0x80000
	v_lshl_add_u64 v[184:185], s[36:37], 0, v[168:169]
	s_addc_u32 s1, s37, 0
	s_add_i32 s66, s50, s40
	global_load_lds_dwordx4 v[184:185], off
	v_lshl_add_u64 v[186:187], s[0:1], 0, v[164:165]
	s_mov_b32 m0, s66
	v_lshl_add_u64 v[188:189], s[38:39], 0, v[166:167]
	global_load_lds_dwordx4 v[186:187], off
	v_lshl_add_u64 v[186:187], s[0:1], 0, v[168:169]
	s_add_i32 m0, s66, 0x2000
	s_nop 0
	global_load_lds_dwordx4 v[186:187], off
	v_lshl_add_u64 v[186:187], s[38:39], 0, v[162:163]
	s_mov_b32 m0, s29
	s_nop 0
	global_load_lds_dwordx4 v[186:187], off
	s_mov_b32 m0, s31
	s_nop 0
	global_load_lds_dwordx4 v[188:189], off
	s_waitcnt vmcnt(8)
	s_waitcnt lgkmcnt(0)
	s_barrier
	s_setprio 1
	s_waitcnt lgkmcnt(0)
	v_mfma_i32_16x16x64_i8 v[62:65], v[158:161], v[194:197], v[62:65]
	v_mfma_i32_16x16x64_i8 v[58:61], v[154:157], v[194:197], v[58:61]
	v_mfma_i32_16x16x64_i8 v[50:53], v[158:161], v[202:205], v[50:53]
	v_mfma_i32_16x16x64_i8 v[42:45], v[154:157], v[202:205], v[42:45]
	v_mfma_i32_16x16x64_i8 v[34:37], v[158:161], v[210:213], v[34:37]
	v_mfma_i32_16x16x64_i8 v[26:29], v[154:157], v[210:213], v[26:29]
	v_mfma_i32_16x16x64_i8 v[18:21], v[158:161], v[218:221], v[18:21]
	v_mfma_i32_16x16x64_i8 v[10:13], v[154:157], v[218:221], v[10:13]
	s_nop 0
	v_mfma_i32_16x16x64_i8 v[62:65], v[150:153], v[198:201], v[62:65]
	v_mfma_i32_16x16x64_i8 v[58:61], v[146:149], v[198:201], v[58:61]
	v_mfma_i32_16x16x64_i8 v[50:53], v[150:153], v[206:209], v[50:53]
	v_mfma_i32_16x16x64_i8 v[42:45], v[146:149], v[206:209], v[42:45]
	v_mfma_i32_16x16x64_i8 v[34:37], v[150:153], v[214:217], v[34:37]
	v_mfma_i32_16x16x64_i8 v[26:29], v[146:149], v[214:217], v[26:29]
	v_mfma_i32_16x16x64_i8 v[18:21], v[150:153], v[222:225], v[18:21]
	v_mfma_i32_16x16x64_i8 v[10:13], v[146:149], v[222:225], v[10:13]
	s_setprio 0
	s_setprio 1
	v_mfma_i32_16x16x64_i8 v[54:57], v[142:145], v[194:197], v[54:57]
	v_mfma_i32_16x16x64_i8 v[46:49], v[138:141], v[194:197], v[46:49]
	v_mfma_i32_16x16x64_i8 v[38:41], v[142:145], v[202:205], v[38:41]
	v_mfma_i32_16x16x64_i8 v[30:33], v[138:141], v[202:205], v[30:33]
	v_mfma_i32_16x16x64_i8 v[22:25], v[142:145], v[210:213], v[22:25]
	v_mfma_i32_16x16x64_i8 v[14:17], v[138:141], v[210:213], v[14:17]
	v_mfma_i32_16x16x64_i8 v[6:9], v[142:145], v[218:221], v[6:9]
	v_mfma_i32_16x16x64_i8 v[2:5], v[138:141], v[218:221], v[2:5]
	s_nop 0
	v_mfma_i32_16x16x64_i8 v[54:57], v[130:133], v[198:201], v[54:57]
	v_mfma_i32_16x16x64_i8 v[46:49], v[134:137], v[198:201], v[46:49]
	v_mfma_i32_16x16x64_i8 v[38:41], v[130:133], v[206:209], v[38:41]
	v_mfma_i32_16x16x64_i8 v[30:33], v[134:137], v[206:209], v[30:33]
	v_mfma_i32_16x16x64_i8 v[22:25], v[130:133], v[214:217], v[22:25]
	v_mfma_i32_16x16x64_i8 v[14:17], v[134:137], v[214:217], v[14:17]
	v_mfma_i32_16x16x64_i8 v[6:9], v[130:133], v[222:225], v[6:9]
	v_mfma_i32_16x16x64_i8 v[2:5], v[134:137], v[222:225], v[2:5]
	s_setprio 2
	s_barrier
	s_add_i32 s66, 0, 0x18000
	s_add_i32 s67, 0, 0x1c000
	v_add_u32_e32 v142, s66, v190
	v_add_u32_e32 v158, s67, v190
	ds_read_b128 v[130:133], v142
	ds_read_b128 v[134:137], v142 offset:1024
	ds_read_b128 v[138:141], v142 offset:2048
	ds_read_b128 v[142:145], v142 offset:3072
	ds_read_b128 v[146:149], v158
	ds_read_b128 v[150:153], v158 offset:1024
	ds_read_b128 v[154:157], v158 offset:2048
	ds_read_b128 v[158:161], v158 offset:3072
	s_add_u32 s0, s38, 0x80000
	s_addc_u32 s1, s39, 0
	s_mov_b32 m0, s42
	v_lshl_add_u64 v[226:227], s[0:1], 0, v[162:163]
	ds_read_b128 v[194:197], v193 offset:32768
	ds_read_b128 v[198:201], v193 offset:33792
	ds_read_b128 v[202:205], v193 offset:34816
	ds_read_b128 v[206:209], v193 offset:35840
	ds_read_b128 v[210:213], v193 offset:36864
	ds_read_b128 v[214:217], v193 offset:37888
	ds_read_b128 v[218:221], v193 offset:38912
	ds_read_b128 v[222:225], v193 offset:39936
	global_load_lds_dwordx4 v[226:227], off
	v_lshl_add_u64 v[226:227], s[0:1], 0, v[166:167]
	s_mov_b32 m0, s43
	s_nop 0
	global_load_lds_dwordx4 v[226:227], off
	s_waitcnt vmcnt(8)
	s_waitcnt lgkmcnt(0)
	s_barrier
	s_setprio 1
	s_waitcnt lgkmcnt(0)
	v_mfma_i32_16x16x64_i8 v[126:129], v[130:133], v[194:197], v[126:129]
	v_mfma_i32_16x16x64_i8 v[122:125], v[138:141], v[194:197], v[122:125]
	v_mfma_i32_16x16x64_i8 v[114:117], v[130:133], v[202:205], v[114:117]
	v_mfma_i32_16x16x64_i8 v[106:109], v[138:141], v[202:205], v[106:109]
	v_mfma_i32_16x16x64_i8 v[98:101], v[130:133], v[210:213], v[98:101]
	v_mfma_i32_16x16x64_i8 v[90:93], v[138:141], v[210:213], v[90:93]
	v_mfma_i32_16x16x64_i8 v[82:85], v[130:133], v[218:221], v[82:85]
	v_mfma_i32_16x16x64_i8 v[74:77], v[138:141], v[218:221], v[74:77]
	s_nop 0
	v_mfma_i32_16x16x64_i8 v[126:129], v[134:137], v[198:201], v[126:129]
	v_mfma_i32_16x16x64_i8 v[122:125], v[142:145], v[198:201], v[122:125]
	v_mfma_i32_16x16x64_i8 v[114:117], v[134:137], v[206:209], v[114:117]
	v_mfma_i32_16x16x64_i8 v[106:109], v[142:145], v[206:209], v[106:109]
	v_mfma_i32_16x16x64_i8 v[98:101], v[134:137], v[214:217], v[98:101]
	v_mfma_i32_16x16x64_i8 v[90:93], v[142:145], v[214:217], v[90:93]
	v_mfma_i32_16x16x64_i8 v[82:85], v[134:137], v[222:225], v[82:85]
	v_mfma_i32_16x16x64_i8 v[74:77], v[142:145], v[222:225], v[74:77]
	s_setprio 0
	s_setprio 1
	v_mfma_i32_16x16x64_i8 v[118:121], v[146:149], v[194:197], v[118:121]
	v_mfma_i32_16x16x64_i8 v[110:113], v[154:157], v[194:197], v[110:113]
	v_mfma_i32_16x16x64_i8 v[102:105], v[146:149], v[202:205], v[102:105]
	v_mfma_i32_16x16x64_i8 v[94:97], v[154:157], v[202:205], v[94:97]
	v_mfma_i32_16x16x64_i8 v[86:89], v[146:149], v[210:213], v[86:89]
	v_mfma_i32_16x16x64_i8 v[78:81], v[154:157], v[210:213], v[78:81]
	v_mfma_i32_16x16x64_i8 v[70:73], v[146:149], v[218:221], v[70:73]
	v_mfma_i32_16x16x64_i8 v[66:69], v[154:157], v[218:221], v[66:69]
	s_nop 0
	v_mfma_i32_16x16x64_i8 v[118:121], v[150:153], v[198:201], v[118:121]
	v_mfma_i32_16x16x64_i8 v[110:113], v[158:161], v[198:201], v[110:113]
	v_mfma_i32_16x16x64_i8 v[102:105], v[150:153], v[206:209], v[102:105]
	v_mfma_i32_16x16x64_i8 v[94:97], v[158:161], v[206:209], v[94:97]
	v_mfma_i32_16x16x64_i8 v[86:89], v[150:153], v[214:217], v[86:89]
	v_mfma_i32_16x16x64_i8 v[78:81], v[158:161], v[214:217], v[78:81]
	v_mfma_i32_16x16x64_i8 v[70:73], v[150:153], v[222:225], v[70:73]
	v_mfma_i32_16x16x64_i8 v[66:69], v[158:161], v[222:225], v[66:69]
	s_setprio 2
	s_barrier
	s_add_i32 s0, s66, s40
	v_lshl_add_u64 v[182:183], v[182:183], 0, s[10:11]
	s_mov_b32 m0, s0
	ds_read_b128 v[194:197], v193 offset:49152
	ds_read_b128 v[198:201], v193 offset:50176
	ds_read_b128 v[202:205], v193 offset:51200
	ds_read_b128 v[206:209], v193 offset:52224
	ds_read_b128 v[210:213], v193 offset:53248
	ds_read_b128 v[214:217], v193 offset:54272
	ds_read_b128 v[218:221], v193 offset:55296
	ds_read_b128 v[222:225], v193 offset:56320
	global_load_lds_dwordx4 v[182:183], off
	s_add_i32 m0, s0, 0x2000
	s_add_u32 s0, s36, 0x80080
	v_lshl_add_u64 v[182:183], v[184:185], 0, s[10:11]
	s_addc_u32 s1, s37, 0
	s_add_i32 s36, s67, s40
	global_load_lds_dwordx4 v[182:183], off
	v_lshl_add_u64 v[182:183], s[0:1], 0, v[164:165]
	s_mov_b32 m0, s36
	s_nop 0
	global_load_lds_dwordx4 v[182:183], off
	v_lshl_add_u64 v[182:183], s[0:1], 0, v[168:169]
	s_add_i32 m0, s36, 0x2000
	s_nop 0
	global_load_lds_dwordx4 v[182:183], off
	v_lshl_add_u64 v[182:183], v[186:187], 0, s[10:11]
	s_mov_b32 m0, s48
	s_nop 0
	global_load_lds_dwordx4 v[182:183], off
	v_lshl_add_u64 v[182:183], v[188:189], 0, s[10:11]
	s_mov_b32 m0, s49
	s_nop 0
	global_load_lds_dwordx4 v[182:183], off
	s_waitcnt vmcnt(8)
	s_waitcnt lgkmcnt(0)
	s_barrier
	s_setprio 1
	s_waitcnt lgkmcnt(0)
	v_mfma_i32_16x16x64_i8 v[62:65], v[130:133], v[194:197], v[62:65]
	v_mfma_i32_16x16x64_i8 v[58:61], v[138:141], v[194:197], v[58:61]
	v_mfma_i32_16x16x64_i8 v[50:53], v[130:133], v[202:205], v[50:53]
	v_mfma_i32_16x16x64_i8 v[42:45], v[138:141], v[202:205], v[42:45]
	v_mfma_i32_16x16x64_i8 v[34:37], v[130:133], v[210:213], v[34:37]
	v_mfma_i32_16x16x64_i8 v[26:29], v[138:141], v[210:213], v[26:29]
	v_mfma_i32_16x16x64_i8 v[18:21], v[130:133], v[218:221], v[18:21]
	v_mfma_i32_16x16x64_i8 v[10:13], v[138:141], v[218:221], v[10:13]
	s_nop 0
	v_mfma_i32_16x16x64_i8 v[62:65], v[134:137], v[198:201], v[62:65]
	v_mfma_i32_16x16x64_i8 v[58:61], v[142:145], v[198:201], v[58:61]
	v_mfma_i32_16x16x64_i8 v[50:53], v[134:137], v[206:209], v[50:53]
	v_mfma_i32_16x16x64_i8 v[42:45], v[142:145], v[206:209], v[42:45]
	v_mfma_i32_16x16x64_i8 v[34:37], v[134:137], v[214:217], v[34:37]
	v_mfma_i32_16x16x64_i8 v[26:29], v[142:145], v[214:217], v[26:29]
	v_mfma_i32_16x16x64_i8 v[18:21], v[134:137], v[222:225], v[18:21]
	v_mfma_i32_16x16x64_i8 v[10:13], v[142:145], v[222:225], v[10:13]
	s_setprio 0
	s_setprio 1
	v_mfma_i32_16x16x64_i8 v[54:57], v[146:149], v[194:197], v[54:57]
	v_mfma_i32_16x16x64_i8 v[46:49], v[154:157], v[194:197], v[46:49]
	v_mfma_i32_16x16x64_i8 v[38:41], v[146:149], v[202:205], v[38:41]
	v_mfma_i32_16x16x64_i8 v[30:33], v[154:157], v[202:205], v[30:33]
	v_mfma_i32_16x16x64_i8 v[22:25], v[146:149], v[210:213], v[22:25]
	v_mfma_i32_16x16x64_i8 v[14:17], v[154:157], v[210:213], v[14:17]
	v_mfma_i32_16x16x64_i8 v[6:9], v[146:149], v[218:221], v[6:9]
	v_mfma_i32_16x16x64_i8 v[2:5], v[154:157], v[218:221], v[2:5]
	s_nop 0
	v_mfma_i32_16x16x64_i8 v[54:57], v[150:153], v[198:201], v[54:57]
	v_mfma_i32_16x16x64_i8 v[46:49], v[158:161], v[198:201], v[46:49]
	v_mfma_i32_16x16x64_i8 v[38:41], v[150:153], v[206:209], v[38:41]
	v_mfma_i32_16x16x64_i8 v[30:33], v[158:161], v[206:209], v[30:33]
	v_mfma_i32_16x16x64_i8 v[22:25], v[150:153], v[214:217], v[22:25]
	v_mfma_i32_16x16x64_i8 v[14:17], v[158:161], v[214:217], v[14:17]
	v_mfma_i32_16x16x64_i8 v[6:9], v[150:153], v[222:225], v[6:9]
	v_mfma_i32_16x16x64_i8 v[2:5], v[158:161], v[222:225], v[2:5]
	s_setprio 2
	s_barrier
	s_add_i32 s64, s64, 2
	s_add_u32 s34, s34, 0x100
	s_addc_u32 s35, s35, 0
	s_add_u32 s62, s62, 0x100
	s_addc_u32 s63, s63, 0
	s_cmp_gt_u32 s64, 29
	s_cbranch_scc1 .LBB0_791

.LBB0_992:
	global_load_dwordx4 v[36:39], v[24:25], off offset:-2048
	global_load_dwordx4 v[40:43], v[24:25], off offset:-1536
	global_load_dwordx4 v[44:47], v[24:25], off offset:-1024
	global_load_dwordx4 v[48:51], v[24:25], off offset:-512
	global_load_dwordx4 v[52:55], v[24:25], off
	global_load_dwordx4 v[56:59], v[24:25], off offset:512
	global_load_dwordx4 v[60:63], v[24:25], off offset:1024
	global_load_dwordx4 v[64:67], v[24:25], off offset:1536
	s_waitcnt vmcnt(0)
	global_load_dwordx4 v[2:5], v[10:11], off offset:16
	global_load_dwordx4 v[6:9], v[10:11], off
	s_add_i32 s3, s3, s92
	v_lshl_add_u64 v[24:25], v[24:25], 0, s[6:7]
	s_cmpk_lt_i32 s3, 0x4000
	s_waitcnt vmcnt(0)
	v_and_b32_e32 v69, 0xffff0000, v36
	v_and_b32_e32 v71, 0xffff0000, v37
	v_lshlrev_b32_e32 v68, 16, v36
	v_lshlrev_b32_e32 v70, 16, v37
	v_and_b32_e32 v73, 0xffff0000, v38
	v_lshlrev_b32_e32 v94, 16, v49
	v_and_b32_e32 v95, 0xffff0000, v49
	v_lshlrev_b32_e32 v96, 16, v50
	v_and_b32_e32 v97, 0xffff0000, v50
	v_lshlrev_b32_e32 v98, 16, v51
	v_and_b32_e32 v99, 0xffff0000, v51
	v_lshlrev_b32_e32 v51, 16, v60
	v_and_b32_e32 v50, 0xffff0000, v60
	v_mul_f32_e32 v49, v69, v69
	v_mul_f32_e32 v60, v71, v71
	v_lshlrev_b32_e32 v72, 16, v38
	v_and_b32_e32 v75, 0xffff0000, v39
	v_lshlrev_b32_e32 v90, 16, v47
	v_and_b32_e32 v91, 0xffff0000, v47
	v_lshlrev_b32_e32 v92, 16, v48
	v_and_b32_e32 v93, 0xffff0000, v48
	v_lshlrev_b32_e32 v48, 16, v61
	v_and_b32_e32 v47, 0xffff0000, v61
	v_mul_f32_e32 v61, v73, v73
	v_fmac_f32_e32 v49, v68, v68
	v_fmac_f32_e32 v60, v70, v70
	v_lshlrev_b32_e32 v74, 16, v39
	v_and_b32_e32 v77, 0xffff0000, v40
	v_lshlrev_b32_e32 v86, 16, v45
	v_and_b32_e32 v87, 0xffff0000, v45
	v_lshlrev_b32_e32 v88, 16, v46
	v_and_b32_e32 v89, 0xffff0000, v46
	v_lshlrev_b32_e32 v46, 16, v62
	v_and_b32_e32 v45, 0xffff0000, v62
	v_mul_f32_e32 v62, v75, v75
	v_fmac_f32_e32 v61, v72, v72
	v_add_f32_e32 v49, v49, v60
	v_lshlrev_b32_e32 v76, 16, v40
	v_and_b32_e32 v79, 0xffff0000, v41
	v_lshlrev_b32_e32 v82, 16, v43
	v_and_b32_e32 v83, 0xffff0000, v43
	v_lshlrev_b32_e32 v84, 16, v44
	v_and_b32_e32 v85, 0xffff0000, v44
	v_lshlrev_b32_e32 v44, 16, v63
	v_and_b32_e32 v43, 0xffff0000, v63
	v_mul_f32_e32 v63, v77, v77
	v_fmac_f32_e32 v62, v74, v74
	v_add_f32_e32 v49, v61, v49
	v_lshlrev_b32_e32 v78, 16, v41
	v_and_b32_e32 v81, 0xffff0000, v42
	v_lshlrev_b32_e32 v35, 16, v64
	v_and_b32_e32 v36, 0xffff0000, v64
	v_mul_f32_e32 v64, v79, v79
	v_fmac_f32_e32 v63, v76, v76
	v_add_f32_e32 v49, v62, v49
	v_lshlrev_b32_e32 v80, 16, v42
	v_lshlrev_b32_e32 v37, 16, v65
	v_and_b32_e32 v38, 0xffff0000, v65
	v_mul_f32_e32 v65, v81, v81
	v_fmac_f32_e32 v64, v78, v78
	v_add_f32_e32 v49, v63, v49
	v_lshlrev_b32_e32 v39, 16, v66
	v_and_b32_e32 v40, 0xffff0000, v66
	v_mul_f32_e32 v66, v83, v83
	v_fmac_f32_e32 v65, v80, v80
	v_add_f32_e32 v49, v64, v49
	v_lshlrev_b32_e32 v41, 16, v67
	v_and_b32_e32 v42, 0xffff0000, v67
	v_mul_f32_e32 v67, v85, v85
	v_fmac_f32_e32 v66, v82, v82
	v_add_f32_e32 v49, v65, v49
	v_mul_f32_e32 v108, v87, v87
	v_fmac_f32_e32 v67, v84, v84
	v_add_f32_e32 v49, v66, v49
	v_mul_f32_e32 v109, v89, v89
	v_fmac_f32_e32 v108, v86, v86
	v_add_f32_e32 v49, v67, v49
	v_mul_f32_e32 v110, v91, v91
	v_fmac_f32_e32 v109, v88, v88
	v_add_f32_e32 v49, v108, v49
	v_mul_f32_e32 v111, v93, v93
	v_fmac_f32_e32 v110, v90, v90
	v_add_f32_e32 v49, v109, v49
	v_mul_f32_e32 v112, v95, v95
	v_fmac_f32_e32 v111, v92, v92
	v_add_f32_e32 v49, v110, v49
	v_mul_f32_e32 v113, v97, v97
	v_fmac_f32_e32 v112, v94, v94
	v_add_f32_e32 v49, v111, v49
	v_lshlrev_b32_e32 v100, 16, v52
	v_and_b32_e32 v52, 0xffff0000, v52
	v_mul_f32_e32 v114, v99, v99
	v_fmac_f32_e32 v113, v96, v96
	v_add_f32_e32 v49, v112, v49
	v_lshlrev_b32_e32 v101, 16, v53
	v_and_b32_e32 v53, 0xffff0000, v53
	v_mul_f32_e32 v115, v52, v52
	v_fmac_f32_e32 v114, v98, v98
	v_add_f32_e32 v49, v113, v49
	v_lshlrev_b32_e32 v102, 16, v54
	v_and_b32_e32 v54, 0xffff0000, v54
	v_mul_f32_e32 v116, v53, v53
	v_fmac_f32_e32 v115, v100, v100
	v_add_f32_e32 v49, v114, v49
	v_lshlrev_b32_e32 v103, 16, v55
	v_and_b32_e32 v55, 0xffff0000, v55
	v_mul_f32_e32 v117, v54, v54
	v_fmac_f32_e32 v116, v101, v101
	v_add_f32_e32 v49, v115, v49
	v_lshlrev_b32_e32 v104, 16, v56
	v_and_b32_e32 v56, 0xffff0000, v56
	v_mul_f32_e32 v118, v55, v55
	v_fmac_f32_e32 v117, v102, v102
	v_add_f32_e32 v49, v116, v49
	v_lshlrev_b32_e32 v105, 16, v57
	v_and_b32_e32 v57, 0xffff0000, v57
	v_mul_f32_e32 v119, v56, v56
	v_fmac_f32_e32 v118, v103, v103
	v_add_f32_e32 v49, v117, v49
	v_lshlrev_b32_e32 v106, 16, v58
	v_and_b32_e32 v58, 0xffff0000, v58
	v_mul_f32_e32 v120, v57, v57
	v_fmac_f32_e32 v119, v104, v104
	v_add_f32_e32 v49, v118, v49
	v_lshlrev_b32_e32 v107, 16, v59
	v_and_b32_e32 v59, 0xffff0000, v59
	v_mul_f32_e32 v121, v58, v58
	v_fmac_f32_e32 v120, v105, v105
	v_add_f32_e32 v49, v119, v49
	v_mul_f32_e32 v122, v59, v59
	v_fmac_f32_e32 v121, v106, v106
	v_add_f32_e32 v49, v120, v49
	v_mul_f32_e32 v123, v50, v50
	v_fmac_f32_e32 v122, v107, v107
	v_add_f32_e32 v49, v121, v49
	v_mul_f32_e32 v124, v47, v47
	v_fmac_f32_e32 v123, v51, v51
	v_add_f32_e32 v49, v122, v49
	v_mul_f32_e32 v125, v45, v45
	v_fmac_f32_e32 v124, v48, v48
	v_add_f32_e32 v49, v123, v49
	v_mul_f32_e32 v126, v43, v43
	v_fmac_f32_e32 v125, v46, v46
	v_add_f32_e32 v49, v124, v49
	v_mul_f32_e32 v127, v36, v36
	v_fmac_f32_e32 v126, v44, v44
	v_add_f32_e32 v49, v125, v49
	v_mul_f32_e32 v128, v38, v38
	v_fmac_f32_e32 v127, v35, v35
	v_add_f32_e32 v49, v126, v49
	v_mul_f32_e32 v129, v40, v40
	v_fmac_f32_e32 v128, v37, v37
	v_add_f32_e32 v49, v127, v49
	v_mul_f32_e32 v130, v42, v42
	v_fmac_f32_e32 v129, v39, v39
	v_add_f32_e32 v49, v128, v49
	v_fmac_f32_e32 v130, v41, v41
	v_add_f32_e32 v49, v129, v49
	v_add_f32_e32 v49, v130, v49
	ds_bpermute_b32 v60, v1, v49
	s_waitcnt lgkmcnt(0)
	v_add_f32_e32 v49, v49, v60
	ds_bpermute_b32 v60, v28, v49
	s_waitcnt lgkmcnt(0)
	v_add_f32_e32 v49, v49, v60
	ds_bpermute_b32 v60, v29, v49
	s_waitcnt lgkmcnt(0)
	v_add_f32_e32 v49, v49, v60
	ds_bpermute_b32 v60, v30, v49
	s_waitcnt lgkmcnt(0)
	v_add_f32_e32 v49, v49, v60
	ds_bpermute_b32 v60, v31, v49
	s_waitcnt lgkmcnt(0)
	v_add_f32_e32 v49, v49, v60
	v_fmamk_f32 v49, v49, 0x3a000000, v32
	v_mul_f32_e32 v60, 0x4f800000, v49
	v_cmp_gt_f32_e32 vcc, s10, v49
	s_nop 1
	v_cndmask_b32_e32 v49, v49, v60, vcc
	v_sqrt_f32_e32 v60, v49
	s_nop 0
	v_add_u32_e32 v61, -1, v60
	v_add_u32_e32 v62, 1, v60
	v_fma_f32 v63, -v61, v60, v49
	v_fma_f32 v64, -v62, v60, v49
	v_cmp_ge_f32_e64 s[4:5], 0, v63
	s_nop 1
	v_cndmask_b32_e64 v60, v60, v61, s[4:5]
	v_cmp_lt_f32_e64 s[4:5], 0, v64
	s_nop 1
	v_cndmask_b32_e64 v60, v60, v62, s[4:5]
	v_mul_f32_e32 v61, 0x37800000, v60
	v_cndmask_b32_e32 v60, v60, v61, vcc
	v_cmp_class_f32_e32 vcc, v49, v33
	s_nop 1
	v_cndmask_b32_e32 v49, v60, v49, vcc
	v_div_scale_f32 v60, s[4:5], v49, v49, 1.0
	v_rcp_f32_e32 v62, v60
	v_div_scale_f32 v61, vcc, 1.0, v49, 1.0
	v_fma_f32 v63, -v60, v62, 1.0
	v_fmac_f32_e32 v62, v63, v62
	v_mul_f32_e32 v63, v61, v62
	v_fma_f32 v64, -v60, v63, v61
	v_fmac_f32_e32 v63, v64, v62
	v_fma_f32 v60, -v60, v63, v61
	v_div_fmas_f32 v60, v60, v62, v63
	v_div_fixup_f32 v49, v60, v49, 1.0
	v_mul_f32_e32 v49, 0x417e0000, v49
	v_mul_f32_e32 v61, v49, v69
	v_mul_f32_e32 v65, v49, v73
	v_mul_f32_e32 v60, v49, v68
	v_mul_f32_e32 v62, v49, v70
	v_mul_f32_e32 v63, v49, v71
	v_mul_f32_e32 v64, v49, v72
	v_mul_f32_e32 v66, v49, v74
	v_mul_f32_e32 v67, v49, v75
	v_mul_f32_e32 v7, v7, v61
	v_mul_f32_e32 v3, v3, v65
	v_mul_f32_e32 v6, v6, v60
	v_mul_f32_e32 v8, v8, v62
	v_mul_f32_e32 v9, v9, v63
	v_mul_f32_e32 v2, v2, v64
	v_mul_f32_e32 v4, v4, v66
	v_mul_f32_e32 v5, v5, v67
	v_med3_f32 v7, v7, s11, v34
	v_med3_f32 v3, v3, s11, v34
	v_med3_f32 v6, v6, s11, v34
	v_med3_f32 v8, v8, s11, v34
	v_med3_f32 v9, v9, s11, v34
	v_med3_f32 v2, v2, s11, v34
	v_med3_f32 v4, v4, s11, v34
	v_med3_f32 v5, v5, s11, v34
	v_rndne_f32_e32 v7, v7
	v_rndne_f32_e32 v3, v3
	v_rndne_f32_e32 v6, v6
	v_rndne_f32_e32 v8, v8
	v_rndne_f32_e32 v9, v9
	v_rndne_f32_e32 v2, v2
	v_rndne_f32_e32 v4, v4
	v_rndne_f32_e32 v5, v5
	v_cvt_i32_f32_e32 v7, v7
	v_cvt_i32_f32_e32 v3, v3
	v_cvt_i32_f32_e32 v6, v6
	v_cvt_i32_f32_sdwa v8, v8 dst_sel:WORD_1 dst_unused:UNUSED_PAD src0_sel:DWORD
	v_cvt_i32_f32_e32 v9, v9
	v_cvt_i32_f32_e32 v2, v2
	v_cvt_i32_f32_sdwa v4, v4 dst_sel:WORD_1 dst_unused:UNUSED_PAD src0_sel:DWORD
	v_cvt_i32_f32_e32 v5, v5
	v_lshlrev_b32_e32 v7, 8, v7
	v_lshlrev_b32_e32 v3, 8, v3
	v_and_b32_e32 v8, 0xff0000, v8
	v_perm_b32 v6, v9, v6, s12
	v_and_b32_e32 v4, 0xff0000, v4
	v_perm_b32 v5, v5, v2, s12
	v_and_b32_e32 v2, 0xff00, v7
	v_and_b32_e32 v3, 0xff00, v3
	v_or3_b32 v2, v6, v2, v8
	v_or3_b32 v3, v5, v3, v4
	global_store_dwordx2 v[26:27], v[2:3], off offset:-1024
	global_load_dwordx4 v[2:5], v[12:13], off
	s_nop 0
	global_load_dwordx4 v[6:9], v[12:13], off offset:16
	v_mul_f32_e32 v68, v49, v76
	v_mul_f32_e32 v69, v49, v77
	v_mul_f32_e32 v71, v49, v79
	v_mul_f32_e32 v73, v49, v81
	v_mul_f32_e32 v70, v49, v78
	v_mul_f32_e32 v72, v49, v80
	v_mul_f32_e32 v74, v49, v82
	v_mul_f32_e32 v75, v49, v83
	v_mul_f32_e32 v76, v49, v84
	v_mul_f32_e32 v77, v49, v85
	v_mul_f32_e32 v79, v49, v87
	v_mul_f32_e32 v81, v49, v89
	v_mul_f32_e32 v78, v49, v86
	v_mul_f32_e32 v80, v49, v88
	v_mul_f32_e32 v82, v49, v90
	v_mul_f32_e32 v83, v49, v91
	v_mul_f32_e32 v84, v49, v92
	v_mul_f32_e32 v85, v49, v93
	v_mul_f32_e32 v87, v49, v95
	v_mul_f32_e32 v89, v49, v97
	v_mul_f32_e32 v86, v49, v94
	v_mul_f32_e32 v88, v49, v96
	v_mul_f32_e32 v90, v49, v98
	v_mul_f32_e32 v91, v49, v99
	v_mul_f32_e32 v92, v49, v100
	v_mul_f32_e32 v52, v49, v52
	v_mul_f32_e32 v53, v49, v53
	v_mul_f32_e32 v54, v49, v54
	v_mul_f32_e32 v93, v49, v101
	v_mul_f32_e32 v94, v49, v102
	v_mul_f32_e32 v95, v49, v103
	v_mul_f32_e32 v55, v49, v55
	v_mul_f32_e32 v96, v49, v104
	v_mul_f32_e32 v56, v49, v56
	v_mul_f32_e32 v57, v49, v57
	v_mul_f32_e32 v58, v49, v58
	v_mul_f32_e32 v97, v49, v105
	v_mul_f32_e32 v98, v49, v106
	v_mul_f32_e32 v99, v49, v107
	v_mul_f32_e32 v59, v49, v59
	v_mul_f32_e32 v51, v49, v51
	v_mul_f32_e32 v50, v49, v50
	v_mul_f32_e32 v47, v49, v47
	v_mul_f32_e32 v45, v49, v45
	v_mul_f32_e32 v48, v49, v48
	v_mul_f32_e32 v46, v49, v46
	v_mul_f32_e32 v44, v49, v44
	v_mul_f32_e32 v43, v49, v43
	v_mul_f32_e32 v35, v49, v35
	v_mul_f32_e32 v36, v49, v36
	v_mul_f32_e32 v38, v49, v38
	v_mul_f32_e32 v40, v49, v40
	v_mul_f32_e32 v37, v49, v37
	v_mul_f32_e32 v39, v49, v39
	v_mul_f32_e32 v41, v49, v41
	v_mul_f32_e32 v42, v49, v42
	s_waitcnt vmcnt(1)
	v_mul_f32_e32 v2, v2, v68
	v_mul_f32_e32 v3, v3, v69
	v_mul_f32_e32 v5, v5, v71
	s_waitcnt vmcnt(0)
	v_mul_f32_e32 v7, v7, v73
	v_mul_f32_e32 v4, v4, v70
	v_mul_f32_e32 v6, v6, v72
	v_mul_f32_e32 v8, v8, v74
	v_mul_f32_e32 v9, v9, v75
	v_med3_f32 v2, v2, s11, v34
	v_med3_f32 v3, v3, s11, v34
	v_med3_f32 v5, v5, s11, v34
	v_med3_f32 v7, v7, s11, v34
	v_med3_f32 v4, v4, s11, v34
	v_med3_f32 v6, v6, s11, v34
	v_med3_f32 v8, v8, s11, v34
	v_med3_f32 v9, v9, s11, v34
	v_rndne_f32_e32 v2, v2
	v_rndne_f32_e32 v3, v3
	v_rndne_f32_e32 v5, v5
	v_rndne_f32_e32 v7, v7
	v_rndne_f32_e32 v4, v4
	v_rndne_f32_e32 v6, v6
	v_rndne_f32_e32 v8, v8
	v_rndne_f32_e32 v9, v9
	v_cvt_i32_f32_e32 v2, v2
	v_cvt_i32_f32_e32 v3, v3
	v_cvt_i32_f32_e32 v5, v5
	v_cvt_i32_f32_e32 v7, v7
	v_cvt_i32_f32_sdwa v4, v4 dst_sel:WORD_1 dst_unused:UNUSED_PAD src0_sel:DWORD
	v_cvt_i32_f32_e32 v6, v6
	v_cvt_i32_f32_sdwa v8, v8 dst_sel:WORD_1 dst_unused:UNUSED_PAD src0_sel:DWORD
	v_cvt_i32_f32_e32 v9, v9
	v_lshlrev_b32_e32 v3, 8, v3
	v_perm_b32 v2, v5, v2, s12
	v_lshlrev_b32_e32 v5, 8, v7
	v_and_b32_e32 v4, 0xff0000, v4
	v_and_b32_e32 v7, 0xff0000, v8
	v_perm_b32 v6, v9, v6, s12
	v_and_b32_e32 v3, 0xff00, v3
	v_and_b32_e32 v5, 0xff00, v5
	v_or3_b32 v2, v2, v3, v4
	v_or3_b32 v3, v6, v5, v7
	global_store_dwordx2 v[26:27], v[2:3], off offset:-768
	global_load_dwordx4 v[2:5], v[10:11], off offset:2048
	s_nop 0
	global_load_dwordx4 v[6:9], v[10:11], off offset:2064
	s_waitcnt vmcnt(1)
	v_mul_f32_e32 v2, v2, v76
	v_mul_f32_e32 v3, v3, v77
	v_mul_f32_e32 v5, v5, v79
	s_waitcnt vmcnt(0)
	v_mul_f32_e32 v7, v7, v81
	v_mul_f32_e32 v4, v4, v78
	v_mul_f32_e32 v6, v6, v80
	v_mul_f32_e32 v8, v8, v82
	v_mul_f32_e32 v9, v9, v83
	v_med3_f32 v2, v2, s11, v34
	v_med3_f32 v3, v3, s11, v34
	v_med3_f32 v5, v5, s11, v34
	v_med3_f32 v7, v7, s11, v34
	v_med3_f32 v4, v4, s11, v34
	v_med3_f32 v6, v6, s11, v34
	v_med3_f32 v8, v8, s11, v34
	v_med3_f32 v9, v9, s11, v34
	v_rndne_f32_e32 v2, v2
	v_rndne_f32_e32 v3, v3
	v_rndne_f32_e32 v5, v5
	v_rndne_f32_e32 v7, v7
	v_rndne_f32_e32 v4, v4
	v_rndne_f32_e32 v6, v6
	v_rndne_f32_e32 v8, v8
	v_rndne_f32_e32 v9, v9
	v_cvt_i32_f32_e32 v2, v2
	v_cvt_i32_f32_e32 v3, v3
	v_cvt_i32_f32_e32 v5, v5
	v_cvt_i32_f32_e32 v7, v7
	v_cvt_i32_f32_sdwa v4, v4 dst_sel:WORD_1 dst_unused:UNUSED_PAD src0_sel:DWORD
	v_cvt_i32_f32_e32 v6, v6
	v_cvt_i32_f32_sdwa v8, v8 dst_sel:WORD_1 dst_unused:UNUSED_PAD src0_sel:DWORD
	v_cvt_i32_f32_e32 v9, v9
	v_lshlrev_b32_e32 v3, 8, v3
	v_perm_b32 v2, v5, v2, s12
	v_lshlrev_b32_e32 v5, 8, v7
	v_and_b32_e32 v4, 0xff0000, v4
	v_and_b32_e32 v7, 0xff0000, v8
	v_perm_b32 v6, v9, v6, s12
	v_and_b32_e32 v3, 0xff00, v3
	v_and_b32_e32 v5, 0xff00, v5
	v_or3_b32 v2, v2, v3, v4
	v_or3_b32 v3, v6, v5, v7
	global_store_dwordx2 v[26:27], v[2:3], off offset:-512
	global_load_dwordx4 v[2:5], v[14:15], off
	s_nop 0
	global_load_dwordx4 v[6:9], v[14:15], off offset:16
	s_waitcnt vmcnt(1)
	v_mul_f32_e32 v2, v2, v84
	v_mul_f32_e32 v3, v3, v85
	v_mul_f32_e32 v5, v5, v87
	s_waitcnt vmcnt(0)
	v_mul_f32_e32 v7, v7, v89
	v_mul_f32_e32 v4, v4, v86
	v_mul_f32_e32 v6, v6, v88
	v_mul_f32_e32 v8, v8, v90
	v_mul_f32_e32 v9, v9, v91
	v_med3_f32 v2, v2, s11, v34
	v_med3_f32 v3, v3, s11, v34
	v_med3_f32 v5, v5, s11, v34
	v_med3_f32 v7, v7, s11, v34
	v_med3_f32 v4, v4, s11, v34
	v_med3_f32 v6, v6, s11, v34
	v_med3_f32 v8, v8, s11, v34
	v_med3_f32 v9, v9, s11, v34
	v_rndne_f32_e32 v2, v2
	v_rndne_f32_e32 v3, v3
	v_rndne_f32_e32 v5, v5
	v_rndne_f32_e32 v7, v7
	v_rndne_f32_e32 v4, v4
	v_rndne_f32_e32 v6, v6
	v_rndne_f32_e32 v8, v8
	v_rndne_f32_e32 v9, v9
	v_cvt_i32_f32_e32 v2, v2
	v_cvt_i32_f32_e32 v3, v3
	v_cvt_i32_f32_e32 v5, v5
	v_cvt_i32_f32_e32 v7, v7
	v_cvt_i32_f32_sdwa v4, v4 dst_sel:WORD_1 dst_unused:UNUSED_PAD src0_sel:DWORD
	v_cvt_i32_f32_e32 v6, v6
	v_cvt_i32_f32_sdwa v8, v8 dst_sel:WORD_1 dst_unused:UNUSED_PAD src0_sel:DWORD
	v_cvt_i32_f32_e32 v9, v9
	v_lshlrev_b32_e32 v3, 8, v3
	v_perm_b32 v2, v5, v2, s12
	v_lshlrev_b32_e32 v5, 8, v7
	v_and_b32_e32 v4, 0xff0000, v4
	v_and_b32_e32 v7, 0xff0000, v8
	v_perm_b32 v6, v9, v6, s12
	v_and_b32_e32 v3, 0xff00, v3
	v_and_b32_e32 v5, 0xff00, v5
	v_or3_b32 v2, v2, v3, v4
	v_or3_b32 v3, v6, v5, v7
	global_store_dwordx2 v[26:27], v[2:3], off offset:-256
	global_load_dwordx4 v[2:5], v[16:17], off
	s_nop 0
	global_load_dwordx4 v[6:9], v[16:17], off offset:16
	s_waitcnt vmcnt(1)
	v_mul_f32_e32 v2, v2, v92
	v_mul_f32_e32 v3, v3, v52
	v_mul_f32_e32 v5, v5, v53
	s_waitcnt vmcnt(0)
	v_mul_f32_e32 v7, v7, v54
	v_mul_f32_e32 v4, v4, v93
	v_mul_f32_e32 v6, v6, v94
	v_mul_f32_e32 v8, v8, v95
	v_mul_f32_e32 v9, v9, v55
	v_med3_f32 v2, v2, s11, v34
	v_med3_f32 v3, v3, s11, v34
	v_med3_f32 v5, v5, s11, v34
	v_med3_f32 v7, v7, s11, v34
	v_med3_f32 v4, v4, s11, v34
	v_med3_f32 v6, v6, s11, v34
	v_med3_f32 v8, v8, s11, v34
	v_med3_f32 v9, v9, s11, v34
	v_rndne_f32_e32 v2, v2
	v_rndne_f32_e32 v3, v3
	v_rndne_f32_e32 v5, v5
	v_rndne_f32_e32 v7, v7
	v_rndne_f32_e32 v4, v4
	v_rndne_f32_e32 v6, v6
	v_rndne_f32_e32 v8, v8
	v_rndne_f32_e32 v9, v9
	v_cvt_i32_f32_e32 v2, v2
	v_cvt_i32_f32_e32 v3, v3
	v_cvt_i32_f32_e32 v5, v5
	v_cvt_i32_f32_e32 v7, v7
	v_cvt_i32_f32_sdwa v4, v4 dst_sel:WORD_1 dst_unused:UNUSED_PAD src0_sel:DWORD
	v_cvt_i32_f32_e32 v6, v6
	v_cvt_i32_f32_sdwa v8, v8 dst_sel:WORD_1 dst_unused:UNUSED_PAD src0_sel:DWORD
	v_cvt_i32_f32_e32 v9, v9
	v_lshlrev_b32_e32 v3, 8, v3
	v_perm_b32 v2, v5, v2, s12
	v_lshlrev_b32_e32 v5, 8, v7
	v_and_b32_e32 v4, 0xff0000, v4
	v_and_b32_e32 v7, 0xff0000, v8
	v_perm_b32 v6, v9, v6, s12
	v_and_b32_e32 v3, 0xff00, v3
	v_and_b32_e32 v5, 0xff00, v5
	v_or3_b32 v2, v2, v3, v4
	v_or3_b32 v3, v6, v5, v7
	global_store_dwordx2 v[26:27], v[2:3], off
	global_load_dwordx4 v[2:5], v[18:19], off
	s_nop 0
	global_load_dwordx4 v[6:9], v[18:19], off offset:16
	s_waitcnt vmcnt(1)
	v_mul_f32_e32 v2, v2, v96
	v_mul_f32_e32 v3, v3, v56
	v_mul_f32_e32 v5, v5, v57
	s_waitcnt vmcnt(0)
	v_mul_f32_e32 v7, v7, v58
	v_mul_f32_e32 v4, v4, v97
	v_mul_f32_e32 v6, v6, v98
	v_mul_f32_e32 v8, v8, v99
	v_mul_f32_e32 v9, v9, v59
	v_med3_f32 v2, v2, s11, v34
	v_med3_f32 v3, v3, s11, v34
	v_med3_f32 v5, v5, s11, v34
	v_med3_f32 v7, v7, s11, v34
	v_med3_f32 v4, v4, s11, v34
	v_med3_f32 v6, v6, s11, v34
	v_med3_f32 v8, v8, s11, v34
	v_med3_f32 v9, v9, s11, v34
	v_rndne_f32_e32 v2, v2
	v_rndne_f32_e32 v3, v3
	v_rndne_f32_e32 v5, v5
	v_rndne_f32_e32 v7, v7
	v_rndne_f32_e32 v4, v4
	v_rndne_f32_e32 v6, v6
	v_rndne_f32_e32 v8, v8
	v_rndne_f32_e32 v9, v9
	v_cvt_i32_f32_e32 v2, v2
	v_cvt_i32_f32_e32 v3, v3
	v_cvt_i32_f32_e32 v5, v5
	v_cvt_i32_f32_e32 v7, v7
	v_cvt_i32_f32_sdwa v4, v4 dst_sel:WORD_1 dst_unused:UNUSED_PAD src0_sel:DWORD
	v_cvt_i32_f32_e32 v6, v6
	v_cvt_i32_f32_sdwa v8, v8 dst_sel:WORD_1 dst_unused:UNUSED_PAD src0_sel:DWORD
	v_cvt_i32_f32_e32 v9, v9
	v_lshlrev_b32_e32 v3, 8, v3
	v_perm_b32 v2, v5, v2, s12
	v_lshlrev_b32_e32 v5, 8, v7
	v_and_b32_e32 v4, 0xff0000, v4
	v_and_b32_e32 v7, 0xff0000, v8
	v_perm_b32 v6, v9, v6, s12
	v_and_b32_e32 v3, 0xff00, v3
	v_and_b32_e32 v5, 0xff00, v5
	v_or3_b32 v2, v2, v3, v4
	v_or3_b32 v3, v6, v5, v7
	global_store_dwordx2 v[26:27], v[2:3], off offset:256
	global_load_dwordx4 v[2:5], v[20:21], off
	s_nop 0
	global_load_dwordx4 v[6:9], v[20:21], off offset:16
	s_waitcnt vmcnt(1)
	v_mul_f32_e32 v2, v2, v51
	v_mul_f32_e32 v3, v3, v50
	v_mul_f32_e32 v5, v5, v47
	s_waitcnt vmcnt(0)
	v_mul_f32_e32 v7, v7, v45
	v_mul_f32_e32 v4, v4, v48
	v_mul_f32_e32 v6, v6, v46
	v_mul_f32_e32 v8, v8, v44
	v_mul_f32_e32 v9, v9, v43
	v_med3_f32 v2, v2, s11, v34
	v_med3_f32 v3, v3, s11, v34
	v_med3_f32 v5, v5, s11, v34
	v_med3_f32 v7, v7, s11, v34
	v_med3_f32 v4, v4, s11, v34
	v_med3_f32 v6, v6, s11, v34
	v_med3_f32 v8, v8, s11, v34
	v_med3_f32 v9, v9, s11, v34
	v_rndne_f32_e32 v2, v2
	v_rndne_f32_e32 v3, v3
	v_rndne_f32_e32 v5, v5
	v_rndne_f32_e32 v7, v7
	v_rndne_f32_e32 v4, v4
	v_rndne_f32_e32 v6, v6
	v_rndne_f32_e32 v8, v8
	v_rndne_f32_e32 v9, v9
	v_cvt_i32_f32_e32 v2, v2
	v_cvt_i32_f32_e32 v3, v3
	v_cvt_i32_f32_e32 v5, v5
	v_cvt_i32_f32_e32 v7, v7
	v_cvt_i32_f32_sdwa v4, v4 dst_sel:WORD_1 dst_unused:UNUSED_PAD src0_sel:DWORD
	v_cvt_i32_f32_e32 v6, v6
	v_cvt_i32_f32_sdwa v8, v8 dst_sel:WORD_1 dst_unused:UNUSED_PAD src0_sel:DWORD
	v_cvt_i32_f32_e32 v9, v9
	v_lshlrev_b32_e32 v3, 8, v3
	v_perm_b32 v2, v5, v2, s12
	v_lshlrev_b32_e32 v5, 8, v7
	v_and_b32_e32 v4, 0xff0000, v4
	v_and_b32_e32 v7, 0xff0000, v8
	v_perm_b32 v6, v9, v6, s12
	v_and_b32_e32 v3, 0xff00, v3
	v_and_b32_e32 v5, 0xff00, v5
	v_or3_b32 v2, v2, v3, v4
	v_or3_b32 v3, v6, v5, v7
	global_store_dwordx2 v[26:27], v[2:3], off offset:512
	global_load_dwordx4 v[2:5], v[22:23], off
	s_nop 0
	global_load_dwordx4 v[6:9], v[22:23], off offset:16
	s_waitcnt vmcnt(1)
	v_mul_f32_e32 v2, v2, v35
	v_mul_f32_e32 v3, v3, v36
	v_mul_f32_e32 v5, v5, v38
	s_waitcnt vmcnt(0)
	v_mul_f32_e32 v7, v7, v40
	v_mul_f32_e32 v4, v4, v37
	v_mul_f32_e32 v6, v6, v39
	v_mul_f32_e32 v8, v8, v41
	v_mul_f32_e32 v9, v9, v42
	v_med3_f32 v2, v2, s11, v34
	v_med3_f32 v3, v3, s11, v34
	v_med3_f32 v5, v5, s11, v34
	v_med3_f32 v7, v7, s11, v34
	v_med3_f32 v4, v4, s11, v34
	v_med3_f32 v6, v6, s11, v34
	v_med3_f32 v8, v8, s11, v34
	v_med3_f32 v9, v9, s11, v34
	v_rndne_f32_e32 v2, v2
	v_rndne_f32_e32 v3, v3
	v_rndne_f32_e32 v5, v5
	v_rndne_f32_e32 v7, v7
	v_rndne_f32_e32 v4, v4
	v_rndne_f32_e32 v6, v6
	v_rndne_f32_e32 v8, v8
	v_rndne_f32_e32 v9, v9
	v_cvt_i32_f32_e32 v2, v2
	v_cvt_i32_f32_e32 v3, v3
	v_cvt_i32_f32_e32 v5, v5
	v_cvt_i32_f32_e32 v7, v7
	v_cvt_i32_f32_sdwa v4, v4 dst_sel:WORD_1 dst_unused:UNUSED_PAD src0_sel:DWORD
	v_cvt_i32_f32_e32 v6, v6
	v_cvt_i32_f32_sdwa v8, v8 dst_sel:WORD_1 dst_unused:UNUSED_PAD src0_sel:DWORD
	v_cvt_i32_f32_e32 v9, v9
	v_lshlrev_b32_e32 v3, 8, v3
	v_perm_b32 v2, v5, v2, s12
	v_lshlrev_b32_e32 v5, 8, v7
	v_and_b32_e32 v4, 0xff0000, v4
	v_and_b32_e32 v7, 0xff0000, v8
	v_perm_b32 v6, v9, v6, s12
	v_and_b32_e32 v3, 0xff00, v3
	v_and_b32_e32 v5, 0xff00, v5
	v_or3_b32 v2, v2, v3, v4
	v_or3_b32 v3, v6, v5, v7
	global_store_dwordx2 v[26:27], v[2:3], off offset:768
	v_lshl_add_u64 v[26:27], v[26:27], 0, s[8:9]
	s_cbranch_scc1 .LBB0_992
	v_readlane_b32 s93, v246, 7

.LBB0_1051:
	s_add_u32 s8, s17, s6
	s_addc_u32 s9, s48, s7
	s_add_u32 s8, s8, 0x32800100
	s_addc_u32 s9, s9, 0
	s_add_u32 s65, s49, s6
	s_addc_u32 s68, s50, s7
	s_add_i32 s69, 0, 0x10000
	s_cmpk_eq_i32 s6, 0xf00
	s_cselect_b32 s41, s5, s9
	s_cselect_b32 s40, s4, s8
	s_cselect_b32 s9, s21, s68
	s_cselect_b32 s8, s20, s65
	s_add_i32 s65, 0, 0x14000
	v_add_u32_e32 v130, s69, v187
	v_add_u32_e32 v134, s65, v187
	ds_read_b128 v[158:161], v130
	ds_read_b128 v[150:153], v130 offset:1024
	ds_read_b128 v[154:157], v130 offset:2048
	ds_read_b128 v[146:149], v130 offset:3072
	ds_read_b128 v[142:145], v134
	ds_read_b128 v[130:133], v134 offset:1024
	ds_read_b128 v[138:141], v134 offset:2048
	ds_read_b128 v[134:137], v134 offset:3072
	v_lshl_add_u64 v[214:215], v[168:169], 0, s[6:7]
	s_add_i32 m0, s43, 0xc000
	ds_read_b128 v[172:175], v188
	ds_read_b128 v[176:179], v188 offset:1024
	ds_read_b128 v[190:193], v188 offset:2048
	ds_read_b128 v[194:197], v188 offset:3072
	ds_read_b128 v[198:201], v188 offset:4096
	ds_read_b128 v[202:205], v188 offset:5120
	ds_read_b128 v[206:209], v188 offset:6144
	ds_read_b128 v[210:213], v188 offset:7168
	global_load_lds_dwordx4 v[214:215], off
	v_lshl_add_u64 v[214:215], v[170:171], 0, s[6:7]
	s_add_i32 m0, s43, 0xe000
	s_nop 0
	global_load_lds_dwordx4 v[214:215], off
	s_waitcnt vmcnt(8)
	s_waitcnt lgkmcnt(0)
	s_barrier
	s_setprio 1
	s_waitcnt lgkmcnt(0)
	v_mfma_i32_16x16x64_i8 v[70:73], v[158:161], v[172:175], v[70:73]
	v_mfma_i32_16x16x64_i8 v[34:37], v[154:157], v[172:175], v[34:37]
	v_mfma_i32_16x16x64_i8 v[102:105], v[158:161], v[190:193], v[102:105]
	v_mfma_i32_16x16x64_i8 v[54:57], v[154:157], v[190:193], v[54:57]
	v_mfma_i32_16x16x64_i8 v[114:117], v[158:161], v[198:201], v[114:117]
	v_mfma_i32_16x16x64_i8 v[86:89], v[154:157], v[198:201], v[86:89]
	v_mfma_i32_16x16x64_i8 v[126:129], v[158:161], v[206:209], v[126:129]
	v_mfma_i32_16x16x64_i8 v[110:113], v[154:157], v[206:209], v[110:113]
	s_nop 0
	v_mfma_i32_16x16x64_i8 v[70:73], v[150:153], v[176:179], v[70:73]
	v_mfma_i32_16x16x64_i8 v[34:37], v[146:149], v[176:179], v[34:37]
	v_mfma_i32_16x16x64_i8 v[102:105], v[150:153], v[194:197], v[102:105]
	v_mfma_i32_16x16x64_i8 v[54:57], v[146:149], v[194:197], v[54:57]
	v_mfma_i32_16x16x64_i8 v[114:117], v[150:153], v[202:205], v[114:117]
	v_mfma_i32_16x16x64_i8 v[86:89], v[146:149], v[202:205], v[86:89]
	v_mfma_i32_16x16x64_i8 v[126:129], v[150:153], v[210:213], v[126:129]
	v_mfma_i32_16x16x64_i8 v[110:113], v[146:149], v[210:213], v[110:113]
	s_setprio 0
	s_setprio 1
	v_mfma_i32_16x16x64_i8 v[18:21], v[142:145], v[172:175], v[18:21]
	v_mfma_i32_16x16x64_i8 v[2:5], v[138:141], v[172:175], v[2:5]
	v_mfma_i32_16x16x64_i8 v[38:41], v[142:145], v[190:193], v[38:41]
	v_mfma_i32_16x16x64_i8 v[6:9], v[138:141], v[190:193], v[6:9]
	v_mfma_i32_16x16x64_i8 v[66:69], v[142:145], v[198:201], v[66:69]
	v_mfma_i32_16x16x64_i8 v[26:29], v[138:141], v[198:201], v[26:29]
	v_mfma_i32_16x16x64_i8 v[90:93], v[142:145], v[206:209], v[90:93]
	v_mfma_i32_16x16x64_i8 v[50:53], v[138:141], v[206:209], v[50:53]
	s_nop 0
	v_mfma_i32_16x16x64_i8 v[18:21], v[130:133], v[176:179], v[18:21]
	v_mfma_i32_16x16x64_i8 v[2:5], v[134:137], v[176:179], v[2:5]
	v_mfma_i32_16x16x64_i8 v[38:41], v[130:133], v[194:197], v[38:41]
	v_mfma_i32_16x16x64_i8 v[6:9], v[134:137], v[194:197], v[6:9]
	v_mfma_i32_16x16x64_i8 v[66:69], v[130:133], v[202:205], v[66:69]
	v_mfma_i32_16x16x64_i8 v[26:29], v[134:137], v[202:205], v[26:29]
	v_mfma_i32_16x16x64_i8 v[90:93], v[130:133], v[210:213], v[90:93]
	v_mfma_i32_16x16x64_i8 v[50:53], v[134:137], v[210:213], v[50:53]
	s_setprio 2
	s_barrier
	s_add_i32 s68, s69, s42
	v_lshl_add_u64 v[172:173], s[8:9], 0, v[162:163]
	s_mov_b32 m0, s68
	ds_read_b128 v[190:193], v188 offset:16384
	ds_read_b128 v[194:197], v188 offset:17408
	ds_read_b128 v[198:201], v188 offset:18432
	ds_read_b128 v[202:205], v188 offset:19456
	ds_read_b128 v[206:209], v188 offset:20480
	ds_read_b128 v[210:213], v188 offset:21504
	ds_read_b128 v[214:217], v188 offset:22528
	ds_read_b128 v[218:221], v188 offset:23552
	global_load_lds_dwordx4 v[172:173], off
	s_add_i32 m0, s68, 0x2000
	s_add_u32 s68, s8, 0x80000
	v_lshl_add_u64 v[174:175], s[8:9], 0, v[166:167]
	s_addc_u32 s69, s9, 0
	s_add_i32 s65, s65, s42
	global_load_lds_dwordx4 v[174:175], off
	v_lshl_add_u64 v[176:177], s[68:69], 0, v[162:163]
	s_mov_b32 m0, s65
	v_lshl_add_u64 v[178:179], s[40:41], 0, v[166:167]
	global_load_lds_dwordx4 v[176:177], off
	v_lshl_add_u64 v[176:177], s[68:69], 0, v[166:167]
	s_add_i32 m0, s65, 0x2000
	s_nop 0
	global_load_lds_dwordx4 v[176:177], off
	v_lshl_add_u64 v[176:177], s[40:41], 0, v[162:163]
	s_mov_b32 m0, s43
	s_nop 0
	global_load_lds_dwordx4 v[176:177], off
	s_mov_b32 m0, s60
	s_nop 0
	global_load_lds_dwordx4 v[178:179], off
	s_waitcnt vmcnt(8)
	s_waitcnt lgkmcnt(0)
	s_barrier
	s_setprio 1
	s_waitcnt lgkmcnt(0)
	v_mfma_i32_16x16x64_i8 v[122:125], v[158:161], v[190:193], v[122:125]
	v_mfma_i32_16x16x64_i8 v[118:121], v[154:157], v[190:193], v[118:121]
	v_mfma_i32_16x16x64_i8 v[98:101], v[158:161], v[198:201], v[98:101]
	v_mfma_i32_16x16x64_i8 v[94:97], v[154:157], v[198:201], v[94:97]
	v_mfma_i32_16x16x64_i8 v[62:65], v[158:161], v[206:209], v[62:65]
	v_mfma_i32_16x16x64_i8 v[58:61], v[154:157], v[206:209], v[58:61]
	v_mfma_i32_16x16x64_i8 v[30:33], v[158:161], v[214:217], v[30:33]
	v_mfma_i32_16x16x64_i8 v[22:25], v[154:157], v[214:217], v[22:25]
	s_nop 0
	v_mfma_i32_16x16x64_i8 v[122:125], v[150:153], v[194:197], v[122:125]
	v_mfma_i32_16x16x64_i8 v[118:121], v[146:149], v[194:197], v[118:121]
	v_mfma_i32_16x16x64_i8 v[98:101], v[150:153], v[202:205], v[98:101]
	v_mfma_i32_16x16x64_i8 v[94:97], v[146:149], v[202:205], v[94:97]
	v_mfma_i32_16x16x64_i8 v[62:65], v[150:153], v[210:213], v[62:65]
	v_mfma_i32_16x16x64_i8 v[58:61], v[146:149], v[210:213], v[58:61]
	v_mfma_i32_16x16x64_i8 v[30:33], v[150:153], v[218:221], v[30:33]
	v_mfma_i32_16x16x64_i8 v[22:25], v[146:149], v[218:221], v[22:25]
	s_setprio 0
	s_setprio 1
	v_mfma_i32_16x16x64_i8 v[106:109], v[142:145], v[190:193], v[106:109]
	v_mfma_i32_16x16x64_i8 v[82:85], v[138:141], v[190:193], v[82:85]
	v_mfma_i32_16x16x64_i8 v[78:81], v[142:145], v[198:201], v[78:81]
	v_mfma_i32_16x16x64_i8 v[74:77], v[138:141], v[198:201], v[74:77]
	v_mfma_i32_16x16x64_i8 v[46:49], v[142:145], v[206:209], v[46:49]
	v_mfma_i32_16x16x64_i8 v[42:45], v[138:141], v[206:209], v[42:45]
	v_mfma_i32_16x16x64_i8 v[14:17], v[142:145], v[214:217], v[14:17]
	v_mfma_i32_16x16x64_i8 v[10:13], v[138:141], v[214:217], v[10:13]
	s_nop 0
	v_mfma_i32_16x16x64_i8 v[106:109], v[130:133], v[194:197], v[106:109]
	v_mfma_i32_16x16x64_i8 v[82:85], v[134:137], v[194:197], v[82:85]
	v_mfma_i32_16x16x64_i8 v[78:81], v[130:133], v[202:205], v[78:81]
	v_mfma_i32_16x16x64_i8 v[74:77], v[134:137], v[202:205], v[74:77]
	v_mfma_i32_16x16x64_i8 v[46:49], v[130:133], v[210:213], v[46:49]
	v_mfma_i32_16x16x64_i8 v[42:45], v[134:137], v[210:213], v[42:45]
	v_mfma_i32_16x16x64_i8 v[14:17], v[130:133], v[218:221], v[14:17]
	v_mfma_i32_16x16x64_i8 v[10:13], v[134:137], v[218:221], v[10:13]
	s_setprio 2
	s_barrier
	s_add_i32 s65, 0, 0x18000
	s_add_i32 s68, 0, 0x1c000
	v_add_u32_e32 v142, s65, v187
	v_add_u32_e32 v158, s68, v187
	ds_read_b128 v[130:133], v142
	ds_read_b128 v[134:137], v142 offset:1024
	ds_read_b128 v[138:141], v142 offset:2048
	ds_read_b128 v[142:145], v142 offset:3072
	ds_read_b128 v[146:149], v158
	ds_read_b128 v[150:153], v158 offset:1024
	ds_read_b128 v[154:157], v158 offset:2048
	ds_read_b128 v[158:161], v158 offset:3072
	s_add_u32 s40, s40, 0x80000
	s_addc_u32 s41, s41, 0
	s_mov_b32 m0, s61
	v_lshl_add_u64 v[222:223], s[40:41], 0, v[162:163]
	ds_read_b128 v[190:193], v188 offset:32768
	ds_read_b128 v[194:197], v188 offset:33792
	ds_read_b128 v[198:201], v188 offset:34816
	ds_read_b128 v[202:205], v188 offset:35840
	ds_read_b128 v[206:209], v188 offset:36864
	ds_read_b128 v[210:213], v188 offset:37888
	ds_read_b128 v[214:217], v188 offset:38912
	ds_read_b128 v[218:221], v188 offset:39936
	global_load_lds_dwordx4 v[222:223], off
	v_lshl_add_u64 v[222:223], s[40:41], 0, v[166:167]
	s_mov_b32 m0, s62
	s_nop 0
	global_load_lds_dwordx4 v[222:223], off
	s_waitcnt vmcnt(8)
	s_waitcnt lgkmcnt(0)
	s_barrier
	s_setprio 1
	s_waitcnt lgkmcnt(0)
	v_mfma_i32_16x16x64_i8 v[70:73], v[130:133], v[190:193], v[70:73]
	v_mfma_i32_16x16x64_i8 v[34:37], v[138:141], v[190:193], v[34:37]
	v_mfma_i32_16x16x64_i8 v[102:105], v[130:133], v[198:201], v[102:105]
	v_mfma_i32_16x16x64_i8 v[54:57], v[138:141], v[198:201], v[54:57]
	v_mfma_i32_16x16x64_i8 v[114:117], v[130:133], v[206:209], v[114:117]
	v_mfma_i32_16x16x64_i8 v[86:89], v[138:141], v[206:209], v[86:89]
	v_mfma_i32_16x16x64_i8 v[126:129], v[130:133], v[214:217], v[126:129]
	v_mfma_i32_16x16x64_i8 v[110:113], v[138:141], v[214:217], v[110:113]
	s_nop 0
	v_mfma_i32_16x16x64_i8 v[70:73], v[134:137], v[194:197], v[70:73]
	v_mfma_i32_16x16x64_i8 v[34:37], v[142:145], v[194:197], v[34:37]
	v_mfma_i32_16x16x64_i8 v[102:105], v[134:137], v[202:205], v[102:105]
	v_mfma_i32_16x16x64_i8 v[54:57], v[142:145], v[202:205], v[54:57]
	v_mfma_i32_16x16x64_i8 v[114:117], v[134:137], v[210:213], v[114:117]
	v_mfma_i32_16x16x64_i8 v[86:89], v[142:145], v[210:213], v[86:89]
	v_mfma_i32_16x16x64_i8 v[126:129], v[134:137], v[218:221], v[126:129]
	v_mfma_i32_16x16x64_i8 v[110:113], v[142:145], v[218:221], v[110:113]
	s_setprio 0
	s_setprio 1
	v_mfma_i32_16x16x64_i8 v[18:21], v[146:149], v[190:193], v[18:21]
	v_mfma_i32_16x16x64_i8 v[2:5], v[154:157], v[190:193], v[2:5]
	v_mfma_i32_16x16x64_i8 v[38:41], v[146:149], v[198:201], v[38:41]
	v_mfma_i32_16x16x64_i8 v[6:9], v[154:157], v[198:201], v[6:9]
	v_mfma_i32_16x16x64_i8 v[66:69], v[146:149], v[206:209], v[66:69]
	v_mfma_i32_16x16x64_i8 v[26:29], v[154:157], v[206:209], v[26:29]
	v_mfma_i32_16x16x64_i8 v[90:93], v[146:149], v[214:217], v[90:93]
	v_mfma_i32_16x16x64_i8 v[50:53], v[154:157], v[214:217], v[50:53]
	s_nop 0
	v_mfma_i32_16x16x64_i8 v[18:21], v[150:153], v[194:197], v[18:21]
	v_mfma_i32_16x16x64_i8 v[2:5], v[158:161], v[194:197], v[2:5]
	v_mfma_i32_16x16x64_i8 v[38:41], v[150:153], v[202:205], v[38:41]
	v_mfma_i32_16x16x64_i8 v[6:9], v[158:161], v[202:205], v[6:9]
	v_mfma_i32_16x16x64_i8 v[66:69], v[150:153], v[210:213], v[66:69]
	v_mfma_i32_16x16x64_i8 v[26:29], v[158:161], v[210:213], v[26:29]
	v_mfma_i32_16x16x64_i8 v[90:93], v[150:153], v[218:221], v[90:93]
	v_mfma_i32_16x16x64_i8 v[50:53], v[158:161], v[218:221], v[50:53]
	s_setprio 2
	s_barrier
	s_add_i32 s40, s65, s42
	v_lshl_add_u64 v[172:173], v[172:173], 0, s[36:37]
	s_mov_b32 m0, s40
	ds_read_b128 v[190:193], v188 offset:49152
	ds_read_b128 v[194:197], v188 offset:50176
	ds_read_b128 v[198:201], v188 offset:51200
	ds_read_b128 v[202:205], v188 offset:52224
	ds_read_b128 v[206:209], v188 offset:53248
	ds_read_b128 v[210:213], v188 offset:54272
	ds_read_b128 v[214:217], v188 offset:55296
	ds_read_b128 v[218:221], v188 offset:56320
	global_load_lds_dwordx4 v[172:173], off
	s_add_i32 m0, s40, 0x2000
	s_add_u32 s8, s8, 0x80080
	v_lshl_add_u64 v[172:173], v[174:175], 0, s[36:37]
	s_addc_u32 s9, s9, 0
	s_add_i32 s40, s68, s42
	global_load_lds_dwordx4 v[172:173], off
	v_lshl_add_u64 v[172:173], s[8:9], 0, v[162:163]
	s_mov_b32 m0, s40
	s_nop 0
	global_load_lds_dwordx4 v[172:173], off
	v_lshl_add_u64 v[172:173], s[8:9], 0, v[166:167]
	s_add_i32 m0, s40, 0x2000
	s_nop 0
	global_load_lds_dwordx4 v[172:173], off
	v_lshl_add_u64 v[172:173], v[176:177], 0, s[36:37]
	s_mov_b32 m0, s66
	s_nop 0
	global_load_lds_dwordx4 v[172:173], off
	v_lshl_add_u64 v[172:173], v[178:179], 0, s[36:37]
	s_mov_b32 m0, s67
	s_nop 0
	global_load_lds_dwordx4 v[172:173], off
	s_waitcnt vmcnt(8)
	s_waitcnt lgkmcnt(0)
	s_barrier
	s_setprio 1
	s_waitcnt lgkmcnt(0)
	v_mfma_i32_16x16x64_i8 v[122:125], v[130:133], v[190:193], v[122:125]
	v_mfma_i32_16x16x64_i8 v[118:121], v[138:141], v[190:193], v[118:121]
	v_mfma_i32_16x16x64_i8 v[98:101], v[130:133], v[198:201], v[98:101]
	v_mfma_i32_16x16x64_i8 v[94:97], v[138:141], v[198:201], v[94:97]
	v_mfma_i32_16x16x64_i8 v[62:65], v[130:133], v[206:209], v[62:65]
	v_mfma_i32_16x16x64_i8 v[58:61], v[138:141], v[206:209], v[58:61]
	v_mfma_i32_16x16x64_i8 v[30:33], v[130:133], v[214:217], v[30:33]
	v_mfma_i32_16x16x64_i8 v[22:25], v[138:141], v[214:217], v[22:25]
	s_nop 0
	v_mfma_i32_16x16x64_i8 v[122:125], v[134:137], v[194:197], v[122:125]
	v_mfma_i32_16x16x64_i8 v[118:121], v[142:145], v[194:197], v[118:121]
	v_mfma_i32_16x16x64_i8 v[98:101], v[134:137], v[202:205], v[98:101]
	v_mfma_i32_16x16x64_i8 v[94:97], v[142:145], v[202:205], v[94:97]
	v_mfma_i32_16x16x64_i8 v[62:65], v[134:137], v[210:213], v[62:65]
	v_mfma_i32_16x16x64_i8 v[58:61], v[142:145], v[210:213], v[58:61]
	v_mfma_i32_16x16x64_i8 v[30:33], v[134:137], v[218:221], v[30:33]
	v_mfma_i32_16x16x64_i8 v[22:25], v[142:145], v[218:221], v[22:25]
	s_setprio 0
	s_setprio 1
	v_mfma_i32_16x16x64_i8 v[106:109], v[146:149], v[190:193], v[106:109]
	v_mfma_i32_16x16x64_i8 v[82:85], v[154:157], v[190:193], v[82:85]
	v_mfma_i32_16x16x64_i8 v[78:81], v[146:149], v[198:201], v[78:81]
	v_mfma_i32_16x16x64_i8 v[74:77], v[154:157], v[198:201], v[74:77]
	v_mfma_i32_16x16x64_i8 v[46:49], v[146:149], v[206:209], v[46:49]
	v_mfma_i32_16x16x64_i8 v[42:45], v[154:157], v[206:209], v[42:45]
	v_mfma_i32_16x16x64_i8 v[14:17], v[146:149], v[214:217], v[14:17]
	v_mfma_i32_16x16x64_i8 v[10:13], v[154:157], v[214:217], v[10:13]
	s_nop 0
	v_mfma_i32_16x16x64_i8 v[106:109], v[150:153], v[194:197], v[106:109]
	v_mfma_i32_16x16x64_i8 v[82:85], v[158:161], v[194:197], v[82:85]
	v_mfma_i32_16x16x64_i8 v[78:81], v[150:153], v[202:205], v[78:81]
	v_mfma_i32_16x16x64_i8 v[74:77], v[158:161], v[202:205], v[74:77]
	v_mfma_i32_16x16x64_i8 v[46:49], v[150:153], v[210:213], v[46:49]
	v_mfma_i32_16x16x64_i8 v[42:45], v[158:161], v[210:213], v[42:45]
	v_mfma_i32_16x16x64_i8 v[14:17], v[150:153], v[218:221], v[14:17]
	v_mfma_i32_16x16x64_i8 v[10:13], v[158:161], v[218:221], v[10:13]
	s_setprio 2
	s_barrier
	s_add_i32 s64, s64, 2
	s_add_u32 s6, s6, 0x100
	s_addc_u32 s7, s7, 0
	s_cmp_gt_u32 s64, 29
	s_cbranch_scc0 .LBB0_1051
	s_waitcnt vmcnt(0)
	s_cmpk_lt_u32 s59, 0x100
	s_cbranch_scc0 .LBB0_1054
	s_barrier
.LBB0_1054:
	s_lshl_b32 s60, s14, 8
	s_add_i32 s63, s63, s60
	v_lshrrev_b32_e32 v130, 2, v185
	v_or_b32_e32 v132, s63, v186
	v_and_b32_e32 v135, 12, v130
	s_lshl_b32 s61, s15, 5
	v_or_b32_e32 v130, s45, v135
	v_ashrrev_i32_e32 v133, 31, v132
	v_or_b32_e32 v140, s61, v130
	v_lshlrev_b64 v[130:131], 13, v[132:133]
	v_lshl_add_u64 v[130:131], s[56:57], 0, v[130:131]
	v_readlane_b32 s6, v246, 3
	v_lshlrev_b32_e32 v162, 1, v140
	v_lshlrev_b32_e32 v134, 2, v140
	v_readlane_b32 s7, v246, 4
	v_lshl_add_u64 v[130:131], v[130:131], 0, v[162:163]
	s_barrier
	v_cvt_f32_i32_e32 v71, v71
	v_cvt_f32_i32_e32 v70, v70
	v_cvt_f32_i32_e32 v73, v73
	global_load_dwordx4 v[136:139], v134, s[6:7]
	global_load_dwordx4 v[140:143], v134, s[6:7] offset:64
	global_load_dwordx2 v[144:145], v[130:131], off
	global_load_dwordx2 v[146:147], v[130:131], off offset:32
	v_cvt_f32_i32_e32 v72, v72
	v_cvt_f32_i32_e32 v35, v35
	v_cvt_f32_i32_e32 v34, v34
	v_cvt_f32_i32_e32 v37, v37
	v_cvt_f32_i32_e32 v36, v36
	v_cvt_f32_i32_e32 v19, v19
	v_cvt_f32_i32_e32 v18, v18
	v_cvt_f32_i32_e32 v21, v21
	v_cvt_f32_i32_e32 v20, v20
	v_cvt_f32_i32_e32 v3, v3
	v_cvt_f32_i32_e32 v2, v2
	v_cvt_f32_i32_e32 v5, v5
	v_cvt_f32_i32_e32 v4, v4
	v_cvt_f32_i32_e32 v103, v103
	v_cvt_f32_i32_e32 v102, v102
	v_cvt_f32_i32_e32 v105, v105
	v_cvt_f32_i32_e32 v104, v104
	v_cvt_f32_i32_e32 v55, v55
	v_cvt_f32_i32_e32 v54, v54
	v_cvt_f32_i32_e32 v57, v57
	v_cvt_f32_i32_e32 v56, v56
	v_cvt_f32_i32_e32 v39, v39
	v_cvt_f32_i32_e32 v38, v38
	v_cvt_f32_i32_e32 v41, v41
	v_cvt_f32_i32_e32 v40, v40
	v_cvt_f32_i32_e32 v7, v7
	v_cvt_f32_i32_e32 v6, v6
	v_cvt_f32_i32_e32 v9, v9
	v_cvt_f32_i32_e32 v8, v8
	v_cvt_f32_i32_e32 v115, v115
	v_cvt_f32_i32_e32 v114, v114
	v_cvt_f32_i32_e32 v117, v117
	v_cvt_f32_i32_e32 v116, v116
	v_cvt_f32_i32_e32 v87, v87
	v_cvt_f32_i32_e32 v86, v86
	v_cvt_f32_i32_e32 v89, v89
	v_cvt_f32_i32_e32 v88, v88
	v_cvt_f32_i32_e32 v67, v67
	v_cvt_f32_i32_e32 v66, v66
	v_cvt_f32_i32_e32 v69, v69
	v_cvt_f32_i32_e32 v68, v68
	v_cvt_f32_i32_e32 v27, v27
	v_cvt_f32_i32_e32 v26, v26
	v_cvt_f32_i32_e32 v29, v29
	v_cvt_f32_i32_e32 v28, v28
	v_cvt_f32_i32_e32 v127, v127
	v_cvt_f32_i32_e32 v126, v126
	v_cvt_f32_i32_e32 v129, v129
	v_cvt_f32_i32_e32 v128, v128
	v_cvt_f32_i32_e32 v111, v111
	v_cvt_f32_i32_e32 v110, v110
	v_cvt_f32_i32_e32 v113, v113
	v_cvt_f32_i32_e32 v112, v112
	v_cvt_f32_i32_e32 v91, v91
	v_cvt_f32_i32_e32 v90, v90
	v_cvt_f32_i32_e32 v93, v93
	v_cvt_f32_i32_e32 v92, v92
	v_cvt_f32_i32_e32 v51, v51
	v_cvt_f32_i32_e32 v50, v50
	v_cvt_f32_i32_e32 v53, v53
	v_cvt_f32_i32_e32 v52, v52
	s_mov_b32 s4, 0x100000
	v_cvt_f32_i32_e32 v123, v123
	v_cvt_f32_i32_e32 v122, v122
	v_cvt_f32_i32_e32 v125, v125
	v_cvt_f32_i32_e32 v124, v124
	v_cvt_f32_i32_e32 v119, v119
	v_cvt_f32_i32_e32 v118, v118
	v_cvt_f32_i32_e32 v121, v121
	v_cvt_f32_i32_e32 v120, v120
	v_cvt_f32_i32_e32 v107, v107
	v_cvt_f32_i32_e32 v106, v106
	v_cvt_f32_i32_e32 v109, v109
	v_cvt_f32_i32_e32 v108, v108
	v_cvt_f32_i32_e32 v83, v83
	v_cvt_f32_i32_e32 v82, v82
	v_cvt_f32_i32_e32 v85, v85
	s_waitcnt vmcnt(0)
	v_pk_mul_f32 v[138:139], v[138:139], s[38:39] op_sel_hi:[1,0]
	v_pk_mul_f32 v[136:137], v[136:137], s[38:39] op_sel_hi:[1,0]
	v_pk_mul_f32 v[142:143], v[142:143], s[38:39] op_sel_hi:[1,0]
	v_pk_mul_f32 v[140:141], v[140:141], s[38:39] op_sel_hi:[1,0]
	v_lshlrev_b32_e32 v148, 16, v144
	v_and_b32_e32 v149, 0xffff0000, v144
	v_lshlrev_b32_e32 v144, 16, v145
	v_and_b32_e32 v145, 0xffff0000, v145
	v_lshlrev_b32_e32 v150, 16, v146
	v_and_b32_e32 v151, 0xffff0000, v146
	v_lshlrev_b32_e32 v146, 16, v147
	v_and_b32_e32 v147, 0xffff0000, v147
	v_pk_fma_f32 v[72:73], v[138:139], v[72:73], v[144:145]
	v_pk_fma_f32 v[70:71], v[136:137], v[70:71], v[148:149]
	v_pk_fma_f32 v[36:37], v[142:143], v[36:37], v[146:147]
	v_pk_fma_f32 v[34:35], v[140:141], v[34:35], v[150:151]
	v_cvt_pk_bf16_f32 v136, v70, v71
	v_cvt_pk_bf16_f32 v137, v72, v73
	v_or_b32_e32 v148, 16, v132
	v_cvt_pk_bf16_f32 v138, v34, v35
	v_cvt_pk_bf16_f32 v139, v36, v37
	global_store_dwordx2 v[130:131], v[136:137], off
	global_store_dwordx2 v[130:131], v[138:139], off offset:32
	global_load_dwordx2 v[144:145], v[130:131], off offset:256
	global_load_dwordx2 v[146:147], v[130:131], off offset:288
	global_load_dwordx4 v[136:139], v134, s[6:7] offset:512
	global_load_dwordx4 v[140:143], v134, s[6:7] offset:576
	v_ashrrev_i32_e32 v149, 31, v148
	v_lshlrev_b64 v[148:149], 13, v[148:149]
	v_lshl_add_u64 v[148:149], s[56:57], 0, v[148:149]
	v_lshl_add_u64 v[148:149], v[148:149], 0, v[162:163]
	v_cvt_f32_i32_e32 v84, v84
	v_cvt_f32_i32_e32 v99, v99
	v_cvt_f32_i32_e32 v98, v98
	v_cvt_f32_i32_e32 v101, v101
	v_cvt_f32_i32_e32 v100, v100
	v_cvt_f32_i32_e32 v95, v95
	v_cvt_f32_i32_e32 v94, v94
	v_cvt_f32_i32_e32 v97, v97
	v_cvt_f32_i32_e32 v96, v96
	v_cvt_f32_i32_e32 v79, v79
	v_cvt_f32_i32_e32 v78, v78
	v_cvt_f32_i32_e32 v81, v81
	v_cvt_f32_i32_e32 v80, v80
	v_cvt_f32_i32_e32 v75, v75
	v_cvt_f32_i32_e32 v74, v74
	v_cvt_f32_i32_e32 v77, v77
	v_cvt_f32_i32_e32 v76, v76
	v_cvt_f32_i32_e32 v63, v63
	v_cvt_f32_i32_e32 v62, v62
	v_cvt_f32_i32_e32 v65, v65
	v_cvt_f32_i32_e32 v64, v64
	v_cvt_f32_i32_e32 v59, v59
	v_cvt_f32_i32_e32 v58, v58
	v_cvt_f32_i32_e32 v61, v61
	v_cvt_f32_i32_e32 v60, v60
	v_cvt_f32_i32_e32 v47, v47
	v_cvt_f32_i32_e32 v46, v46
	v_cvt_f32_i32_e32 v49, v49
	v_cvt_f32_i32_e32 v48, v48
	v_cvt_f32_i32_e32 v43, v43
	v_cvt_f32_i32_e32 v42, v42
	v_cvt_f32_i32_e32 v45, v45
	v_cvt_f32_i32_e32 v44, v44
	v_cvt_f32_i32_e32 v31, v31
	v_cvt_f32_i32_e32 v30, v30
	v_cvt_f32_i32_e32 v33, v33
	v_cvt_f32_i32_e32 v32, v32
	v_cvt_f32_i32_e32 v23, v23
	v_cvt_f32_i32_e32 v22, v22
	v_cvt_f32_i32_e32 v25, v25
	v_cvt_f32_i32_e32 v24, v24
	v_cvt_f32_i32_e32 v15, v15
	v_cvt_f32_i32_e32 v14, v14
	v_cvt_f32_i32_e32 v17, v17
	v_cvt_f32_i32_e32 v16, v16
	v_cvt_f32_i32_e32 v11, v11
	v_cvt_f32_i32_e32 v10, v10
	v_cvt_f32_i32_e32 v13, v13
	v_cvt_f32_i32_e32 v12, v12
	s_waitcnt vmcnt(3)
	v_lshlrev_b32_e32 v150, 16, v144
	v_and_b32_e32 v151, 0xffff0000, v144
	v_lshlrev_b32_e32 v144, 16, v145
	v_and_b32_e32 v145, 0xffff0000, v145
	s_waitcnt vmcnt(2)
	v_lshlrev_b32_e32 v152, 16, v146
	v_and_b32_e32 v153, 0xffff0000, v146
	v_lshlrev_b32_e32 v146, 16, v147
	v_and_b32_e32 v147, 0xffff0000, v147
	s_waitcnt vmcnt(1)
	v_pk_mul_f32 v[138:139], v[138:139], s[38:39] op_sel_hi:[1,0]
	v_pk_mul_f32 v[136:137], v[136:137], s[38:39] op_sel_hi:[1,0]
	s_waitcnt vmcnt(0)
	v_pk_mul_f32 v[142:143], v[142:143], s[38:39] op_sel_hi:[1,0]
	v_pk_mul_f32 v[140:141], v[140:141], s[38:39] op_sel_hi:[1,0]
	v_pk_fma_f32 v[20:21], v[138:139], v[20:21], v[144:145]
	v_pk_fma_f32 v[18:19], v[136:137], v[18:19], v[150:151]
	v_pk_fma_f32 v[4:5], v[142:143], v[4:5], v[146:147]
	v_pk_fma_f32 v[2:3], v[140:141], v[2:3], v[152:153]
	v_cvt_pk_bf16_f32 v136, v18, v19
	v_cvt_pk_bf16_f32 v137, v20, v21
	s_nop 0
	v_cvt_pk_bf16_f32 v138, v2, v3
	v_cvt_pk_bf16_f32 v139, v4, v5
	global_store_dwordx2 v[130:131], v[136:137], off offset:256
	global_store_dwordx2 v[130:131], v[138:139], off offset:288
	global_load_dwordx2 v[144:145], v[148:149], off
	global_load_dwordx2 v[146:147], v[148:149], off offset:32
	global_load_dwordx4 v[136:139], v134, s[6:7]
	global_load_dwordx4 v[140:143], v134, s[6:7] offset:64
	s_waitcnt vmcnt(3)
	v_lshlrev_b32_e32 v150, 16, v144
	v_and_b32_e32 v151, 0xffff0000, v144
	v_lshlrev_b32_e32 v144, 16, v145
	v_and_b32_e32 v145, 0xffff0000, v145
	s_waitcnt vmcnt(2)
	v_lshlrev_b32_e32 v152, 16, v146
	v_and_b32_e32 v153, 0xffff0000, v146
	v_lshlrev_b32_e32 v146, 16, v147
	v_and_b32_e32 v147, 0xffff0000, v147
	s_waitcnt vmcnt(1)
	v_pk_mul_f32 v[138:139], v[138:139], s[38:39] op_sel_hi:[1,0]
	v_pk_mul_f32 v[136:137], v[136:137], s[38:39] op_sel_hi:[1,0]
	s_waitcnt vmcnt(0)
	v_pk_mul_f32 v[142:143], v[142:143], s[38:39] op_sel_hi:[1,0]
	v_pk_mul_f32 v[140:141], v[140:141], s[38:39] op_sel_hi:[1,0]
	v_pk_fma_f32 v[104:105], v[138:139], v[104:105], v[144:145]
	v_pk_fma_f32 v[102:103], v[136:137], v[102:103], v[150:151]
	v_pk_fma_f32 v[56:57], v[142:143], v[56:57], v[146:147]
	v_pk_fma_f32 v[54:55], v[140:141], v[54:55], v[152:153]
	v_cvt_pk_bf16_f32 v136, v102, v103
	v_cvt_pk_bf16_f32 v137, v104, v105
	v_or_b32_e32 v150, 32, v132
	v_cvt_pk_bf16_f32 v138, v54, v55
	v_cvt_pk_bf16_f32 v139, v56, v57
	global_store_dwordx2 v[148:149], v[136:137], off
	global_store_dwordx2 v[148:149], v[138:139], off offset:32
	global_load_dwordx2 v[144:145], v[148:149], off offset:256
	global_load_dwordx2 v[146:147], v[148:149], off offset:288
	global_load_dwordx4 v[136:139], v134, s[6:7] offset:512
	global_load_dwordx4 v[140:143], v134, s[6:7] offset:576
	v_ashrrev_i32_e32 v151, 31, v150
	v_lshlrev_b64 v[150:151], 13, v[150:151]
	v_lshl_add_u64 v[150:151], s[56:57], 0, v[150:151]
	v_lshl_add_u64 v[150:151], v[150:151], 0, v[162:163]
	v_or_b32_e32 v132, 48, v132
	v_ashrrev_i32_e32 v133, 31, v132
	v_lshlrev_b64 v[132:133], 13, v[132:133]
	v_lshl_add_u64 v[132:133], s[56:57], 0, v[132:133]
	v_lshl_add_u64 v[132:133], v[132:133], 0, v[162:163]
	s_waitcnt vmcnt(3)
	v_lshlrev_b32_e32 v152, 16, v144
	v_and_b32_e32 v153, 0xffff0000, v144
	v_lshlrev_b32_e32 v144, 16, v145
	v_and_b32_e32 v145, 0xffff0000, v145
	s_waitcnt vmcnt(2)
	v_lshlrev_b32_e32 v154, 16, v146
	v_and_b32_e32 v155, 0xffff0000, v146
	v_lshlrev_b32_e32 v146, 16, v147
	v_and_b32_e32 v147, 0xffff0000, v147
	s_waitcnt vmcnt(1)
	v_pk_mul_f32 v[138:139], v[138:139], s[38:39] op_sel_hi:[1,0]
	v_pk_mul_f32 v[136:137], v[136:137], s[38:39] op_sel_hi:[1,0]
	s_waitcnt vmcnt(0)
	v_pk_mul_f32 v[142:143], v[142:143], s[38:39] op_sel_hi:[1,0]
	v_pk_mul_f32 v[140:141], v[140:141], s[38:39] op_sel_hi:[1,0]
	v_pk_fma_f32 v[40:41], v[138:139], v[40:41], v[144:145]
	v_pk_fma_f32 v[38:39], v[136:137], v[38:39], v[152:153]
	v_pk_fma_f32 v[8:9], v[142:143], v[8:9], v[146:147]
	v_pk_fma_f32 v[6:7], v[140:141], v[6:7], v[154:155]
	v_cvt_pk_bf16_f32 v136, v38, v39
	v_cvt_pk_bf16_f32 v137, v40, v41
	s_nop 0
	v_cvt_pk_bf16_f32 v138, v6, v7
	v_cvt_pk_bf16_f32 v139, v8, v9
	global_store_dwordx2 v[148:149], v[136:137], off offset:256
	global_store_dwordx2 v[148:149], v[138:139], off offset:288
	global_load_dwordx2 v[144:145], v[150:151], off
	global_load_dwordx2 v[146:147], v[150:151], off offset:32
	global_load_dwordx4 v[136:139], v134, s[6:7]
	global_load_dwordx4 v[140:143], v134, s[6:7] offset:64
	s_waitcnt vmcnt(3)
	v_lshlrev_b32_e32 v148, 16, v144
	v_and_b32_e32 v149, 0xffff0000, v144
	v_lshlrev_b32_e32 v144, 16, v145
	v_and_b32_e32 v145, 0xffff0000, v145
	s_waitcnt vmcnt(2)
	v_lshlrev_b32_e32 v152, 16, v146
	v_and_b32_e32 v153, 0xffff0000, v146
	v_lshlrev_b32_e32 v146, 16, v147
	v_and_b32_e32 v147, 0xffff0000, v147
	s_waitcnt vmcnt(1)
	v_pk_mul_f32 v[138:139], v[138:139], s[38:39] op_sel_hi:[1,0]
	v_pk_mul_f32 v[136:137], v[136:137], s[38:39] op_sel_hi:[1,0]
	s_waitcnt vmcnt(0)
	v_pk_mul_f32 v[142:143], v[142:143], s[38:39] op_sel_hi:[1,0]
	v_pk_mul_f32 v[140:141], v[140:141], s[38:39] op_sel_hi:[1,0]
	v_pk_fma_f32 v[116:117], v[138:139], v[116:117], v[144:145]
	v_pk_fma_f32 v[114:115], v[136:137], v[114:115], v[148:149]
	v_pk_fma_f32 v[88:89], v[142:143], v[88:89], v[146:147]
	v_pk_fma_f32 v[86:87], v[140:141], v[86:87], v[152:153]
	v_cvt_pk_bf16_f32 v136, v114, v115
	v_cvt_pk_bf16_f32 v137, v116, v117
	s_nop 0
	v_cvt_pk_bf16_f32 v138, v86, v87
	v_cvt_pk_bf16_f32 v139, v88, v89
	global_store_dwordx2 v[150:151], v[136:137], off
	global_store_dwordx2 v[150:151], v[138:139], off offset:32
	global_load_dwordx2 v[144:145], v[150:151], off offset:256
	global_load_dwordx2 v[146:147], v[150:151], off offset:288
	global_load_dwordx4 v[136:139], v134, s[6:7] offset:512
	global_load_dwordx4 v[140:143], v134, s[6:7] offset:576
	s_waitcnt vmcnt(3)
	v_lshlrev_b32_e32 v148, 16, v144
	v_and_b32_e32 v149, 0xffff0000, v144
	v_lshlrev_b32_e32 v144, 16, v145
	v_and_b32_e32 v145, 0xffff0000, v145
	s_waitcnt vmcnt(2)
	v_lshlrev_b32_e32 v152, 16, v146
	v_and_b32_e32 v153, 0xffff0000, v146
	v_lshlrev_b32_e32 v146, 16, v147
	v_and_b32_e32 v147, 0xffff0000, v147
	s_waitcnt vmcnt(1)
	v_pk_mul_f32 v[138:139], v[138:139], s[38:39] op_sel_hi:[1,0]
	v_pk_mul_f32 v[136:137], v[136:137], s[38:39] op_sel_hi:[1,0]
	s_waitcnt vmcnt(0)
	v_pk_mul_f32 v[142:143], v[142:143], s[38:39] op_sel_hi:[1,0]
	v_pk_mul_f32 v[140:141], v[140:141], s[38:39] op_sel_hi:[1,0]
	v_pk_fma_f32 v[68:69], v[138:139], v[68:69], v[144:145]
	v_pk_fma_f32 v[66:67], v[136:137], v[66:67], v[148:149]
	v_pk_fma_f32 v[28:29], v[142:143], v[28:29], v[146:147]
	v_pk_fma_f32 v[26:27], v[140:141], v[26:27], v[152:153]
	v_cvt_pk_bf16_f32 v136, v66, v67
	v_cvt_pk_bf16_f32 v137, v68, v69
	s_nop 0
	v_cvt_pk_bf16_f32 v138, v26, v27
	v_cvt_pk_bf16_f32 v139, v28, v29
	global_store_dwordx2 v[150:151], v[136:137], off offset:256
	global_store_dwordx2 v[150:151], v[138:139], off offset:288
	global_load_dwordx2 v[144:145], v[132:133], off
	global_load_dwordx2 v[146:147], v[132:133], off offset:32
	global_load_dwordx4 v[136:139], v134, s[6:7]
	global_load_dwordx4 v[140:143], v134, s[6:7] offset:64
	s_waitcnt vmcnt(3)
	v_lshlrev_b32_e32 v148, 16, v144
	v_and_b32_e32 v149, 0xffff0000, v144
	v_lshlrev_b32_e32 v144, 16, v145
	v_and_b32_e32 v145, 0xffff0000, v145
	s_waitcnt vmcnt(2)
	v_lshlrev_b32_e32 v150, 16, v146
	v_and_b32_e32 v151, 0xffff0000, v146
	v_lshlrev_b32_e32 v146, 16, v147
	v_and_b32_e32 v147, 0xffff0000, v147
	s_waitcnt vmcnt(1)
	v_pk_mul_f32 v[138:139], v[138:139], s[38:39] op_sel_hi:[1,0]
	v_pk_mul_f32 v[136:137], v[136:137], s[38:39] op_sel_hi:[1,0]
	s_waitcnt vmcnt(0)
	v_pk_mul_f32 v[142:143], v[142:143], s[38:39] op_sel_hi:[1,0]
	v_pk_mul_f32 v[140:141], v[140:141], s[38:39] op_sel_hi:[1,0]
	v_pk_fma_f32 v[128:129], v[138:139], v[128:129], v[144:145]
	v_pk_fma_f32 v[126:127], v[136:137], v[126:127], v[148:149]
	v_pk_fma_f32 v[112:113], v[142:143], v[112:113], v[146:147]
	v_pk_fma_f32 v[110:111], v[140:141], v[110:111], v[150:151]
	v_cvt_pk_bf16_f32 v136, v126, v127
	v_cvt_pk_bf16_f32 v137, v128, v129
	v_add_co_u32_e32 v148, vcc, s4, v130
	v_cvt_pk_bf16_f32 v138, v110, v111
	v_cvt_pk_bf16_f32 v139, v112, v113
	global_store_dwordx2 v[132:133], v[136:137], off
	global_store_dwordx2 v[132:133], v[138:139], off offset:32
	global_load_dwordx2 v[144:145], v[132:133], off offset:256
	global_load_dwordx2 v[146:147], v[132:133], off offset:288
	global_load_dwordx4 v[136:139], v134, s[6:7] offset:512
	global_load_dwordx4 v[140:143], v134, s[6:7] offset:576
	s_mov_b64 s[4:5], 0x100000
	v_addc_co_u32_e32 v149, vcc, 0, v131, vcc
	s_waitcnt vmcnt(3)
	v_lshlrev_b32_e32 v150, 16, v144
	v_and_b32_e32 v151, 0xffff0000, v144
	v_lshlrev_b32_e32 v144, 16, v145
	v_and_b32_e32 v145, 0xffff0000, v145
	s_waitcnt vmcnt(2)
	v_lshlrev_b32_e32 v152, 16, v146
	v_and_b32_e32 v153, 0xffff0000, v146
	v_lshlrev_b32_e32 v146, 16, v147
	v_and_b32_e32 v147, 0xffff0000, v147
	s_waitcnt vmcnt(1)
	v_pk_mul_f32 v[138:139], v[138:139], s[38:39] op_sel_hi:[1,0]
	v_pk_mul_f32 v[136:137], v[136:137], s[38:39] op_sel_hi:[1,0]
	s_waitcnt vmcnt(0)
	v_pk_mul_f32 v[142:143], v[142:143], s[38:39] op_sel_hi:[1,0]
	v_pk_mul_f32 v[140:141], v[140:141], s[38:39] op_sel_hi:[1,0]
	v_pk_fma_f32 v[92:93], v[138:139], v[92:93], v[144:145]
	v_pk_fma_f32 v[90:91], v[136:137], v[90:91], v[150:151]
	v_pk_fma_f32 v[52:53], v[142:143], v[52:53], v[146:147]
	v_pk_fma_f32 v[50:51], v[140:141], v[50:51], v[152:153]
	v_cvt_pk_bf16_f32 v136, v90, v91
	v_cvt_pk_bf16_f32 v137, v92, v93
	v_lshl_add_u64 v[144:145], v[130:131], 0, s[4:5]
	v_cvt_pk_bf16_f32 v138, v50, v51
	v_cvt_pk_bf16_f32 v139, v52, v53
	global_store_dwordx2 v[132:133], v[136:137], off offset:256
	global_store_dwordx2 v[132:133], v[138:139], off offset:288
	global_load_dwordx2 v[132:133], v[148:149], off
	global_load_dwordx2 v[146:147], v[144:145], off offset:32
	global_load_dwordx4 v[136:139], v134, s[6:7]
	global_load_dwordx4 v[140:143], v134, s[6:7] offset:64
	s_mov_b32 s4, 0x120000
	s_waitcnt vmcnt(2)
	v_lshlrev_b32_e32 v152, 16, v146
	v_lshlrev_b32_e32 v150, 16, v132
	v_and_b32_e32 v151, 0xffff0000, v132
	v_lshlrev_b32_e32 v132, 16, v133
	v_and_b32_e32 v133, 0xffff0000, v133
	v_and_b32_e32 v153, 0xffff0000, v146
	v_lshlrev_b32_e32 v146, 16, v147
	v_and_b32_e32 v147, 0xffff0000, v147
	s_waitcnt vmcnt(1)
	v_pk_mul_f32 v[138:139], v[138:139], s[38:39] op_sel_hi:[1,0]
	v_pk_mul_f32 v[136:137], v[136:137], s[38:39] op_sel_hi:[1,0]
	s_waitcnt vmcnt(0)
	v_pk_mul_f32 v[142:143], v[142:143], s[38:39] op_sel_hi:[1,0]
	v_pk_mul_f32 v[140:141], v[140:141], s[38:39] op_sel_hi:[1,0]
	v_pk_fma_f32 v[124:125], v[138:139], v[124:125], v[132:133]
	v_pk_fma_f32 v[122:123], v[136:137], v[122:123], v[150:151]
	v_pk_fma_f32 v[120:121], v[142:143], v[120:121], v[146:147]
	v_pk_fma_f32 v[118:119], v[140:141], v[118:119], v[152:153]
	v_cvt_pk_bf16_f32 v132, v122, v123
	v_cvt_pk_bf16_f32 v133, v124, v125
	s_nop 0
	v_cvt_pk_bf16_f32 v136, v118, v119
	v_cvt_pk_bf16_f32 v137, v120, v121
	global_store_dwordx2 v[148:149], v[132:133], off
	global_store_dwordx2 v[144:145], v[136:137], off offset:32
	global_load_dwordx2 v[132:133], v[144:145], off offset:256
	global_load_dwordx2 v[146:147], v[144:145], off offset:288
	global_load_dwordx4 v[136:139], v134, s[6:7] offset:512
	global_load_dwordx4 v[140:143], v134, s[6:7] offset:576
	v_add_co_u32_e32 v148, vcc, s4, v130
	s_mov_b64 s[4:5], 0x120000
	s_nop 0
	v_addc_co_u32_e32 v149, vcc, 0, v131, vcc
	s_waitcnt vmcnt(3)
	v_lshlrev_b32_e32 v150, 16, v132
	v_and_b32_e32 v151, 0xffff0000, v132
	v_lshlrev_b32_e32 v132, 16, v133
	v_and_b32_e32 v133, 0xffff0000, v133
	s_waitcnt vmcnt(2)
	v_lshlrev_b32_e32 v152, 16, v146
	v_and_b32_e32 v153, 0xffff0000, v146
	v_lshlrev_b32_e32 v146, 16, v147
	v_and_b32_e32 v147, 0xffff0000, v147
	s_waitcnt vmcnt(1)
	v_pk_mul_f32 v[138:139], v[138:139], s[38:39] op_sel_hi:[1,0]
	v_pk_mul_f32 v[136:137], v[136:137], s[38:39] op_sel_hi:[1,0]
	s_waitcnt vmcnt(0)
	v_pk_mul_f32 v[142:143], v[142:143], s[38:39] op_sel_hi:[1,0]
	v_pk_mul_f32 v[140:141], v[140:141], s[38:39] op_sel_hi:[1,0]
	v_pk_fma_f32 v[108:109], v[138:139], v[108:109], v[132:133]
	v_pk_fma_f32 v[106:107], v[136:137], v[106:107], v[150:151]
	v_pk_fma_f32 v[84:85], v[142:143], v[84:85], v[146:147]
	v_pk_fma_f32 v[82:83], v[140:141], v[82:83], v[152:153]
	v_cvt_pk_bf16_f32 v132, v106, v107
	v_cvt_pk_bf16_f32 v133, v108, v109
	s_nop 0
	v_cvt_pk_bf16_f32 v136, v82, v83
	v_cvt_pk_bf16_f32 v137, v84, v85
	global_store_dwordx2 v[144:145], v[132:133], off offset:256
	global_store_dwordx2 v[144:145], v[136:137], off offset:288
	v_lshl_add_u64 v[144:145], v[130:131], 0, s[4:5]
	global_load_dwordx2 v[132:133], v[148:149], off
	global_load_dwordx2 v[146:147], v[144:145], off offset:32
	global_load_dwordx4 v[136:139], v134, s[6:7]
	global_load_dwordx4 v[140:143], v134, s[6:7] offset:64
	s_mov_b32 s4, 0x140000
	s_waitcnt vmcnt(2)
	v_lshlrev_b32_e32 v152, 16, v146
	v_lshlrev_b32_e32 v150, 16, v132
	v_and_b32_e32 v151, 0xffff0000, v132
	v_lshlrev_b32_e32 v132, 16, v133
	v_and_b32_e32 v133, 0xffff0000, v133
	v_and_b32_e32 v153, 0xffff0000, v146
	v_lshlrev_b32_e32 v146, 16, v147
	v_and_b32_e32 v147, 0xffff0000, v147
	s_waitcnt vmcnt(1)
	v_pk_mul_f32 v[138:139], v[138:139], s[38:39] op_sel_hi:[1,0]
	v_pk_mul_f32 v[136:137], v[136:137], s[38:39] op_sel_hi:[1,0]
	s_waitcnt vmcnt(0)
	v_pk_mul_f32 v[142:143], v[142:143], s[38:39] op_sel_hi:[1,0]
	v_pk_mul_f32 v[140:141], v[140:141], s[38:39] op_sel_hi:[1,0]
	v_pk_fma_f32 v[100:101], v[138:139], v[100:101], v[132:133]
	v_pk_fma_f32 v[98:99], v[136:137], v[98:99], v[150:151]
	v_pk_fma_f32 v[96:97], v[142:143], v[96:97], v[146:147]
	v_pk_fma_f32 v[94:95], v[140:141], v[94:95], v[152:153]
	v_cvt_pk_bf16_f32 v132, v98, v99
	v_cvt_pk_bf16_f32 v133, v100, v101
	s_nop 0
	v_cvt_pk_bf16_f32 v136, v94, v95
	v_cvt_pk_bf16_f32 v137, v96, v97
	global_store_dwordx2 v[148:149], v[132:133], off
	global_store_dwordx2 v[144:145], v[136:137], off offset:32
	global_load_dwordx2 v[132:133], v[144:145], off offset:256
	global_load_dwordx2 v[146:147], v[144:145], off offset:288
	global_load_dwordx4 v[136:139], v134, s[6:7] offset:512
	global_load_dwordx4 v[140:143], v134, s[6:7] offset:576
	v_add_co_u32_e32 v148, vcc, s4, v130
	s_mov_b64 s[4:5], 0x140000
	s_nop 0
	v_addc_co_u32_e32 v149, vcc, 0, v131, vcc
	s_waitcnt vmcnt(3)
	v_lshlrev_b32_e32 v150, 16, v132
	v_and_b32_e32 v151, 0xffff0000, v132
	v_lshlrev_b32_e32 v132, 16, v133
	v_and_b32_e32 v133, 0xffff0000, v133
	s_waitcnt vmcnt(2)
	v_lshlrev_b32_e32 v152, 16, v146
	v_and_b32_e32 v153, 0xffff0000, v146
	v_lshlrev_b32_e32 v146, 16, v147
	v_and_b32_e32 v147, 0xffff0000, v147
	s_waitcnt vmcnt(1)
	v_pk_mul_f32 v[138:139], v[138:139], s[38:39] op_sel_hi:[1,0]
	v_pk_mul_f32 v[136:137], v[136:137], s[38:39] op_sel_hi:[1,0]
	s_waitcnt vmcnt(0)
	v_pk_mul_f32 v[142:143], v[142:143], s[38:39] op_sel_hi:[1,0]
	v_pk_mul_f32 v[140:141], v[140:141], s[38:39] op_sel_hi:[1,0]
	v_pk_fma_f32 v[80:81], v[138:139], v[80:81], v[132:133]
	v_pk_fma_f32 v[78:79], v[136:137], v[78:79], v[150:151]
	v_pk_fma_f32 v[76:77], v[142:143], v[76:77], v[146:147]
	v_pk_fma_f32 v[74:75], v[140:141], v[74:75], v[152:153]
	v_cvt_pk_bf16_f32 v132, v78, v79
	v_cvt_pk_bf16_f32 v133, v80, v81
	s_nop 0
	v_cvt_pk_bf16_f32 v136, v74, v75
	v_cvt_pk_bf16_f32 v137, v76, v77
	global_store_dwordx2 v[144:145], v[132:133], off offset:256
	global_store_dwordx2 v[144:145], v[136:137], off offset:288
	v_lshl_add_u64 v[144:145], v[130:131], 0, s[4:5]
	global_load_dwordx2 v[132:133], v[148:149], off
	global_load_dwordx2 v[146:147], v[144:145], off offset:32
	global_load_dwordx4 v[136:139], v134, s[6:7]
	global_load_dwordx4 v[140:143], v134, s[6:7] offset:64
	s_mov_b32 s4, 0x160000
	s_waitcnt vmcnt(2)
	v_lshlrev_b32_e32 v152, 16, v146
	v_lshlrev_b32_e32 v150, 16, v132
	v_and_b32_e32 v151, 0xffff0000, v132
	v_lshlrev_b32_e32 v132, 16, v133
	v_and_b32_e32 v133, 0xffff0000, v133
	v_and_b32_e32 v153, 0xffff0000, v146
	v_lshlrev_b32_e32 v146, 16, v147
	v_and_b32_e32 v147, 0xffff0000, v147
	s_waitcnt vmcnt(1)
	v_pk_mul_f32 v[138:139], v[138:139], s[38:39] op_sel_hi:[1,0]
	v_pk_mul_f32 v[136:137], v[136:137], s[38:39] op_sel_hi:[1,0]
	s_waitcnt vmcnt(0)
	v_pk_mul_f32 v[142:143], v[142:143], s[38:39] op_sel_hi:[1,0]
	v_pk_mul_f32 v[140:141], v[140:141], s[38:39] op_sel_hi:[1,0]
	v_pk_fma_f32 v[64:65], v[138:139], v[64:65], v[132:133]
	v_pk_fma_f32 v[62:63], v[136:137], v[62:63], v[150:151]
	v_pk_fma_f32 v[60:61], v[142:143], v[60:61], v[146:147]
	v_pk_fma_f32 v[58:59], v[140:141], v[58:59], v[152:153]
	v_cvt_pk_bf16_f32 v132, v62, v63
	v_cvt_pk_bf16_f32 v133, v64, v65
	s_nop 0
	v_cvt_pk_bf16_f32 v136, v58, v59
	v_cvt_pk_bf16_f32 v137, v60, v61
	global_store_dwordx2 v[148:149], v[132:133], off
	global_store_dwordx2 v[144:145], v[136:137], off offset:32
	global_load_dwordx2 v[132:133], v[144:145], off offset:256
	global_load_dwordx2 v[146:147], v[144:145], off offset:288
	global_load_dwordx4 v[136:139], v134, s[6:7] offset:512
	global_load_dwordx4 v[140:143], v134, s[6:7] offset:576
	v_add_co_u32_e32 v148, vcc, s4, v130
	s_mov_b64 s[4:5], 0x160000
	s_nop 0
	v_addc_co_u32_e32 v149, vcc, 0, v131, vcc
	v_lshl_add_u64 v[130:131], v[130:131], 0, s[4:5]
	s_lshl_b32 s4, s15, 2
	s_waitcnt vmcnt(3)
	v_lshlrev_b32_e32 v150, 16, v132
	v_and_b32_e32 v151, 0xffff0000, v132
	v_lshlrev_b32_e32 v132, 16, v133
	v_and_b32_e32 v133, 0xffff0000, v133
	s_waitcnt vmcnt(2)
	v_lshlrev_b32_e32 v152, 16, v146
	v_and_b32_e32 v153, 0xffff0000, v146
	v_lshlrev_b32_e32 v146, 16, v147
	v_and_b32_e32 v147, 0xffff0000, v147
	s_waitcnt vmcnt(1)
	v_pk_mul_f32 v[138:139], v[138:139], s[38:39] op_sel_hi:[1,0]
	v_pk_mul_f32 v[136:137], v[136:137], s[38:39] op_sel_hi:[1,0]
	s_waitcnt vmcnt(0)
	v_pk_mul_f32 v[142:143], v[142:143], s[38:39] op_sel_hi:[1,0]
	v_pk_mul_f32 v[140:141], v[140:141], s[38:39] op_sel_hi:[1,0]
	v_pk_fma_f32 v[48:49], v[138:139], v[48:49], v[132:133]
	v_pk_fma_f32 v[46:47], v[136:137], v[46:47], v[150:151]
	v_pk_fma_f32 v[44:45], v[142:143], v[44:45], v[146:147]
	v_pk_fma_f32 v[42:43], v[140:141], v[42:43], v[152:153]
	v_cvt_pk_bf16_f32 v132, v46, v47
	v_cvt_pk_bf16_f32 v133, v48, v49
	v_mul_f32_e32 v152, v37, v37
	v_cvt_pk_bf16_f32 v136, v42, v43
	v_cvt_pk_bf16_f32 v137, v44, v45
	global_store_dwordx2 v[144:145], v[132:133], off offset:256
	global_store_dwordx2 v[144:145], v[136:137], off offset:288
	global_load_dwordx2 v[132:133], v[148:149], off
	global_load_dwordx2 v[144:145], v[130:131], off offset:32
	global_load_dwordx4 v[136:139], v134, s[6:7]
	global_load_dwordx4 v[140:143], v134, s[6:7] offset:64
	v_fmac_f32_e32 v152, v36, v36
	v_mul_f32_e32 v153, v5, v5
	v_fmac_f32_e32 v153, v4, v4
	s_waitcnt vmcnt(2)
	v_lshlrev_b32_e32 v150, 16, v144
	v_lshlrev_b32_e32 v146, 16, v132
	v_and_b32_e32 v147, 0xffff0000, v132
	v_lshlrev_b32_e32 v132, 16, v133
	v_and_b32_e32 v133, 0xffff0000, v133
	v_and_b32_e32 v151, 0xffff0000, v144
	v_lshlrev_b32_e32 v144, 16, v145
	v_and_b32_e32 v145, 0xffff0000, v145
	s_waitcnt vmcnt(1)
	v_pk_mul_f32 v[138:139], v[138:139], s[38:39] op_sel_hi:[1,0]
	v_pk_mul_f32 v[136:137], v[136:137], s[38:39] op_sel_hi:[1,0]
	s_waitcnt vmcnt(0)
	v_pk_mul_f32 v[142:143], v[142:143], s[38:39] op_sel_hi:[1,0]
	v_pk_mul_f32 v[140:141], v[140:141], s[38:39] op_sel_hi:[1,0]
	v_pk_fma_f32 v[32:33], v[138:139], v[32:33], v[132:133]
	v_pk_fma_f32 v[30:31], v[136:137], v[30:31], v[146:147]
	v_pk_fma_f32 v[24:25], v[142:143], v[24:25], v[144:145]
	v_pk_fma_f32 v[22:23], v[140:141], v[22:23], v[150:151]
	v_cvt_pk_bf16_f32 v132, v30, v31
	v_cvt_pk_bf16_f32 v133, v32, v33
	v_mul_f32_e32 v138, v73, v73
	v_cvt_pk_bf16_f32 v136, v22, v23
	v_cvt_pk_bf16_f32 v137, v24, v25
	global_store_dwordx2 v[148:149], v[132:133], off
	global_store_dwordx2 v[130:131], v[136:137], off offset:32
	global_load_dwordx2 v[148:149], v[130:131], off offset:256
	global_load_dwordx2 v[150:151], v[130:131], off offset:288
	global_load_dwordx4 v[140:143], v134, s[6:7] offset:512
	global_load_dwordx4 v[144:147], v134, s[6:7] offset:576
	v_mul_f32_e32 v136, v71, v71
	v_mul_f32_e32 v139, v35, v35
	v_fmac_f32_e32 v136, v70, v70
	v_fmac_f32_e32 v138, v72, v72
	v_fmac_f32_e32 v139, v34, v34
	v_add_f32_e32 v136, v136, v138
	v_add_f32_e32 v138, v139, v152
	v_and_b32_e32 v133, 64, v1
	v_add_f32_e32 v136, v136, v138
	v_mul_f32_e32 v138, v19, v19
	v_mul_f32_e32 v139, v21, v21
	v_xor_b32_e32 v132, 16, v1
	v_add_u32_e32 v133, 64, v133
	v_mul_f32_e32 v152, v3, v3
	v_fmac_f32_e32 v138, v18, v18
	v_fmac_f32_e32 v139, v20, v20
	v_cmp_lt_i32_e32 vcc, v132, v133
	v_fmac_f32_e32 v152, v2, v2
	v_add_f32_e32 v138, v138, v139
	v_cndmask_b32_e32 v132, v1, v132, vcc
	v_add_f32_e32 v139, v152, v153
	v_add_f32_e32 v136, v136, v138
	v_lshlrev_b32_e32 v132, 2, v132
	v_add_f32_e32 v136, v139, v136
	ds_bpermute_b32 v138, v132, v136
	v_xor_b32_e32 v139, 32, v1
	v_cmp_lt_i32_e32 vcc, v139, v133
	v_and_b32_e32 v137, 63, v185
	s_add_i32 s6, s4, 0
	v_cndmask_b32_e32 v133, v1, v139, vcc
	v_lshlrev_b32_e32 v133, 2, v133
	s_waitcnt lgkmcnt(0)
	v_add_f32_e32 v136, v136, v138
	ds_bpermute_b32 v138, v133, v136
	v_cmp_gt_u32_e32 vcc, 16, v137
	s_waitcnt vmcnt(3)
	v_lshlrev_b32_e32 v152, 16, v148
	v_and_b32_e32 v153, 0xffff0000, v148
	v_lshlrev_b32_e32 v148, 16, v149
	v_and_b32_e32 v149, 0xffff0000, v149
	s_waitcnt vmcnt(2)
	v_lshlrev_b32_e32 v154, 16, v150
	v_and_b32_e32 v155, 0xffff0000, v150
	v_lshlrev_b32_e32 v150, 16, v151
	v_and_b32_e32 v151, 0xffff0000, v151
	s_waitcnt vmcnt(1)
	v_pk_mul_f32 v[142:143], v[142:143], s[38:39] op_sel_hi:[1,0]
	v_pk_mul_f32 v[140:141], v[140:141], s[38:39] op_sel_hi:[1,0]
	s_waitcnt vmcnt(0)
	v_pk_mul_f32 v[146:147], v[146:147], s[38:39] op_sel_hi:[1,0]
	v_pk_mul_f32 v[144:145], v[144:145], s[38:39] op_sel_hi:[1,0]
	v_pk_fma_f32 v[16:17], v[142:143], v[16:17], v[148:149]
	v_pk_fma_f32 v[14:15], v[140:141], v[14:15], v[152:153]
	v_pk_fma_f32 v[12:13], v[146:147], v[12:13], v[150:151]
	v_pk_fma_f32 v[10:11], v[144:145], v[10:11], v[154:155]
	v_cvt_pk_bf16_f32 v140, v14, v15
	v_cvt_pk_bf16_f32 v141, v16, v17
	s_nop 0
	v_cvt_pk_bf16_f32 v142, v10, v11
	v_cvt_pk_bf16_f32 v143, v12, v13
	global_store_dwordx2 v[130:131], v[140:141], off offset:256
	global_store_dwordx2 v[130:131], v[142:143], off offset:288
	s_and_saveexec_b64 s[4:5], vcc
	s_cbranch_execz .LBB0_1056
	s_lshl_b32 s7, s19, 10
	s_add_i32 s7, s6, s7
	v_lshl_add_u32 v130, v186, 4, s7
	s_waitcnt lgkmcnt(0)
	v_add_f32_e32 v131, v136, v138
	ds_write_b32 v130, v131

.LBB0_1437:
	v_and_b32_e32 v188, 15, v189
	v_and_b32_e32 v2, 48, v189
	v_lshlrev_b32_e32 v3, 2, v189
	s_and_b32 s8, s6, 3
	s_lshl_b32 s9, s7, 13
	v_lshl_or_b32 v2, v188, 6, v2
	v_and_b32_e32 v3, 32, v3
	v_bitop3_b32 v4, v2, s9, v3 bitop3:0xde
	s_lshl_b32 s9, s8, 12
	v_lshl_add_u64 v[180:181], s[20:21], 0, v[154:155]
	v_bitop3_b32 v2, v2, s9, v3 bitop3:0xde
	s_add_i32 s9, s60, s72
	v_lshl_add_u64 v[178:179], s[20:21], 0, v[182:183]
	v_lshl_add_u64 v[72:73], v[180:181], 0, s[36:37]
	s_mov_b32 m0, s9
	s_add_i32 s19, s9, 0x2000
	s_waitcnt vmcnt(2)
	s_barrier
	global_load_lds_dwordx4 v[72:73], off
	v_lshl_add_u64 v[158:159], v[178:179], 0, s[36:37]
	s_mov_b32 m0, s19
	s_add_i32 s18, s67, 0x8000
	global_load_lds_dwordx4 v[158:159], off
	v_lshl_add_u64 v[70:71], v[172:173], 0, s[36:37]
	s_mov_b32 m0, s18
	s_add_i32 s43, s67, 0xa000
	global_load_lds_dwordx4 v[70:71], off
	v_lshl_add_u64 v[160:161], v[170:171], 0, s[36:37]
	s_mov_b32 m0, s43
	s_add_i32 s44, s61, s72
	global_load_lds_dwordx4 v[160:161], off
	v_lshl_add_u64 v[162:163], s[24:25], 0, v[154:155]
	s_mov_b32 m0, s44
	s_add_i32 s45, s44, 0x2000
	global_load_lds_dwordx4 v[162:163], off
	v_lshl_add_u64 v[164:165], s[24:25], 0, v[182:183]
	s_mov_b32 m0, s45
	s_add_i32 s73, 0, 0x10000
	global_load_lds_dwordx4 v[164:165], off
	v_add_u32_e32 v195, s73, v2
	s_add_i32 s75, 0, 0x14000
	s_waitcnt vmcnt(6)
	s_barrier
	v_add_u32_e32 v194, s75, v2
	v_add_u32_e32 v191, 0, v4
	v_add_u32_e32 v193, s60, v2
	v_add_u32_e32 v192, s61, v2
	ds_read_b128 v[54:57], v195
	ds_read_b128 v[58:61], v195 offset:1024
	ds_read_b128 v[196:199], v195 offset:2048
	ds_read_b128 v[200:203], v195 offset:3072
	ds_read_b128 v[10:13], v194
	ds_read_b128 v[14:17], v194 offset:1024
	ds_read_b128 v[2:5], v194 offset:2048
	ds_read_b128 v[6:9], v194 offset:3072
	s_lshl_b32 s66, s7, 6
	v_lshl_add_u64 v[176:177], s[22:23], 0, v[154:155]
	v_lshl_add_u64 v[174:175], s[22:23], 0, v[182:183]
	s_add_u32 s70, s4, 0x10080
	s_addc_u32 s71, s5, 0
	s_add_i32 s74, s67, 0xc000
	v_lshl_add_u64 v[30:31], s[70:71], 0, v[154:155]
	s_mov_b32 m0, s74
	s_add_i32 s69, s67, 0xe000
	ds_read_b128 v[22:25], v191
	ds_read_b128 v[26:29], v191 offset:1024
	ds_read_b128 v[34:37], v191 offset:2048
	ds_read_b128 v[38:41], v191 offset:3072
	ds_read_b128 v[82:85], v191 offset:4096
	ds_read_b128 v[86:89], v191 offset:5120
	ds_read_b128 v[94:97], v191 offset:6144
	ds_read_b128 v[98:101], v191 offset:7168
	global_load_lds_dwordx4 v[30:31], off
	v_lshl_add_u64 v[30:31], s[70:71], 0, v[182:183]
	s_mov_b32 m0, s69
	s_nop 0
	global_load_lds_dwordx4 v[30:31], off
	s_waitcnt vmcnt(8)
	s_waitcnt lgkmcnt(0)
	s_barrier
	s_setprio 1
	v_mov_b64_e32 v[32:33], v[20:21]
	v_mov_b64_e32 v[152:153], v[20:21]
	v_mov_b64_e32 v[92:93], v[20:21]
	v_mov_b64_e32 v[44:45], v[20:21]
	v_mov_b64_e32 v[116:117], v[20:21]
	v_mov_b64_e32 v[64:65], v[20:21]
	v_mov_b64_e32 v[80:81], v[20:21]
	v_mov_b64_e32 v[52:53], v[20:21]
	v_mov_b64_e32 v[30:31], v[18:19]
	v_mov_b64_e32 v[150:151], v[18:19]
	v_mov_b64_e32 v[90:91], v[18:19]
	v_mov_b64_e32 v[42:43], v[18:19]
	v_mov_b64_e32 v[114:115], v[18:19]
	v_mov_b64_e32 v[62:63], v[18:19]
	v_mov_b64_e32 v[78:79], v[18:19]
	v_mov_b64_e32 v[50:51], v[18:19]
	s_waitcnt lgkmcnt(0)
	v_mfma_scale_f32_16x16x128_f8f6f4 v[30:33], v[54:61], v[22:29], v[30:33], v190, v190 op_sel_hi:[0,0,0]
	v_mfma_scale_f32_16x16x128_f8f6f4 v[150:153], v[196:203], v[22:29], v[150:153], v190, v190 op_sel_hi:[0,0,0]
	v_mfma_scale_f32_16x16x128_f8f6f4 v[90:93], v[54:61], v[34:41], v[90:93], v190, v190 op_sel_hi:[0,0,0]
	v_mfma_scale_f32_16x16x128_f8f6f4 v[42:45], v[196:203], v[34:41], v[42:45], v190, v190 op_sel_hi:[0,0,0]
	v_mfma_scale_f32_16x16x128_f8f6f4 v[114:117], v[54:61], v[82:89], v[114:117], v190, v190 op_sel_hi:[0,0,0]
	v_mfma_scale_f32_16x16x128_f8f6f4 v[62:65], v[196:203], v[82:89], v[62:65], v190, v190 op_sel_hi:[0,0,0]
	v_mfma_scale_f32_16x16x128_f8f6f4 v[78:81], v[54:61], v[94:101], v[78:81], v190, v190 op_sel_hi:[0,0,0]
	v_mfma_scale_f32_16x16x128_f8f6f4 v[50:53], v[196:203], v[94:101], v[50:53], v190, v190 op_sel_hi:[0,0,0]
	s_setprio 0
	s_setprio 1
	v_mov_b64_e32 v[144:145], v[20:21]
	v_mov_b64_e32 v[148:149], v[20:21]
	v_mov_b64_e32 v[142:143], v[18:19]
	v_mov_b64_e32 v[146:147], v[18:19]
	v_mfma_scale_f32_16x16x128_f8f6f4 v[142:145], v[10:17], v[22:29], v[142:145], v190, v190 op_sel_hi:[0,0,0]
	v_mfma_scale_f32_16x16x128_f8f6f4 v[146:149], v[2:9], v[22:29], v[146:149], v190, v190 op_sel_hi:[0,0,0]
	v_mov_b64_e32 v[28:29], v[20:21]
	v_mov_b64_e32 v[140:141], v[20:21]
	v_mov_b64_e32 v[26:27], v[18:19]
	v_mov_b64_e32 v[138:139], v[18:19]
	v_mfma_scale_f32_16x16x128_f8f6f4 v[26:29], v[10:17], v[34:41], v[26:29], v190, v190 op_sel_hi:[0,0,0]
	v_mfma_scale_f32_16x16x128_f8f6f4 v[138:141], v[2:9], v[34:41], v[138:141], v190, v190 op_sel_hi:[0,0,0]
	v_mov_b64_e32 v[40:41], v[20:21]
	v_mov_b64_e32 v[128:129], v[20:21]
	v_mov_b64_e32 v[24:25], v[20:21]
	v_mov_b64_e32 v[76:77], v[20:21]
	v_mov_b64_e32 v[38:39], v[18:19]
	v_mov_b64_e32 v[126:127], v[18:19]
	v_mov_b64_e32 v[22:23], v[18:19]
	v_mov_b64_e32 v[74:75], v[18:19]
	v_mfma_scale_f32_16x16x128_f8f6f4 v[38:41], v[10:17], v[82:89], v[38:41], v190, v190 op_sel_hi:[0,0,0]
	v_mfma_scale_f32_16x16x128_f8f6f4 v[126:129], v[2:9], v[82:89], v[126:129], v190, v190 op_sel_hi:[0,0,0]
	v_mfma_scale_f32_16x16x128_f8f6f4 v[22:25], v[10:17], v[94:101], v[22:25], v190, v190 op_sel_hi:[0,0,0]
	v_mfma_scale_f32_16x16x128_f8f6f4 v[74:77], v[2:9], v[94:101], v[74:77], v190, v190 op_sel_hi:[0,0,0]
	s_setprio 2
	s_barrier
	s_add_i32 s70, s73, s72
	v_lshl_add_u64 v[34:35], v[180:181], 0, s[14:15]
	s_mov_b32 m0, s70
	s_add_i32 s71, s70, 0x2000
	ds_read_b128 v[204:207], v191 offset:16384
	ds_read_b128 v[208:211], v191 offset:17408
	ds_read_b128 v[212:215], v191 offset:18432
	ds_read_b128 v[216:219], v191 offset:19456
	ds_read_b128 v[220:223], v191 offset:20480
	ds_read_b128 v[224:227], v191 offset:21504
	ds_read_b128 v[228:231], v191 offset:22528
	ds_read_b128 v[232:235], v191 offset:23552
	global_load_lds_dwordx4 v[34:35], off
	v_lshl_add_u64 v[34:35], v[178:179], 0, s[14:15]
	s_mov_b32 m0, s71
	s_add_i32 s72, s75, s72
	global_load_lds_dwordx4 v[34:35], off
	v_lshl_add_u64 v[34:35], s[26:27], 0, v[154:155]
	s_mov_b32 m0, s72
	s_add_i32 s73, s72, 0x2000
	global_load_lds_dwordx4 v[34:35], off
	v_lshl_add_u64 v[34:35], s[26:27], 0, v[182:183]
	s_mov_b32 m0, s73
	s_nop 0
	global_load_lds_dwordx4 v[34:35], off
	v_lshl_add_u64 v[34:35], v[172:173], 0, s[14:15]
	s_mov_b32 m0, s67
	s_nop 0
	global_load_lds_dwordx4 v[34:35], off
	v_lshl_add_u64 v[34:35], v[170:171], 0, s[14:15]
	s_mov_b32 m0, s68
	s_nop 0
	global_load_lds_dwordx4 v[34:35], off
	s_waitcnt vmcnt(8)
	s_waitcnt lgkmcnt(0)
	s_barrier
	s_setprio 1
	v_mov_b64_e32 v[136:137], v[20:21]
	v_mov_b64_e32 v[104:105], v[20:21]
	v_mov_b64_e32 v[124:125], v[20:21]
	v_mov_b64_e32 v[100:101], v[20:21]
	v_mov_b64_e32 v[112:113], v[20:21]
	v_mov_b64_e32 v[108:109], v[20:21]
	v_mov_b64_e32 v[88:89], v[20:21]
	v_mov_b64_e32 v[84:85], v[20:21]
	v_mov_b64_e32 v[134:135], v[18:19]
	v_mov_b64_e32 v[102:103], v[18:19]
	v_mov_b64_e32 v[122:123], v[18:19]
	v_mov_b64_e32 v[98:99], v[18:19]
	v_mov_b64_e32 v[110:111], v[18:19]
	v_mov_b64_e32 v[106:107], v[18:19]
	v_mov_b64_e32 v[86:87], v[18:19]
	v_mov_b64_e32 v[82:83], v[18:19]
	s_waitcnt lgkmcnt(0)
	v_mfma_scale_f32_16x16x128_f8f6f4 v[134:137], v[54:61], v[204:211], v[134:137], v190, v190 op_sel_hi:[0,0,0]
	v_mfma_scale_f32_16x16x128_f8f6f4 v[102:105], v[196:203], v[204:211], v[102:105], v190, v190 op_sel_hi:[0,0,0]
	v_mfma_scale_f32_16x16x128_f8f6f4 v[122:125], v[54:61], v[212:219], v[122:125], v190, v190 op_sel_hi:[0,0,0]
	v_mfma_scale_f32_16x16x128_f8f6f4 v[98:101], v[196:203], v[212:219], v[98:101], v190, v190 op_sel_hi:[0,0,0]
	v_mfma_scale_f32_16x16x128_f8f6f4 v[110:113], v[54:61], v[220:227], v[110:113], v190, v190 op_sel_hi:[0,0,0]
	v_mfma_scale_f32_16x16x128_f8f6f4 v[106:109], v[196:203], v[220:227], v[106:109], v190, v190 op_sel_hi:[0,0,0]
	v_mfma_scale_f32_16x16x128_f8f6f4 v[86:89], v[54:61], v[228:235], v[86:89], v190, v190 op_sel_hi:[0,0,0]
	v_mfma_scale_f32_16x16x128_f8f6f4 v[82:85], v[196:203], v[228:235], v[82:85], v190, v190 op_sel_hi:[0,0,0]
	s_setprio 0
	s_setprio 1
	v_mov_b64_e32 v[36:37], v[20:21]
	v_mov_b64_e32 v[132:133], v[20:21]
	v_mov_b64_e32 v[48:49], v[20:21]
	v_mov_b64_e32 v[120:121], v[20:21]
	v_mov_b64_e32 v[68:69], v[20:21]
	v_mov_b64_e32 v[96:97], v[20:21]
	v_mov_b64_e32 v[56:57], v[20:21]
	v_mov_b64_e32 v[60:61], v[20:21]
	v_mov_b64_e32 v[34:35], v[18:19]
	v_mov_b64_e32 v[130:131], v[18:19]
	v_mov_b64_e32 v[46:47], v[18:19]
	v_mov_b64_e32 v[118:119], v[18:19]
	v_mov_b64_e32 v[66:67], v[18:19]
	v_mov_b64_e32 v[94:95], v[18:19]
	v_mov_b64_e32 v[54:55], v[18:19]
	v_mov_b64_e32 v[58:59], v[18:19]
	v_mfma_scale_f32_16x16x128_f8f6f4 v[34:37], v[10:17], v[204:211], v[34:37], v190, v190 op_sel_hi:[0,0,0]
	v_mfma_scale_f32_16x16x128_f8f6f4 v[130:133], v[2:9], v[204:211], v[130:133], v190, v190 op_sel_hi:[0,0,0]
	v_mfma_scale_f32_16x16x128_f8f6f4 v[46:49], v[10:17], v[212:219], v[46:49], v190, v190 op_sel_hi:[0,0,0]
	v_mfma_scale_f32_16x16x128_f8f6f4 v[118:121], v[2:9], v[212:219], v[118:121], v190, v190 op_sel_hi:[0,0,0]
	v_mfma_scale_f32_16x16x128_f8f6f4 v[66:69], v[10:17], v[220:227], v[66:69], v190, v190 op_sel_hi:[0,0,0]
	v_mfma_scale_f32_16x16x128_f8f6f4 v[94:97], v[2:9], v[220:227], v[94:97], v190, v190 op_sel_hi:[0,0,0]
	v_mfma_scale_f32_16x16x128_f8f6f4 v[54:57], v[10:17], v[228:235], v[54:57], v190, v190 op_sel_hi:[0,0,0]
	v_mfma_scale_f32_16x16x128_f8f6f4 v[58:61], v[2:9], v[228:235], v[58:61], v190, v190 op_sel_hi:[0,0,0]
	s_setprio 2
	s_barrier
	ds_read_b128 v[2:5], v193
	ds_read_b128 v[6:9], v193 offset:1024
	ds_read_b128 v[10:13], v193 offset:2048
	ds_read_b128 v[14:17], v193 offset:3072
	ds_read_b128 v[196:199], v192
	ds_read_b128 v[200:203], v192 offset:1024
	ds_read_b128 v[204:207], v192 offset:2048
	ds_read_b128 v[208:211], v192 offset:3072
	s_add_u32 s76, s4, 0x10100
	s_addc_u32 s77, s5, 0
	s_mov_b32 m0, s48
	v_lshl_add_u64 v[244:245], s[76:77], 0, v[154:155]
	ds_read_b128 v[212:215], v191 offset:32768
	ds_read_b128 v[216:219], v191 offset:33792
	ds_read_b128 v[220:223], v191 offset:34816
	ds_read_b128 v[224:227], v191 offset:35840
	ds_read_b128 v[228:231], v191 offset:36864
	ds_read_b128 v[232:235], v191 offset:37888
	ds_read_b128 v[236:239], v191 offset:38912
	ds_read_b128 v[240:243], v191 offset:39936
	global_load_lds_dwordx4 v[244:245], off
	v_lshl_add_u64 v[244:245], s[76:77], 0, v[182:183]
	s_mov_b32 m0, s49
	s_nop 0
	global_load_lds_dwordx4 v[244:245], off
	s_waitcnt vmcnt(8)
	s_waitcnt lgkmcnt(0)
	s_barrier
	s_setprio 1
	s_waitcnt lgkmcnt(0)
	v_mfma_scale_f32_16x16x128_f8f6f4 v[30:33], v[2:9], v[212:219], v[30:33], v190, v190 op_sel_hi:[0,0,0]
	v_mfma_scale_f32_16x16x128_f8f6f4 v[150:153], v[10:17], v[212:219], v[150:153], v190, v190 op_sel_hi:[0,0,0]
	v_mfma_scale_f32_16x16x128_f8f6f4 v[90:93], v[2:9], v[220:227], v[90:93], v190, v190 op_sel_hi:[0,0,0]
	v_mfma_scale_f32_16x16x128_f8f6f4 v[42:45], v[10:17], v[220:227], v[42:45], v190, v190 op_sel_hi:[0,0,0]
	v_mfma_scale_f32_16x16x128_f8f6f4 v[114:117], v[2:9], v[228:235], v[114:117], v190, v190 op_sel_hi:[0,0,0]
	v_mfma_scale_f32_16x16x128_f8f6f4 v[62:65], v[10:17], v[228:235], v[62:65], v190, v190 op_sel_hi:[0,0,0]
	v_mfma_scale_f32_16x16x128_f8f6f4 v[78:81], v[2:9], v[236:243], v[78:81], v190, v190 op_sel_hi:[0,0,0]
	v_mfma_scale_f32_16x16x128_f8f6f4 v[50:53], v[10:17], v[236:243], v[50:53], v190, v190 op_sel_hi:[0,0,0]
	s_setprio 0
	s_setprio 1
	v_mfma_scale_f32_16x16x128_f8f6f4 v[142:145], v[196:203], v[212:219], v[142:145], v190, v190 op_sel_hi:[0,0,0]
	v_mfma_scale_f32_16x16x128_f8f6f4 v[146:149], v[204:211], v[212:219], v[146:149], v190, v190 op_sel_hi:[0,0,0]
	v_mfma_scale_f32_16x16x128_f8f6f4 v[26:29], v[196:203], v[220:227], v[26:29], v190, v190 op_sel_hi:[0,0,0]
	v_mfma_scale_f32_16x16x128_f8f6f4 v[138:141], v[204:211], v[220:227], v[138:141], v190, v190 op_sel_hi:[0,0,0]
	v_mfma_scale_f32_16x16x128_f8f6f4 v[38:41], v[196:203], v[228:235], v[38:41], v190, v190 op_sel_hi:[0,0,0]
	v_mfma_scale_f32_16x16x128_f8f6f4 v[126:129], v[204:211], v[228:235], v[126:129], v190, v190 op_sel_hi:[0,0,0]
	v_mfma_scale_f32_16x16x128_f8f6f4 v[22:25], v[196:203], v[236:243], v[22:25], v190, v190 op_sel_hi:[0,0,0]
	v_mfma_scale_f32_16x16x128_f8f6f4 v[74:77], v[204:211], v[236:243], v[74:77], v190, v190 op_sel_hi:[0,0,0]
	s_setprio 2
	s_barrier
	s_mov_b32 m0, s9
	v_lshl_add_u64 v[244:245], v[180:181], 0, s[38:39]
	ds_read_b128 v[212:215], v191 offset:49152
	ds_read_b128 v[216:219], v191 offset:50176
	ds_read_b128 v[220:223], v191 offset:51200
	ds_read_b128 v[224:227], v191 offset:52224
	ds_read_b128 v[228:231], v191 offset:53248
	ds_read_b128 v[232:235], v191 offset:54272
	ds_read_b128 v[236:239], v191 offset:55296
	ds_read_b128 v[240:243], v191 offset:56320
	global_load_lds_dwordx4 v[244:245], off
	v_lshl_add_u64 v[244:245], v[178:179], 0, s[38:39]
	s_mov_b32 m0, s19
	s_nop 0
	global_load_lds_dwordx4 v[244:245], off
	v_lshl_add_u64 v[244:245], s[28:29], 0, v[154:155]
	s_mov_b32 m0, s44
	s_nop 0
	global_load_lds_dwordx4 v[244:245], off
	v_lshl_add_u64 v[244:245], s[28:29], 0, v[182:183]
	s_mov_b32 m0, s45
	s_nop 0
	global_load_lds_dwordx4 v[244:245], off
	v_lshl_add_u64 v[244:245], v[172:173], 0, s[38:39]
	s_mov_b32 m0, s18
	s_nop 0
	global_load_lds_dwordx4 v[244:245], off
	v_lshl_add_u64 v[244:245], v[170:171], 0, s[38:39]
	s_mov_b32 m0, s43
	s_nop 0
	global_load_lds_dwordx4 v[244:245], off
	s_waitcnt vmcnt(8)
	s_waitcnt lgkmcnt(0)
	s_barrier
	s_setprio 1
	s_waitcnt lgkmcnt(0)
	v_mfma_scale_f32_16x16x128_f8f6f4 v[134:137], v[2:9], v[212:219], v[134:137], v190, v190 op_sel_hi:[0,0,0]
	v_mfma_scale_f32_16x16x128_f8f6f4 v[102:105], v[10:17], v[212:219], v[102:105], v190, v190 op_sel_hi:[0,0,0]
	v_mfma_scale_f32_16x16x128_f8f6f4 v[122:125], v[2:9], v[220:227], v[122:125], v190, v190 op_sel_hi:[0,0,0]
	v_mfma_scale_f32_16x16x128_f8f6f4 v[98:101], v[10:17], v[220:227], v[98:101], v190, v190 op_sel_hi:[0,0,0]
	v_mfma_scale_f32_16x16x128_f8f6f4 v[110:113], v[2:9], v[228:235], v[110:113], v190, v190 op_sel_hi:[0,0,0]
	v_mfma_scale_f32_16x16x128_f8f6f4 v[106:109], v[10:17], v[228:235], v[106:109], v190, v190 op_sel_hi:[0,0,0]
	v_mfma_scale_f32_16x16x128_f8f6f4 v[86:89], v[2:9], v[236:243], v[86:89], v190, v190 op_sel_hi:[0,0,0]
	v_mfma_scale_f32_16x16x128_f8f6f4 v[82:85], v[10:17], v[236:243], v[82:85], v190, v190 op_sel_hi:[0,0,0]
	s_setprio 0
	s_setprio 1
	v_mfma_scale_f32_16x16x128_f8f6f4 v[34:37], v[196:203], v[212:219], v[34:37], v190, v190 op_sel_hi:[0,0,0]
	v_mfma_scale_f32_16x16x128_f8f6f4 v[130:133], v[204:211], v[212:219], v[130:133], v190, v190 op_sel_hi:[0,0,0]
	v_mfma_scale_f32_16x16x128_f8f6f4 v[46:49], v[196:203], v[220:227], v[46:49], v190, v190 op_sel_hi:[0,0,0]
	v_mfma_scale_f32_16x16x128_f8f6f4 v[118:121], v[204:211], v[220:227], v[118:121], v190, v190 op_sel_hi:[0,0,0]
	v_mfma_scale_f32_16x16x128_f8f6f4 v[66:69], v[196:203], v[228:235], v[66:69], v190, v190 op_sel_hi:[0,0,0]
	v_mfma_scale_f32_16x16x128_f8f6f4 v[94:97], v[204:211], v[228:235], v[94:97], v190, v190 op_sel_hi:[0,0,0]
	v_mfma_scale_f32_16x16x128_f8f6f4 v[54:57], v[196:203], v[236:243], v[54:57], v190, v190 op_sel_hi:[0,0,0]
	v_mfma_scale_f32_16x16x128_f8f6f4 v[58:61], v[204:211], v[236:243], v[58:61], v190, v190 op_sel_hi:[0,0,0]
	s_setprio 2
	s_barrier
	ds_read_b128 v[2:5], v195
	ds_read_b128 v[6:9], v195 offset:1024
	ds_read_b128 v[10:13], v195 offset:2048
	ds_read_b128 v[14:17], v195 offset:3072
	ds_read_b128 v[196:199], v194
	ds_read_b128 v[200:203], v194 offset:1024
	ds_read_b128 v[204:207], v194 offset:2048
	ds_read_b128 v[208:211], v194 offset:3072
	s_add_u32 s4, s4, 0x10180
	s_addc_u32 s5, s5, 0
	s_mov_b32 m0, s74
	v_lshl_add_u64 v[194:195], s[4:5], 0, v[154:155]
	ds_read_b128 v[212:215], v191
	ds_read_b128 v[216:219], v191 offset:1024
	ds_read_b128 v[220:223], v191 offset:2048
	ds_read_b128 v[224:227], v191 offset:3072
	ds_read_b128 v[228:231], v191 offset:4096
	ds_read_b128 v[232:235], v191 offset:5120
	ds_read_b128 v[236:239], v191 offset:6144
	ds_read_b128 v[240:243], v191 offset:7168
	global_load_lds_dwordx4 v[194:195], off
	v_lshl_add_u64 v[182:183], s[4:5], 0, v[182:183]
	s_mov_b32 m0, s69
	s_nop 0
	global_load_lds_dwordx4 v[182:183], off
	s_waitcnt vmcnt(8)
	s_waitcnt lgkmcnt(0)
	s_barrier
	s_setprio 1
	s_waitcnt lgkmcnt(0)
	v_mfma_scale_f32_16x16x128_f8f6f4 v[30:33], v[2:9], v[212:219], v[30:33], v190, v190 op_sel_hi:[0,0,0]
	v_mfma_scale_f32_16x16x128_f8f6f4 v[150:153], v[10:17], v[212:219], v[150:153], v190, v190 op_sel_hi:[0,0,0]
	v_mfma_scale_f32_16x16x128_f8f6f4 v[90:93], v[2:9], v[220:227], v[90:93], v190, v190 op_sel_hi:[0,0,0]
	v_mfma_scale_f32_16x16x128_f8f6f4 v[42:45], v[10:17], v[220:227], v[42:45], v190, v190 op_sel_hi:[0,0,0]
	v_mfma_scale_f32_16x16x128_f8f6f4 v[114:117], v[2:9], v[228:235], v[114:117], v190, v190 op_sel_hi:[0,0,0]
	v_mfma_scale_f32_16x16x128_f8f6f4 v[62:65], v[10:17], v[228:235], v[62:65], v190, v190 op_sel_hi:[0,0,0]
	v_mfma_scale_f32_16x16x128_f8f6f4 v[78:81], v[2:9], v[236:243], v[78:81], v190, v190 op_sel_hi:[0,0,0]
	v_mfma_scale_f32_16x16x128_f8f6f4 v[50:53], v[10:17], v[236:243], v[50:53], v190, v190 op_sel_hi:[0,0,0]
	s_setprio 0
	s_setprio 1
	v_mfma_scale_f32_16x16x128_f8f6f4 v[142:145], v[196:203], v[212:219], v[142:145], v190, v190 op_sel_hi:[0,0,0]
	v_mfma_scale_f32_16x16x128_f8f6f4 v[146:149], v[204:211], v[212:219], v[146:149], v190, v190 op_sel_hi:[0,0,0]
	v_mfma_scale_f32_16x16x128_f8f6f4 v[26:29], v[196:203], v[220:227], v[26:29], v190, v190 op_sel_hi:[0,0,0]
	v_mfma_scale_f32_16x16x128_f8f6f4 v[138:141], v[204:211], v[220:227], v[138:141], v190, v190 op_sel_hi:[0,0,0]
	v_mfma_scale_f32_16x16x128_f8f6f4 v[38:41], v[196:203], v[228:235], v[38:41], v190, v190 op_sel_hi:[0,0,0]
	v_mfma_scale_f32_16x16x128_f8f6f4 v[126:129], v[204:211], v[228:235], v[126:129], v190, v190 op_sel_hi:[0,0,0]
	v_mfma_scale_f32_16x16x128_f8f6f4 v[22:25], v[196:203], v[236:243], v[22:25], v190, v190 op_sel_hi:[0,0,0]
	v_mfma_scale_f32_16x16x128_f8f6f4 v[74:77], v[204:211], v[236:243], v[74:77], v190, v190 op_sel_hi:[0,0,0]
	s_setprio 2
	s_barrier
	s_mov_b32 m0, s70
	ds_read_b128 v[212:215], v191 offset:16384
	ds_read_b128 v[216:219], v191 offset:17408
	ds_read_b128 v[220:223], v191 offset:18432
	ds_read_b128 v[224:227], v191 offset:19456
	ds_read_b128 v[228:231], v191 offset:20480
	ds_read_b128 v[232:235], v191 offset:21504
	ds_read_b128 v[236:239], v191 offset:22528
	ds_read_b128 v[240:243], v191 offset:23552
	global_load_lds_dwordx4 v[180:181], off
	s_mov_b32 m0, s71
	s_nop 0
	global_load_lds_dwordx4 v[178:179], off
	s_mov_b32 m0, s72
	s_nop 0
	global_load_lds_dwordx4 v[176:177], off
	s_mov_b32 m0, s73
	s_nop 0
	global_load_lds_dwordx4 v[174:175], off
	s_mov_b32 m0, s67
	s_nop 0
	global_load_lds_dwordx4 v[172:173], off
	s_mov_b32 m0, s68
	s_nop 0
	global_load_lds_dwordx4 v[170:171], off
	s_waitcnt vmcnt(8)
	s_waitcnt lgkmcnt(0)
	s_barrier
	s_setprio 1
	s_waitcnt lgkmcnt(0)
	v_mfma_scale_f32_16x16x128_f8f6f4 v[134:137], v[2:9], v[212:219], v[134:137], v190, v190 op_sel_hi:[0,0,0]
	v_mfma_scale_f32_16x16x128_f8f6f4 v[102:105], v[10:17], v[212:219], v[102:105], v190, v190 op_sel_hi:[0,0,0]
	v_mfma_scale_f32_16x16x128_f8f6f4 v[122:125], v[2:9], v[220:227], v[122:125], v190, v190 op_sel_hi:[0,0,0]
	v_mfma_scale_f32_16x16x128_f8f6f4 v[98:101], v[10:17], v[220:227], v[98:101], v190, v190 op_sel_hi:[0,0,0]
	v_mfma_scale_f32_16x16x128_f8f6f4 v[110:113], v[2:9], v[228:235], v[110:113], v190, v190 op_sel_hi:[0,0,0]
	v_mfma_scale_f32_16x16x128_f8f6f4 v[106:109], v[10:17], v[228:235], v[106:109], v190, v190 op_sel_hi:[0,0,0]
	v_mfma_scale_f32_16x16x128_f8f6f4 v[86:89], v[2:9], v[236:243], v[86:89], v190, v190 op_sel_hi:[0,0,0]
	v_mfma_scale_f32_16x16x128_f8f6f4 v[82:85], v[10:17], v[236:243], v[82:85], v190, v190 op_sel_hi:[0,0,0]
	s_setprio 0
	s_setprio 1
	v_mfma_scale_f32_16x16x128_f8f6f4 v[34:37], v[196:203], v[212:219], v[34:37], v190, v190 op_sel_hi:[0,0,0]
	v_mfma_scale_f32_16x16x128_f8f6f4 v[130:133], v[204:211], v[212:219], v[130:133], v190, v190 op_sel_hi:[0,0,0]
	v_mfma_scale_f32_16x16x128_f8f6f4 v[46:49], v[196:203], v[220:227], v[46:49], v190, v190 op_sel_hi:[0,0,0]
	v_mfma_scale_f32_16x16x128_f8f6f4 v[118:121], v[204:211], v[220:227], v[118:121], v190, v190 op_sel_hi:[0,0,0]
	v_mfma_scale_f32_16x16x128_f8f6f4 v[66:69], v[196:203], v[228:235], v[66:69], v190, v190 op_sel_hi:[0,0,0]
	v_mfma_scale_f32_16x16x128_f8f6f4 v[94:97], v[204:211], v[228:235], v[94:97], v190, v190 op_sel_hi:[0,0,0]
	v_mfma_scale_f32_16x16x128_f8f6f4 v[54:57], v[196:203], v[236:243], v[54:57], v190, v190 op_sel_hi:[0,0,0]
	v_mfma_scale_f32_16x16x128_f8f6f4 v[58:61], v[204:211], v[236:243], v[58:61], v190, v190 op_sel_hi:[0,0,0]
	s_setprio 2
	s_barrier
	ds_read_b128 v[2:5], v193
	ds_read_b128 v[6:9], v193 offset:1024
	ds_read_b128 v[10:13], v193 offset:2048
	ds_read_b128 v[14:17], v193 offset:3072
	ds_read_b128 v[170:173], v192
	ds_read_b128 v[174:177], v192 offset:1024
	ds_read_b128 v[194:197], v192 offset:2048
	ds_read_b128 v[198:201], v192 offset:3072
	s_mov_b32 m0, s48
	ds_read_b128 v[202:205], v191 offset:32768
	ds_read_b128 v[206:209], v191 offset:33792
	ds_read_b128 v[210:213], v191 offset:34816
	ds_read_b128 v[214:217], v191 offset:35840
	ds_read_b128 v[218:221], v191 offset:36864
	ds_read_b128 v[222:225], v191 offset:37888
	ds_read_b128 v[226:229], v191 offset:38912
	ds_read_b128 v[230:233], v191 offset:39936
	global_load_lds_dwordx4 v[166:167], off
	s_mov_b32 m0, s49
	s_nop 0
	global_load_lds_dwordx4 v[168:169], off
	s_waitcnt vmcnt(8)
	s_waitcnt lgkmcnt(0)
	s_barrier
	s_setprio 1
	s_waitcnt lgkmcnt(0)
	v_mfma_scale_f32_16x16x128_f8f6f4 v[30:33], v[2:9], v[202:209], v[30:33], v190, v190 op_sel_hi:[0,0,0]
	v_mfma_scale_f32_16x16x128_f8f6f4 v[150:153], v[10:17], v[202:209], v[150:153], v190, v190 op_sel_hi:[0,0,0]
	v_mfma_scale_f32_16x16x128_f8f6f4 v[90:93], v[2:9], v[210:217], v[90:93], v190, v190 op_sel_hi:[0,0,0]
	v_mfma_scale_f32_16x16x128_f8f6f4 v[42:45], v[10:17], v[210:217], v[42:45], v190, v190 op_sel_hi:[0,0,0]
	v_mfma_scale_f32_16x16x128_f8f6f4 v[114:117], v[2:9], v[218:225], v[114:117], v190, v190 op_sel_hi:[0,0,0]
	v_mfma_scale_f32_16x16x128_f8f6f4 v[62:65], v[10:17], v[218:225], v[62:65], v190, v190 op_sel_hi:[0,0,0]
	v_mfma_scale_f32_16x16x128_f8f6f4 v[78:81], v[2:9], v[226:233], v[78:81], v190, v190 op_sel_hi:[0,0,0]
	v_mfma_scale_f32_16x16x128_f8f6f4 v[50:53], v[10:17], v[226:233], v[50:53], v190, v190 op_sel_hi:[0,0,0]
	s_setprio 0
	s_setprio 1
	v_mfma_scale_f32_16x16x128_f8f6f4 v[142:145], v[170:177], v[202:209], v[142:145], v190, v190 op_sel_hi:[0,0,0]
	v_mfma_scale_f32_16x16x128_f8f6f4 v[146:149], v[194:201], v[202:209], v[146:149], v190, v190 op_sel_hi:[0,0,0]
	v_mfma_scale_f32_16x16x128_f8f6f4 v[26:29], v[170:177], v[210:217], v[26:29], v190, v190 op_sel_hi:[0,0,0]
	v_mfma_scale_f32_16x16x128_f8f6f4 v[138:141], v[194:201], v[210:217], v[138:141], v190, v190 op_sel_hi:[0,0,0]
	v_mfma_scale_f32_16x16x128_f8f6f4 v[38:41], v[170:177], v[218:225], v[38:41], v190, v190 op_sel_hi:[0,0,0]
	v_mfma_scale_f32_16x16x128_f8f6f4 v[126:129], v[194:201], v[218:225], v[126:129], v190, v190 op_sel_hi:[0,0,0]
	v_mfma_scale_f32_16x16x128_f8f6f4 v[22:25], v[170:177], v[226:233], v[22:25], v190, v190 op_sel_hi:[0,0,0]
	v_mfma_scale_f32_16x16x128_f8f6f4 v[74:77], v[194:201], v[226:233], v[74:77], v190, v190 op_sel_hi:[0,0,0]
	s_setprio 2
	s_barrier
	s_mov_b32 m0, s9
	ds_read_b128 v[202:205], v191 offset:49152
	ds_read_b128 v[206:209], v191 offset:50176
	ds_read_b128 v[210:213], v191 offset:51200
	ds_read_b128 v[214:217], v191 offset:52224
	ds_read_b128 v[218:221], v191 offset:53248
	ds_read_b128 v[222:225], v191 offset:54272
	ds_read_b128 v[226:229], v191 offset:55296
	ds_read_b128 v[230:233], v191 offset:56320
	global_load_lds_dwordx4 v[72:73], off
	s_mov_b32 m0, s19
	s_nop 0
	global_load_lds_dwordx4 v[158:159], off
	s_mov_b32 m0, s44
	s_nop 0
	global_load_lds_dwordx4 v[162:163], off
	s_mov_b32 m0, s45
	s_nop 0
	global_load_lds_dwordx4 v[164:165], off
	s_mov_b32 m0, s18
	s_nop 0
	global_load_lds_dwordx4 v[70:71], off
	s_mov_b32 m0, s43
	s_nop 0
	global_load_lds_dwordx4 v[160:161], off
	s_waitcnt vmcnt(8)
	s_waitcnt lgkmcnt(0)
	s_barrier
	s_setprio 1
	s_waitcnt lgkmcnt(0)
	v_mfma_scale_f32_16x16x128_f8f6f4 v[134:137], v[2:9], v[202:209], v[134:137], v190, v190 op_sel_hi:[0,0,0]
	v_mfma_scale_f32_16x16x128_f8f6f4 v[102:105], v[10:17], v[202:209], v[102:105], v190, v190 op_sel_hi:[0,0,0]
	v_mfma_scale_f32_16x16x128_f8f6f4 v[122:125], v[2:9], v[210:217], v[122:125], v190, v190 op_sel_hi:[0,0,0]
	v_mfma_scale_f32_16x16x128_f8f6f4 v[98:101], v[10:17], v[210:217], v[98:101], v190, v190 op_sel_hi:[0,0,0]
	v_mfma_scale_f32_16x16x128_f8f6f4 v[110:113], v[2:9], v[218:225], v[110:113], v190, v190 op_sel_hi:[0,0,0]
	v_mfma_scale_f32_16x16x128_f8f6f4 v[106:109], v[10:17], v[218:225], v[106:109], v190, v190 op_sel_hi:[0,0,0]
	v_mfma_scale_f32_16x16x128_f8f6f4 v[86:89], v[2:9], v[226:233], v[86:89], v190, v190 op_sel_hi:[0,0,0]
	v_mfma_scale_f32_16x16x128_f8f6f4 v[82:85], v[10:17], v[226:233], v[82:85], v190, v190 op_sel_hi:[0,0,0]
	s_setprio 0
	s_setprio 1
	v_mfma_scale_f32_16x16x128_f8f6f4 v[34:37], v[170:177], v[202:209], v[34:37], v190, v190 op_sel_hi:[0,0,0]
	v_mfma_scale_f32_16x16x128_f8f6f4 v[130:133], v[194:201], v[202:209], v[130:133], v190, v190 op_sel_hi:[0,0,0]
	v_mfma_scale_f32_16x16x128_f8f6f4 v[46:49], v[170:177], v[210:217], v[46:49], v190, v190 op_sel_hi:[0,0,0]
	v_mfma_scale_f32_16x16x128_f8f6f4 v[118:121], v[194:201], v[210:217], v[118:121], v190, v190 op_sel_hi:[0,0,0]
	v_mfma_scale_f32_16x16x128_f8f6f4 v[66:69], v[170:177], v[218:225], v[66:69], v190, v190 op_sel_hi:[0,0,0]
	v_mfma_scale_f32_16x16x128_f8f6f4 v[94:97], v[194:201], v[218:225], v[94:97], v190, v190 op_sel_hi:[0,0,0]
	v_mfma_scale_f32_16x16x128_f8f6f4 v[54:57], v[170:177], v[226:233], v[54:57], v190, v190 op_sel_hi:[0,0,0]
	v_mfma_scale_f32_16x16x128_f8f6f4 v[58:61], v[194:201], v[226:233], v[58:61], v190, v190 op_sel_hi:[0,0,0]
	s_setprio 2
	s_barrier
	s_waitcnt vmcnt(0)
	s_cmpk_gt_u32 s65, 0xff
	s_cbranch_scc1 .LBB0_1439
	s_barrier

.LBB0_1681:
	ds_read_b128 v[26:29], v189
	ds_read_b128 v[30:33], v189 offset:1024
	ds_read_b128 v[18:21], v189 offset:2048
	ds_read_b128 v[22:25], v189 offset:3072
	ds_read_b128 v[10:13], v190
	ds_read_b128 v[14:17], v190 offset:1024
	ds_read_b128 v[2:5], v190 offset:2048
	ds_read_b128 v[6:9], v190 offset:3072
	s_add_u32 s34, s30, 0xfff80080
	s_addc_u32 s35, s31, -1
	s_cmp_eq_u32 s60, 28
	s_cselect_b32 s37, s18, s35
	s_cselect_b32 s36, s19, s34
	s_cselect_b32 s35, s21, s59
	s_cselect_b32 s34, s23, s58
	v_lshl_add_u64 v[218:219], s[30:31], 0, v[170:171]
	s_add_i32 m0, s29, 0xc000
	ds_read_b128 v[178:181], v191
	ds_read_b128 v[182:185], v191 offset:1024
	ds_read_b128 v[194:197], v191 offset:2048
	ds_read_b128 v[198:201], v191 offset:3072
	ds_read_b128 v[202:205], v191 offset:4096
	ds_read_b128 v[206:209], v191 offset:5120
	ds_read_b128 v[210:213], v191 offset:6144
	ds_read_b128 v[214:217], v191 offset:7168
	global_load_lds_dwordx4 v[218:219], off
	v_lshl_add_u64 v[218:219], s[30:31], 0, v[172:173]
	s_add_i32 m0, s29, 0xe000
	s_nop 0
	global_load_lds_dwordx4 v[218:219], off
	s_waitcnt vmcnt(8)
	s_waitcnt lgkmcnt(0)
	s_barrier
	s_setprio 1
	s_waitcnt lgkmcnt(0)
	v_mfma_scale_f32_16x16x128_f8f6f4 v[158:161], v[26:33], v[178:185], v[158:161], v1, v1 op_sel_hi:[0,0,0]
	v_mfma_scale_f32_16x16x128_f8f6f4 v[154:157], v[18:25], v[178:185], v[154:157], v1, v1 op_sel_hi:[0,0,0]
	v_mfma_scale_f32_16x16x128_f8f6f4 v[142:145], v[26:33], v[194:201], v[142:145], v1, v1 op_sel_hi:[0,0,0]
	v_mfma_scale_f32_16x16x128_f8f6f4 v[138:141], v[18:25], v[194:201], v[138:141], v1, v1 op_sel_hi:[0,0,0]
	v_mfma_scale_f32_16x16x128_f8f6f4 v[126:129], v[26:33], v[202:209], v[126:129], v1, v1 op_sel_hi:[0,0,0]
	v_mfma_scale_f32_16x16x128_f8f6f4 v[122:125], v[18:25], v[202:209], v[122:125], v1, v1 op_sel_hi:[0,0,0]
	v_mfma_scale_f32_16x16x128_f8f6f4 v[110:113], v[26:33], v[210:217], v[110:113], v1, v1 op_sel_hi:[0,0,0]
	v_mfma_scale_f32_16x16x128_f8f6f4 v[106:109], v[18:25], v[210:217], v[106:109], v1, v1 op_sel_hi:[0,0,0]
	s_setprio 0
	s_setprio 1
	v_mfma_scale_f32_16x16x128_f8f6f4 v[150:153], v[10:17], v[178:185], v[150:153], v1, v1 op_sel_hi:[0,0,0]
	v_mfma_scale_f32_16x16x128_f8f6f4 v[146:149], v[2:9], v[178:185], v[146:149], v1, v1 op_sel_hi:[0,0,0]
	v_mfma_scale_f32_16x16x128_f8f6f4 v[134:137], v[10:17], v[194:201], v[134:137], v1, v1 op_sel_hi:[0,0,0]
	v_mfma_scale_f32_16x16x128_f8f6f4 v[130:133], v[2:9], v[194:201], v[130:133], v1, v1 op_sel_hi:[0,0,0]
	v_mfma_scale_f32_16x16x128_f8f6f4 v[118:121], v[10:17], v[202:209], v[118:121], v1, v1 op_sel_hi:[0,0,0]
	v_mfma_scale_f32_16x16x128_f8f6f4 v[114:117], v[2:9], v[202:209], v[114:117], v1, v1 op_sel_hi:[0,0,0]
	v_mfma_scale_f32_16x16x128_f8f6f4 v[102:105], v[10:17], v[210:217], v[102:105], v1, v1 op_sel_hi:[0,0,0]
	v_mfma_scale_f32_16x16x128_f8f6f4 v[98:101], v[2:9], v[210:217], v[98:101], v1, v1 op_sel_hi:[0,0,0]
	s_setprio 2
	s_barrier
	s_add_i32 s61, s45, s3
	v_lshl_add_u64 v[178:179], s[34:35], 0, v[166:167]
	s_mov_b32 m0, s61
	ds_read_b128 v[194:197], v191 offset:16384
	ds_read_b128 v[198:201], v191 offset:17408
	ds_read_b128 v[202:205], v191 offset:18432
	ds_read_b128 v[206:209], v191 offset:19456
	ds_read_b128 v[210:213], v191 offset:20480
	ds_read_b128 v[214:217], v191 offset:21504
	ds_read_b128 v[218:221], v191 offset:22528
	ds_read_b128 v[222:225], v191 offset:23552
	global_load_lds_dwordx4 v[178:179], off
	s_add_i32 m0, s61, 0x2000
	s_add_u32 s62, s34, 0x80000
	v_lshl_add_u64 v[180:181], s[34:35], 0, v[162:163]
	s_addc_u32 s63, s35, 0
	s_add_i32 s61, s48, s3
	global_load_lds_dwordx4 v[180:181], off
	v_lshl_add_u64 v[182:183], s[62:63], 0, v[166:167]
	s_mov_b32 m0, s61
	v_lshl_add_u64 v[184:185], s[36:37], 0, v[164:165]
	global_load_lds_dwordx4 v[182:183], off
	v_lshl_add_u64 v[182:183], s[62:63], 0, v[162:163]
	s_add_i32 m0, s61, 0x2000
	s_nop 0
	global_load_lds_dwordx4 v[182:183], off
	v_lshl_add_u64 v[182:183], s[36:37], 0, v[168:169]
	s_mov_b32 m0, s29
	s_nop 0
	global_load_lds_dwordx4 v[182:183], off
	s_mov_b32 m0, s38
	s_nop 0
	global_load_lds_dwordx4 v[184:185], off
	s_waitcnt vmcnt(8)
	s_waitcnt lgkmcnt(0)
	s_barrier
	s_setprio 1
	s_waitcnt lgkmcnt(0)
	v_mfma_scale_f32_16x16x128_f8f6f4 v[94:97], v[26:33], v[194:201], v[94:97], v1, v1 op_sel_hi:[0,0,0]
	v_mfma_scale_f32_16x16x128_f8f6f4 v[90:93], v[18:25], v[194:201], v[90:93], v1, v1 op_sel_hi:[0,0,0]
	v_mfma_scale_f32_16x16x128_f8f6f4 v[78:81], v[26:33], v[202:209], v[78:81], v1, v1 op_sel_hi:[0,0,0]
	v_mfma_scale_f32_16x16x128_f8f6f4 v[74:77], v[18:25], v[202:209], v[74:77], v1, v1 op_sel_hi:[0,0,0]
	v_mfma_scale_f32_16x16x128_f8f6f4 v[62:65], v[26:33], v[210:217], v[62:65], v1, v1 op_sel_hi:[0,0,0]
	v_mfma_scale_f32_16x16x128_f8f6f4 v[58:61], v[18:25], v[210:217], v[58:61], v1, v1 op_sel_hi:[0,0,0]
	v_mfma_scale_f32_16x16x128_f8f6f4 v[46:49], v[26:33], v[218:225], v[46:49], v1, v1 op_sel_hi:[0,0,0]
	v_mfma_scale_f32_16x16x128_f8f6f4 v[42:45], v[18:25], v[218:225], v[42:45], v1, v1 op_sel_hi:[0,0,0]
	s_setprio 0
	s_setprio 1
	v_mfma_scale_f32_16x16x128_f8f6f4 v[86:89], v[10:17], v[194:201], v[86:89], v1, v1 op_sel_hi:[0,0,0]
	v_mfma_scale_f32_16x16x128_f8f6f4 v[82:85], v[2:9], v[194:201], v[82:85], v1, v1 op_sel_hi:[0,0,0]
	v_mfma_scale_f32_16x16x128_f8f6f4 v[70:73], v[10:17], v[202:209], v[70:73], v1, v1 op_sel_hi:[0,0,0]
	v_mfma_scale_f32_16x16x128_f8f6f4 v[66:69], v[2:9], v[202:209], v[66:69], v1, v1 op_sel_hi:[0,0,0]
	v_mfma_scale_f32_16x16x128_f8f6f4 v[54:57], v[10:17], v[210:217], v[54:57], v1, v1 op_sel_hi:[0,0,0]
	v_mfma_scale_f32_16x16x128_f8f6f4 v[50:53], v[2:9], v[210:217], v[50:53], v1, v1 op_sel_hi:[0,0,0]
	v_mfma_scale_f32_16x16x128_f8f6f4 v[38:41], v[10:17], v[218:225], v[38:41], v1, v1 op_sel_hi:[0,0,0]
	v_mfma_scale_f32_16x16x128_f8f6f4 v[34:37], v[2:9], v[218:225], v[34:37], v1, v1 op_sel_hi:[0,0,0]
	s_setprio 2
	s_barrier
	s_add_i32 s61, 0, 0x18000
	s_add_i32 s62, 0, 0x1c000
	v_add_u32_e32 v14, s61, v187
	v_add_u32_e32 v30, s62, v187
	ds_read_b128 v[2:5], v14
	ds_read_b128 v[6:9], v14 offset:1024
	ds_read_b128 v[10:13], v14 offset:2048
	ds_read_b128 v[14:17], v14 offset:3072
	ds_read_b128 v[18:21], v30
	ds_read_b128 v[22:25], v30 offset:1024
	ds_read_b128 v[26:29], v30 offset:2048
	ds_read_b128 v[30:33], v30 offset:3072
	s_add_u32 s36, s36, 0x80000
	s_addc_u32 s37, s37, 0
	s_mov_b32 m0, s39
	v_lshl_add_u64 v[226:227], s[36:37], 0, v[168:169]
	ds_read_b128 v[194:197], v191 offset:32768
	ds_read_b128 v[198:201], v191 offset:33792
	ds_read_b128 v[202:205], v191 offset:34816
	ds_read_b128 v[206:209], v191 offset:35840
	ds_read_b128 v[210:213], v191 offset:36864
	ds_read_b128 v[214:217], v191 offset:37888
	ds_read_b128 v[218:221], v191 offset:38912
	ds_read_b128 v[222:225], v191 offset:39936
	global_load_lds_dwordx4 v[226:227], off
	v_lshl_add_u64 v[226:227], s[36:37], 0, v[164:165]
	s_mov_b32 m0, s40
	s_nop 0
	global_load_lds_dwordx4 v[226:227], off
	s_waitcnt vmcnt(8)
	s_waitcnt lgkmcnt(0)
	s_barrier
	s_setprio 1
	s_waitcnt lgkmcnt(0)
	v_mfma_scale_f32_16x16x128_f8f6f4 v[158:161], v[2:9], v[194:201], v[158:161], v1, v1 op_sel_hi:[0,0,0]
	v_mfma_scale_f32_16x16x128_f8f6f4 v[154:157], v[10:17], v[194:201], v[154:157], v1, v1 op_sel_hi:[0,0,0]
	v_mfma_scale_f32_16x16x128_f8f6f4 v[142:145], v[2:9], v[202:209], v[142:145], v1, v1 op_sel_hi:[0,0,0]
	v_mfma_scale_f32_16x16x128_f8f6f4 v[138:141], v[10:17], v[202:209], v[138:141], v1, v1 op_sel_hi:[0,0,0]
	v_mfma_scale_f32_16x16x128_f8f6f4 v[126:129], v[2:9], v[210:217], v[126:129], v1, v1 op_sel_hi:[0,0,0]
	v_mfma_scale_f32_16x16x128_f8f6f4 v[122:125], v[10:17], v[210:217], v[122:125], v1, v1 op_sel_hi:[0,0,0]
	v_mfma_scale_f32_16x16x128_f8f6f4 v[110:113], v[2:9], v[218:225], v[110:113], v1, v1 op_sel_hi:[0,0,0]
	v_mfma_scale_f32_16x16x128_f8f6f4 v[106:109], v[10:17], v[218:225], v[106:109], v1, v1 op_sel_hi:[0,0,0]
	s_setprio 0
	s_setprio 1
	v_mfma_scale_f32_16x16x128_f8f6f4 v[150:153], v[18:25], v[194:201], v[150:153], v1, v1 op_sel_hi:[0,0,0]
	v_mfma_scale_f32_16x16x128_f8f6f4 v[146:149], v[26:33], v[194:201], v[146:149], v1, v1 op_sel_hi:[0,0,0]
	v_mfma_scale_f32_16x16x128_f8f6f4 v[134:137], v[18:25], v[202:209], v[134:137], v1, v1 op_sel_hi:[0,0,0]
	v_mfma_scale_f32_16x16x128_f8f6f4 v[130:133], v[26:33], v[202:209], v[130:133], v1, v1 op_sel_hi:[0,0,0]
	v_mfma_scale_f32_16x16x128_f8f6f4 v[118:121], v[18:25], v[210:217], v[118:121], v1, v1 op_sel_hi:[0,0,0]
	v_mfma_scale_f32_16x16x128_f8f6f4 v[114:117], v[26:33], v[210:217], v[114:117], v1, v1 op_sel_hi:[0,0,0]
	v_mfma_scale_f32_16x16x128_f8f6f4 v[102:105], v[18:25], v[218:225], v[102:105], v1, v1 op_sel_hi:[0,0,0]
	v_mfma_scale_f32_16x16x128_f8f6f4 v[98:101], v[26:33], v[218:225], v[98:101], v1, v1 op_sel_hi:[0,0,0]
	s_setprio 2
	s_barrier
	s_add_i32 s36, s61, s3
	v_lshl_add_u64 v[178:179], v[178:179], 0, s[8:9]
	s_mov_b32 m0, s36
	ds_read_b128 v[194:197], v191 offset:49152
	ds_read_b128 v[198:201], v191 offset:50176
	ds_read_b128 v[202:205], v191 offset:51200
	ds_read_b128 v[206:209], v191 offset:52224
	ds_read_b128 v[210:213], v191 offset:53248
	ds_read_b128 v[214:217], v191 offset:54272
	ds_read_b128 v[218:221], v191 offset:55296
	ds_read_b128 v[222:225], v191 offset:56320
	global_load_lds_dwordx4 v[178:179], off
	s_add_i32 m0, s36, 0x2000
	s_add_u32 s34, s34, 0x80080
	v_lshl_add_u64 v[178:179], v[180:181], 0, s[8:9]
	s_addc_u32 s35, s35, 0
	s_add_i32 s36, s62, s3
	global_load_lds_dwordx4 v[178:179], off
	v_lshl_add_u64 v[178:179], s[34:35], 0, v[166:167]
	s_mov_b32 m0, s36
	s_nop 0
	global_load_lds_dwordx4 v[178:179], off
	v_lshl_add_u64 v[178:179], s[34:35], 0, v[162:163]
	s_add_i32 m0, s36, 0x2000
	s_nop 0
	global_load_lds_dwordx4 v[178:179], off
	v_lshl_add_u64 v[178:179], v[182:183], 0, s[8:9]
	s_mov_b32 m0, s43
	s_nop 0
	global_load_lds_dwordx4 v[178:179], off
	v_lshl_add_u64 v[178:179], v[184:185], 0, s[8:9]
	s_mov_b32 m0, s44
	s_nop 0
	global_load_lds_dwordx4 v[178:179], off
	s_waitcnt vmcnt(8)
	s_waitcnt lgkmcnt(0)
	s_barrier
	s_setprio 1
	s_waitcnt lgkmcnt(0)
	v_mfma_scale_f32_16x16x128_f8f6f4 v[94:97], v[2:9], v[194:201], v[94:97], v1, v1 op_sel_hi:[0,0,0]
	v_mfma_scale_f32_16x16x128_f8f6f4 v[90:93], v[10:17], v[194:201], v[90:93], v1, v1 op_sel_hi:[0,0,0]
	v_mfma_scale_f32_16x16x128_f8f6f4 v[78:81], v[2:9], v[202:209], v[78:81], v1, v1 op_sel_hi:[0,0,0]
	v_mfma_scale_f32_16x16x128_f8f6f4 v[74:77], v[10:17], v[202:209], v[74:77], v1, v1 op_sel_hi:[0,0,0]
	v_mfma_scale_f32_16x16x128_f8f6f4 v[62:65], v[2:9], v[210:217], v[62:65], v1, v1 op_sel_hi:[0,0,0]
	v_mfma_scale_f32_16x16x128_f8f6f4 v[58:61], v[10:17], v[210:217], v[58:61], v1, v1 op_sel_hi:[0,0,0]
	v_mfma_scale_f32_16x16x128_f8f6f4 v[46:49], v[2:9], v[218:225], v[46:49], v1, v1 op_sel_hi:[0,0,0]
	v_mfma_scale_f32_16x16x128_f8f6f4 v[42:45], v[10:17], v[218:225], v[42:45], v1, v1 op_sel_hi:[0,0,0]
	s_setprio 0
	s_setprio 1
	v_mfma_scale_f32_16x16x128_f8f6f4 v[86:89], v[18:25], v[194:201], v[86:89], v1, v1 op_sel_hi:[0,0,0]
	v_mfma_scale_f32_16x16x128_f8f6f4 v[82:85], v[26:33], v[194:201], v[82:85], v1, v1 op_sel_hi:[0,0,0]
	v_mfma_scale_f32_16x16x128_f8f6f4 v[70:73], v[18:25], v[202:209], v[70:73], v1, v1 op_sel_hi:[0,0,0]
	v_mfma_scale_f32_16x16x128_f8f6f4 v[66:69], v[26:33], v[202:209], v[66:69], v1, v1 op_sel_hi:[0,0,0]
	v_mfma_scale_f32_16x16x128_f8f6f4 v[54:57], v[18:25], v[210:217], v[54:57], v1, v1 op_sel_hi:[0,0,0]
	v_mfma_scale_f32_16x16x128_f8f6f4 v[50:53], v[26:33], v[210:217], v[50:53], v1, v1 op_sel_hi:[0,0,0]
	v_mfma_scale_f32_16x16x128_f8f6f4 v[38:41], v[18:25], v[218:225], v[38:41], v1, v1 op_sel_hi:[0,0,0]
	v_mfma_scale_f32_16x16x128_f8f6f4 v[34:37], v[26:33], v[218:225], v[34:37], v1, v1 op_sel_hi:[0,0,0]
	s_setprio 2
	s_barrier
	s_add_i32 s60, s60, 2
	s_add_u32 s30, s30, 0x100
	s_addc_u32 s31, s31, 0
	s_add_u32 s58, s58, 0x100
	s_addc_u32 s59, s59, 0
	s_cmp_gt_u32 s60, 29
	s_cbranch_scc0 .LBB0_1681
	s_and_b64 vcc, exec, s[12:13]
	s_cbranch_vccz .LBB0_1684
	s_barrier

.LBB0_1745:
	s_add_u32 s8, s49, s6
	s_addc_u32 s9, s50, s7
	s_add_u32 s8, s8, 0x32800100
	s_addc_u32 s9, s9, 0
	s_add_u32 s73, s51, s6
	s_addc_u32 s74, s54, s7
	s_add_i32 s72, 0, 0x10000
	s_cmpk_eq_i32 s6, 0x2a00
	s_cselect_b32 s37, s5, s9
	s_cselect_b32 s36, s4, s8
	s_cselect_b32 s9, s13, s74
	s_cselect_b32 s8, s12, s73
	s_add_i32 s73, 0, 0x14000
	v_add_u32_e32 v2, s72, v188
	v_add_u32_e32 v6, s73, v188
	ds_read_b128 v[26:29], v2
	ds_read_b128 v[30:33], v2 offset:1024
	ds_read_b128 v[18:21], v2 offset:2048
	ds_read_b128 v[22:25], v2 offset:3072
	ds_read_b128 v[10:13], v6
	ds_read_b128 v[14:17], v6 offset:1024
	ds_read_b128 v[2:5], v6 offset:2048
	ds_read_b128 v[6:9], v6 offset:3072
	v_lshl_add_u64 v[214:215], v[168:169], 0, s[6:7]
	s_add_i32 m0, s64, 0xc000
	ds_read_b128 v[172:175], v189
	ds_read_b128 v[176:179], v189 offset:1024
	ds_read_b128 v[190:193], v189 offset:2048
	ds_read_b128 v[194:197], v189 offset:3072
	ds_read_b128 v[198:201], v189 offset:4096
	ds_read_b128 v[202:205], v189 offset:5120
	ds_read_b128 v[206:209], v189 offset:6144
	ds_read_b128 v[210:213], v189 offset:7168
	global_load_lds_dwordx4 v[214:215], off
	v_lshl_add_u64 v[214:215], v[170:171], 0, s[6:7]
	s_add_i32 m0, s64, 0xe000
	s_nop 0
	global_load_lds_dwordx4 v[214:215], off
	s_waitcnt vmcnt(8)
	s_waitcnt lgkmcnt(0)
	s_barrier
	s_setprio 1
	s_waitcnt lgkmcnt(0)
	v_mfma_scale_f32_16x16x128_f8f6f4 v[158:161], v[26:33], v[172:179], v[158:161], v187, v187 op_sel_hi:[0,0,0]
	v_mfma_scale_f32_16x16x128_f8f6f4 v[154:157], v[18:25], v[172:179], v[154:157], v187, v187 op_sel_hi:[0,0,0]
	v_mfma_scale_f32_16x16x128_f8f6f4 v[122:125], v[26:33], v[190:197], v[122:125], v187, v187 op_sel_hi:[0,0,0]
	v_mfma_scale_f32_16x16x128_f8f6f4 v[118:121], v[18:25], v[190:197], v[118:121], v187, v187 op_sel_hi:[0,0,0]
	v_mfma_scale_f32_16x16x128_f8f6f4 v[126:129], v[26:33], v[198:205], v[126:129], v187, v187 op_sel_hi:[0,0,0]
	v_mfma_scale_f32_16x16x128_f8f6f4 v[114:117], v[18:25], v[198:205], v[114:117], v187, v187 op_sel_hi:[0,0,0]
	v_mfma_scale_f32_16x16x128_f8f6f4 v[110:113], v[26:33], v[206:213], v[110:113], v187, v187 op_sel_hi:[0,0,0]
	v_mfma_scale_f32_16x16x128_f8f6f4 v[106:109], v[18:25], v[206:213], v[106:109], v187, v187 op_sel_hi:[0,0,0]
	s_setprio 0
	s_setprio 1
	v_mfma_scale_f32_16x16x128_f8f6f4 v[150:153], v[10:17], v[172:179], v[150:153], v187, v187 op_sel_hi:[0,0,0]
	v_mfma_scale_f32_16x16x128_f8f6f4 v[146:149], v[2:9], v[172:179], v[146:149], v187, v187 op_sel_hi:[0,0,0]
	v_mfma_scale_f32_16x16x128_f8f6f4 v[142:145], v[10:17], v[190:197], v[142:145], v187, v187 op_sel_hi:[0,0,0]
	v_mfma_scale_f32_16x16x128_f8f6f4 v[138:141], v[2:9], v[190:197], v[138:141], v187, v187 op_sel_hi:[0,0,0]
	v_mfma_scale_f32_16x16x128_f8f6f4 v[134:137], v[10:17], v[198:205], v[134:137], v187, v187 op_sel_hi:[0,0,0]
	v_mfma_scale_f32_16x16x128_f8f6f4 v[130:133], v[2:9], v[198:205], v[130:133], v187, v187 op_sel_hi:[0,0,0]
	v_mfma_scale_f32_16x16x128_f8f6f4 v[102:105], v[10:17], v[206:213], v[102:105], v187, v187 op_sel_hi:[0,0,0]
	v_mfma_scale_f32_16x16x128_f8f6f4 v[98:101], v[2:9], v[206:213], v[98:101], v187, v187 op_sel_hi:[0,0,0]
	s_setprio 2
	s_barrier
	s_add_i32 s72, s72, s43
	v_lshl_add_u64 v[172:173], s[8:9], 0, v[162:163]
	s_mov_b32 m0, s72
	ds_read_b128 v[190:193], v189 offset:16384
	ds_read_b128 v[194:197], v189 offset:17408
	ds_read_b128 v[198:201], v189 offset:18432
	ds_read_b128 v[202:205], v189 offset:19456
	ds_read_b128 v[206:209], v189 offset:20480
	ds_read_b128 v[210:213], v189 offset:21504
	ds_read_b128 v[214:217], v189 offset:22528
	ds_read_b128 v[218:221], v189 offset:23552
	global_load_lds_dwordx4 v[172:173], off
	s_add_i32 m0, s72, 0x2000
	s_add_u32 s74, s8, 0x158000
	v_lshl_add_u64 v[174:175], s[8:9], 0, v[166:167]
	s_addc_u32 s75, s9, 0
	s_add_i32 s72, s73, s43
	global_load_lds_dwordx4 v[174:175], off
	v_lshl_add_u64 v[176:177], s[74:75], 0, v[162:163]
	s_mov_b32 m0, s72
	v_lshl_add_u64 v[178:179], s[36:37], 0, v[166:167]
	global_load_lds_dwordx4 v[176:177], off
	v_lshl_add_u64 v[176:177], s[74:75], 0, v[166:167]
	s_add_i32 m0, s72, 0x2000
	s_nop 0
	global_load_lds_dwordx4 v[176:177], off
	v_lshl_add_u64 v[176:177], s[36:37], 0, v[162:163]
	s_mov_b32 m0, s64
	s_nop 0
	global_load_lds_dwordx4 v[176:177], off
	s_mov_b32 m0, s65
	s_nop 0
	global_load_lds_dwordx4 v[178:179], off
	s_waitcnt vmcnt(8)
	s_waitcnt lgkmcnt(0)
	s_barrier
	s_setprio 1
	s_waitcnt lgkmcnt(0)
	v_mfma_scale_f32_16x16x128_f8f6f4 v[94:97], v[26:33], v[190:197], v[94:97], v187, v187 op_sel_hi:[0,0,0]
	v_mfma_scale_f32_16x16x128_f8f6f4 v[90:93], v[18:25], v[190:197], v[90:93], v187, v187 op_sel_hi:[0,0,0]
	v_mfma_scale_f32_16x16x128_f8f6f4 v[78:81], v[26:33], v[198:205], v[78:81], v187, v187 op_sel_hi:[0,0,0]
	v_mfma_scale_f32_16x16x128_f8f6f4 v[74:77], v[18:25], v[198:205], v[74:77], v187, v187 op_sel_hi:[0,0,0]
	v_mfma_scale_f32_16x16x128_f8f6f4 v[62:65], v[26:33], v[206:213], v[62:65], v187, v187 op_sel_hi:[0,0,0]
	v_mfma_scale_f32_16x16x128_f8f6f4 v[58:61], v[18:25], v[206:213], v[58:61], v187, v187 op_sel_hi:[0,0,0]
	v_mfma_scale_f32_16x16x128_f8f6f4 v[46:49], v[26:33], v[214:221], v[46:49], v187, v187 op_sel_hi:[0,0,0]
	v_mfma_scale_f32_16x16x128_f8f6f4 v[42:45], v[18:25], v[214:221], v[42:45], v187, v187 op_sel_hi:[0,0,0]
	s_setprio 0
	s_setprio 1
	v_mfma_scale_f32_16x16x128_f8f6f4 v[86:89], v[10:17], v[190:197], v[86:89], v187, v187 op_sel_hi:[0,0,0]
	v_mfma_scale_f32_16x16x128_f8f6f4 v[82:85], v[2:9], v[190:197], v[82:85], v187, v187 op_sel_hi:[0,0,0]
	v_mfma_scale_f32_16x16x128_f8f6f4 v[70:73], v[10:17], v[198:205], v[70:73], v187, v187 op_sel_hi:[0,0,0]
	v_mfma_scale_f32_16x16x128_f8f6f4 v[66:69], v[2:9], v[198:205], v[66:69], v187, v187 op_sel_hi:[0,0,0]
	v_mfma_scale_f32_16x16x128_f8f6f4 v[54:57], v[10:17], v[206:213], v[54:57], v187, v187 op_sel_hi:[0,0,0]
	v_mfma_scale_f32_16x16x128_f8f6f4 v[50:53], v[2:9], v[206:213], v[50:53], v187, v187 op_sel_hi:[0,0,0]
	v_mfma_scale_f32_16x16x128_f8f6f4 v[38:41], v[10:17], v[214:221], v[38:41], v187, v187 op_sel_hi:[0,0,0]
	v_mfma_scale_f32_16x16x128_f8f6f4 v[34:37], v[2:9], v[214:221], v[34:37], v187, v187 op_sel_hi:[0,0,0]
	s_setprio 2
	s_barrier
	s_add_i32 s72, 0, 0x18000
	s_add_i32 s73, 0, 0x1c000
	v_add_u32_e32 v14, s72, v188
	v_add_u32_e32 v30, s73, v188
	ds_read_b128 v[2:5], v14
	ds_read_b128 v[6:9], v14 offset:1024
	ds_read_b128 v[10:13], v14 offset:2048
	ds_read_b128 v[14:17], v14 offset:3072
	ds_read_b128 v[18:21], v30
	ds_read_b128 v[22:25], v30 offset:1024
	ds_read_b128 v[26:29], v30 offset:2048
	ds_read_b128 v[30:33], v30 offset:3072
	s_add_u32 s36, s36, 0x158000
	s_addc_u32 s37, s37, 0
	s_mov_b32 m0, s66
	v_lshl_add_u64 v[222:223], s[36:37], 0, v[162:163]
	ds_read_b128 v[190:193], v189 offset:32768
	ds_read_b128 v[194:197], v189 offset:33792
	ds_read_b128 v[198:201], v189 offset:34816
	ds_read_b128 v[202:205], v189 offset:35840
	ds_read_b128 v[206:209], v189 offset:36864
	ds_read_b128 v[210:213], v189 offset:37888
	ds_read_b128 v[214:217], v189 offset:38912
	ds_read_b128 v[218:221], v189 offset:39936
	global_load_lds_dwordx4 v[222:223], off
	v_lshl_add_u64 v[222:223], s[36:37], 0, v[166:167]
	s_mov_b32 m0, s67
	s_nop 0
	global_load_lds_dwordx4 v[222:223], off
	s_waitcnt vmcnt(8)
	s_waitcnt lgkmcnt(0)
	s_barrier
	s_setprio 1
	s_waitcnt lgkmcnt(0)
	v_mfma_scale_f32_16x16x128_f8f6f4 v[158:161], v[2:9], v[190:197], v[158:161], v187, v187 op_sel_hi:[0,0,0]
	v_mfma_scale_f32_16x16x128_f8f6f4 v[154:157], v[10:17], v[190:197], v[154:157], v187, v187 op_sel_hi:[0,0,0]
	v_mfma_scale_f32_16x16x128_f8f6f4 v[122:125], v[2:9], v[198:205], v[122:125], v187, v187 op_sel_hi:[0,0,0]
	v_mfma_scale_f32_16x16x128_f8f6f4 v[118:121], v[10:17], v[198:205], v[118:121], v187, v187 op_sel_hi:[0,0,0]
	v_mfma_scale_f32_16x16x128_f8f6f4 v[126:129], v[2:9], v[206:213], v[126:129], v187, v187 op_sel_hi:[0,0,0]
	v_mfma_scale_f32_16x16x128_f8f6f4 v[114:117], v[10:17], v[206:213], v[114:117], v187, v187 op_sel_hi:[0,0,0]
	v_mfma_scale_f32_16x16x128_f8f6f4 v[110:113], v[2:9], v[214:221], v[110:113], v187, v187 op_sel_hi:[0,0,0]
	v_mfma_scale_f32_16x16x128_f8f6f4 v[106:109], v[10:17], v[214:221], v[106:109], v187, v187 op_sel_hi:[0,0,0]
	s_setprio 0
	s_setprio 1
	v_mfma_scale_f32_16x16x128_f8f6f4 v[150:153], v[18:25], v[190:197], v[150:153], v187, v187 op_sel_hi:[0,0,0]
	v_mfma_scale_f32_16x16x128_f8f6f4 v[146:149], v[26:33], v[190:197], v[146:149], v187, v187 op_sel_hi:[0,0,0]
	v_mfma_scale_f32_16x16x128_f8f6f4 v[142:145], v[18:25], v[198:205], v[142:145], v187, v187 op_sel_hi:[0,0,0]
	v_mfma_scale_f32_16x16x128_f8f6f4 v[138:141], v[26:33], v[198:205], v[138:141], v187, v187 op_sel_hi:[0,0,0]
	v_mfma_scale_f32_16x16x128_f8f6f4 v[134:137], v[18:25], v[206:213], v[134:137], v187, v187 op_sel_hi:[0,0,0]
	v_mfma_scale_f32_16x16x128_f8f6f4 v[130:133], v[26:33], v[206:213], v[130:133], v187, v187 op_sel_hi:[0,0,0]
	v_mfma_scale_f32_16x16x128_f8f6f4 v[102:105], v[18:25], v[214:221], v[102:105], v187, v187 op_sel_hi:[0,0,0]
	v_mfma_scale_f32_16x16x128_f8f6f4 v[98:101], v[26:33], v[214:221], v[98:101], v187, v187 op_sel_hi:[0,0,0]
	s_setprio 2
	s_barrier
	s_add_i32 s36, s72, s43
	v_lshl_add_u64 v[172:173], v[172:173], 0, s[22:23]
	s_mov_b32 m0, s36
	ds_read_b128 v[190:193], v189 offset:49152
	ds_read_b128 v[194:197], v189 offset:50176
	ds_read_b128 v[198:201], v189 offset:51200
	ds_read_b128 v[202:205], v189 offset:52224
	ds_read_b128 v[206:209], v189 offset:53248
	ds_read_b128 v[210:213], v189 offset:54272
	ds_read_b128 v[214:217], v189 offset:55296
	ds_read_b128 v[218:221], v189 offset:56320
	global_load_lds_dwordx4 v[172:173], off
	s_add_i32 m0, s36, 0x2000
	s_add_u32 s8, s8, 0x158080
	v_lshl_add_u64 v[172:173], v[174:175], 0, s[22:23]
	s_addc_u32 s9, s9, 0
	s_add_i32 s36, s73, s43
	global_load_lds_dwordx4 v[172:173], off
	v_lshl_add_u64 v[172:173], s[8:9], 0, v[162:163]
	s_mov_b32 m0, s36
	s_nop 0
	global_load_lds_dwordx4 v[172:173], off
	v_lshl_add_u64 v[172:173], s[8:9], 0, v[166:167]
	s_add_i32 m0, s36, 0x2000
	s_nop 0
	global_load_lds_dwordx4 v[172:173], off
	v_lshl_add_u64 v[172:173], v[176:177], 0, s[22:23]
	s_mov_b32 m0, s69
	s_nop 0
	global_load_lds_dwordx4 v[172:173], off
	v_lshl_add_u64 v[172:173], v[178:179], 0, s[22:23]
	s_mov_b32 m0, s70
	s_nop 0
	global_load_lds_dwordx4 v[172:173], off
	s_waitcnt vmcnt(8)
	s_waitcnt lgkmcnt(0)
	s_barrier
	s_setprio 1
	s_waitcnt lgkmcnt(0)
	v_mfma_scale_f32_16x16x128_f8f6f4 v[94:97], v[2:9], v[190:197], v[94:97], v187, v187 op_sel_hi:[0,0,0]
	v_mfma_scale_f32_16x16x128_f8f6f4 v[90:93], v[10:17], v[190:197], v[90:93], v187, v187 op_sel_hi:[0,0,0]
	v_mfma_scale_f32_16x16x128_f8f6f4 v[78:81], v[2:9], v[198:205], v[78:81], v187, v187 op_sel_hi:[0,0,0]
	v_mfma_scale_f32_16x16x128_f8f6f4 v[74:77], v[10:17], v[198:205], v[74:77], v187, v187 op_sel_hi:[0,0,0]
	v_mfma_scale_f32_16x16x128_f8f6f4 v[62:65], v[2:9], v[206:213], v[62:65], v187, v187 op_sel_hi:[0,0,0]
	v_mfma_scale_f32_16x16x128_f8f6f4 v[58:61], v[10:17], v[206:213], v[58:61], v187, v187 op_sel_hi:[0,0,0]
	v_mfma_scale_f32_16x16x128_f8f6f4 v[46:49], v[2:9], v[214:221], v[46:49], v187, v187 op_sel_hi:[0,0,0]
	v_mfma_scale_f32_16x16x128_f8f6f4 v[42:45], v[10:17], v[214:221], v[42:45], v187, v187 op_sel_hi:[0,0,0]
	s_setprio 0
	s_setprio 1
	v_mfma_scale_f32_16x16x128_f8f6f4 v[86:89], v[18:25], v[190:197], v[86:89], v187, v187 op_sel_hi:[0,0,0]
	v_mfma_scale_f32_16x16x128_f8f6f4 v[82:85], v[26:33], v[190:197], v[82:85], v187, v187 op_sel_hi:[0,0,0]
	v_mfma_scale_f32_16x16x128_f8f6f4 v[70:73], v[18:25], v[198:205], v[70:73], v187, v187 op_sel_hi:[0,0,0]
	v_mfma_scale_f32_16x16x128_f8f6f4 v[66:69], v[26:33], v[198:205], v[66:69], v187, v187 op_sel_hi:[0,0,0]
	v_mfma_scale_f32_16x16x128_f8f6f4 v[54:57], v[18:25], v[206:213], v[54:57], v187, v187 op_sel_hi:[0,0,0]
	v_mfma_scale_f32_16x16x128_f8f6f4 v[50:53], v[26:33], v[206:213], v[50:53], v187, v187 op_sel_hi:[0,0,0]
	v_mfma_scale_f32_16x16x128_f8f6f4 v[38:41], v[18:25], v[214:221], v[38:41], v187, v187 op_sel_hi:[0,0,0]
	v_mfma_scale_f32_16x16x128_f8f6f4 v[34:37], v[26:33], v[214:221], v[34:37], v187, v187 op_sel_hi:[0,0,0]
	s_setprio 2
	s_barrier
	s_add_i32 s71, s71, 2
	s_add_u32 s6, s6, 0x100
	s_addc_u32 s7, s7, 0
	s_cmpk_lt_u32 s71, 0x54
	s_cbranch_scc1 .LBB0_1745
	s_waitcnt vmcnt(0)
	s_cmpk_gt_u32 s40, 0xff
	s_cbranch_scc1 .LBB0_1748
	s_barrier

	.amdhsa_kernel _Z9hymba_fwd4Args
		.amdhsa_group_segment_fixed_size 0
		.amdhsa_private_segment_fixed_size 0
		.amdhsa_kernarg_size 480
		.amdhsa_user_sgpr_count 2
		.amdhsa_user_sgpr_dispatch_ptr 0
		.amdhsa_user_sgpr_queue_ptr 0
		.amdhsa_user_sgpr_kernarg_segment_ptr 1
		.amdhsa_user_sgpr_dispatch_id 0
		.amdhsa_user_sgpr_kernarg_preload_length 0
		.amdhsa_user_sgpr_kernarg_preload_offset 0
		.amdhsa_user_sgpr_private_segment_size 0
		.amdhsa_uses_dynamic_stack 0
		.amdhsa_enable_private_segment 0
		.amdhsa_system_sgpr_workgroup_id_x 1
		.amdhsa_system_sgpr_workgroup_id_y 0
		.amdhsa_system_sgpr_workgroup_id_z 0
		.amdhsa_system_sgpr_workgroup_info 0
		.amdhsa_system_vgpr_workitem_id 0
		.amdhsa_next_free_vgpr 256
		.amdhsa_next_free_sgpr 102
		.amdhsa_accum_offset 256
		.amdhsa_reserve_vcc 1
		.amdhsa_float_round_mode_32 0
		.amdhsa_float_round_mode_16_64 0
		.amdhsa_float_denorm_mode_32 3
		.amdhsa_float_denorm_mode_16_64 3
		.amdhsa_dx10_clamp 1
		.amdhsa_ieee_mode 1
		.amdhsa_fp16_overflow 0
		.amdhsa_tg_split 0
		.amdhsa_exception_fp_ieee_invalid_op 0
		.amdhsa_exception_fp_denorm_src 0
		.amdhsa_exception_fp_ieee_div_zero 0
		.amdhsa_exception_fp_ieee_overflow 0
		.amdhsa_exception_fp_ieee_underflow 0
		.amdhsa_exception_fp_ieee_inexact 0
		.amdhsa_exception_int_div_zero 0
	.end_amdhsa_kernel

amdhsa.kernels:
  - .agpr_count:     0
    .args:
      - .offset:         0
        .size:           224
        .value_kind:     by_value
      - .offset:         224
        .size:           4
        .value_kind:     hidden_block_count_x
      - .offset:         228
        .size:           4
        .value_kind:     hidden_block_count_y
      - .offset:         232
        .size:           4
        .value_kind:     hidden_block_count_z
      - .offset:         236
        .size:           2
        .value_kind:     hidden_group_size_x
      - .offset:         238
        .size:           2
        .value_kind:     hidden_group_size_y
      - .offset:         240
        .size:           2
        .value_kind:     hidden_group_size_z
      - .offset:         242
        .size:           2
        .value_kind:     hidden_remainder_x
      - .offset:         244
        .size:           2
        .value_kind:     hidden_remainder_y
      - .offset:         246
        .size:           2
        .value_kind:     hidden_remainder_z
      - .offset:         264
        .size:           8
        .value_kind:     hidden_global_offset_x
      - .offset:         272
        .size:           8
        .value_kind:     hidden_global_offset_y
      - .offset:         280
        .size:           8
        .value_kind:     hidden_global_offset_z
      - .offset:         288
        .size:           2
        .value_kind:     hidden_grid_dims
      - .offset:         344
        .size:           4
        .value_kind:     hidden_dynamic_lds_size
    .group_segment_fixed_size: 0
    .kernarg_segment_align: 8
    .kernarg_segment_size: 480
    .language:       OpenCL C
    .language_version:
      - 2
      - 0
    .max_flat_workgroup_size: 512
    .name:           _Z9hymba_fwd4Args
    .private_segment_fixed_size: 0
    .sgpr_count:     108
    .sgpr_spill_count: 127
    .symbol:         _Z9hymba_fwd4Args.kd
    .uniform_work_group_size: 1
    .uses_dynamic_stack: false
    .vgpr_count:     256
    .vgpr_spill_count: 0
    .wavefront_size: 64
